# v14 + removed 266 s_waitcnt lgkmcnt(N) inside MFMA runs that follow an lgkmcnt(0) with no LDS/SMEM op since (pure issue-slot removal)
# speedup vs baseline: 1.0090x; 1.0047x over previous
; #define PG8_STAGE(bufoff, rs_, soff_, voff) do { _Pragma("unroll") for (int _i = 0; _i < 2; ++_i) \
;         __builtin_amdgcn_raw_ptr_buffer_load_lds(rs_, (LAS void*)(lds + (bufoff) + ldsw + _i * 8192), 16, (int)(voff)[_i], (int)(soff_), 0, 0); } while (0)
; #define PG8_LDA(dst, b, h) do { _Pragma("unroll") for (int m = 0; m < 4; ++m) dst[m] = PG8_LD2(lds + PG8_SA(b, h) + aoff + m * 2048); } while (0)
; #define PG8_LDB(dst, b, h) do { _Pragma("unroll") for (int n = 0; n < 2; ++n) dst[n] = PG8_LD2(lds + PG8_SB(b, h) + boff + n * 2048); } while (0)
; #define PG8_WAIT_V(n) asm volatile("s_waitcnt vmcnt(" #n ")" ::: "memory")
; #define PG8_WAIT_L(n) asm volatile("s_waitcnt lgkmcnt(" #n ")" ::: "memory")
; #define PG8_BAR __builtin_amdgcn_s_barrier()
; #define PG8_SCHED __builtin_amdgcn_sched_barrier(0)
; template <class Epi, class Sched, bool ALIGN_EPI = false, bool SP2 = false, bool FP8 = false>
; __device__ __forceinline__ void gemm_phase(LAS unsigned char* lds, const Gemm g, const Sched& S, const Epi& E, int wbase) {
;     ...
;             PG8_LDB(B0, 0, 0); PG8_LDB(B1, 0, 1); PG8_SCHED; PG8_LDA(At, 0, 0); PG8_STAGE(PG8_SA(1, 1), rAc, a1 + hstep, voffA);
;             PG8_WAIT_V(8); PG8_WAIT_L(0); PG8_BAR; PG8_MMA(0, 0, At, B0); PG8_MMA(0, 1, At, B1); PG8_BAR; PG8_SCHED;
;             PG8_LDA(At, 0, 1); PG8_STAGE(PG8_SB(0, 0), rB2, b2, voffB); PG8_STAGE(PG8_SB(0, 1), rB2, b2 + hstep, voffB); PG8_STAGE(PG8_SA(0, 0), rA2, a2, voffA);
;             PG8_WAIT_V(8); PG8_WAIT_L(0); PG8_BAR; PG8_MMA(1, 0, At, B0); PG8_MMA(1, 1, At, B1); PG8_BAR; PG8_SCHED;
.LBB0_258:
	ds_read_b128 v[128:131], v252
	ds_read_b128 v[132:135], v252 offset:1024
	ds_read_b128 v[136:139], v252 offset:2048
	ds_read_b128 v[140:143], v252 offset:3072
	ds_read_b128 v[144:147], v225
	ds_read_b128 v[148:151], v225 offset:1024
	ds_read_b128 v[152:155], v225 offset:2048
	ds_read_b128 v[156:159], v225 offset:3072
	s_add_i32 s6, s16, 0x80
	s_cmp_eq_u32 s18, s29
	s_cselect_b32 s46, s2, s6
	s_cselect_b32 s31, s3, s28
	s_or_b32 s30, s46, 0x80
	s_add_i32 s6, s41, s16
	s_mov_b32 m0, s19
	ds_read_b128 v[176:179], v172
	ds_read_b128 v[180:183], v172 offset:1024
	ds_read_b128 v[184:187], v172 offset:2048
	ds_read_b128 v[188:191], v172 offset:3072
	ds_read_b128 v[194:197], v172 offset:4096
	ds_read_b128 v[198:201], v172 offset:5120
	ds_read_b128 v[202:205], v172 offset:6144
	ds_read_b128 v[206:209], v172 offset:7168
	buffer_load_dwordx4 v192, s[36:39], s6 offen lds
	s_mov_b32 m0, s20
	s_nop 0
	buffer_load_dwordx4 v223, s[36:39], s6 offen lds
	s_waitcnt vmcnt(8)
	s_waitcnt lgkmcnt(0)
	s_barrier
	s_setprio 1
	v_mfma_f32_16x16x128_f8f6f4 v[124:127], v[128:135], v[176:183], v[124:127]
	v_mfma_f32_16x16x128_f8f6f4 v[120:123], v[136:143], v[176:183], v[120:123]
	v_mfma_f32_16x16x128_f8f6f4 v[108:111], v[128:135], v[184:191], v[108:111]
	v_mfma_f32_16x16x128_f8f6f4 v[104:107], v[136:143], v[184:191], v[104:107]
	v_mfma_f32_16x16x128_f8f6f4 v[160:163], v[128:135], v[194:201], v[92:95]
	v_mfma_f32_16x16x128_f8f6f4 v[210:213], v[136:143], v[194:201], v[88:91]
	v_mfma_f32_16x16x128_f8f6f4 v[214:217], v[128:135], v[202:209], v[76:79]
	v_mfma_f32_16x16x128_f8f6f4 v[218:221], v[136:143], v[202:209], v[72:75]
	s_setprio 0
	s_setprio 1
	v_mfma_f32_16x16x128_f8f6f4 v[116:119], v[144:151], v[176:183], v[116:119]
	v_mfma_f32_16x16x128_f8f6f4 v[112:115], v[152:159], v[176:183], v[112:115]
	v_mfma_f32_16x16x128_f8f6f4 v[100:103], v[144:151], v[184:191], v[100:103]
	v_mfma_f32_16x16x128_f8f6f4 v[96:99], v[152:159], v[184:191], v[96:99]
	v_mfma_f32_16x16x128_f8f6f4 v[176:179], v[144:151], v[194:201], v[84:87]
	v_mfma_f32_16x16x128_f8f6f4 v[180:183], v[152:159], v[194:201], v[80:83]
	v_mfma_f32_16x16x128_f8f6f4 v[184:187], v[144:151], v[202:209], v[68:71]
	v_mfma_f32_16x16x128_f8f6f4 v[188:191], v[152:159], v[202:209], v[64:67]
	s_setprio 0
	s_barrier
	s_mov_b32 m0, s43
	s_mov_b32 s6, s38
	s_mov_b32 s7, s39
	s_nop 1
	ds_read_b128 v[64:67], v172 offset:16384
	ds_read_b128 v[68:71], v172 offset:17408
	ds_read_b128 v[72:75], v172 offset:18432
	ds_read_b128 v[76:79], v172 offset:19456
	ds_read_b128 v[80:83], v172 offset:20480
	ds_read_b128 v[84:87], v172 offset:21504
	ds_read_b128 v[88:91], v172 offset:22528
	ds_read_b128 v[92:95], v172 offset:23552
	buffer_load_dwordx4 v222, s[4:7], s31 offen lds
	s_mov_b32 m0, s44
	s_add_i32 s47, s31, s41
	buffer_load_dwordx4 v193, s[4:7], s31 offen lds
	s_mov_b32 m0, s45
	s_nop 0
	buffer_load_dwordx4 v222, s[4:7], s47 offen lds
	s_mov_b32 m0, s52
	s_nop 0
	buffer_load_dwordx4 v193, s[4:7], s47 offen lds
	s_mov_b32 m0, s42
	s_nop 0
	buffer_load_dwordx4 v192, s[36:39], s46 offen lds
	s_mov_b32 m0, s53
	s_nop 0
	buffer_load_dwordx4 v223, s[36:39], s46 offen lds
	s_waitcnt vmcnt(8)
	s_waitcnt lgkmcnt(0)
	s_barrier
	s_setprio 1
	v_mfma_f32_16x16x128_f8f6f4 v[60:63], v[128:135], v[64:71], v[60:63]
	v_mfma_f32_16x16x128_f8f6f4 v[56:59], v[136:143], v[64:71], v[56:59]
	v_mfma_f32_16x16x128_f8f6f4 v[194:197], v[128:135], v[72:79], v[44:47]
	v_mfma_f32_16x16x128_f8f6f4 v[198:201], v[136:143], v[72:79], v[40:43]
	v_mfma_f32_16x16x128_f8f6f4 v[202:205], v[128:135], v[80:87], v[28:31]
	v_mfma_f32_16x16x128_f8f6f4 v[206:209], v[136:143], v[80:87], v[24:27]
	v_mfma_f32_16x16x128_f8f6f4 v[236:239], v[128:135], v[88:95], v[12:15]
	v_mfma_f32_16x16x128_f8f6f4 v[240:243], v[136:143], v[88:95], v[8:11]
	s_setprio 0
	s_setprio 1
	v_mfma_f32_16x16x128_f8f6f4 v[52:55], v[144:151], v[64:71], v[52:55]
	v_mfma_f32_16x16x128_f8f6f4 v[48:51], v[152:159], v[64:71], v[48:51]
	v_mfma_f32_16x16x128_f8f6f4 v[244:247], v[144:151], v[72:79], v[36:39]
	v_mfma_f32_16x16x128_f8f6f4 v[248:251], v[152:159], v[72:79], v[32:35]
	v_mfma_f32_16x16x128_f8f6f4 v[226:229], v[144:151], v[80:87], v[20:23]
	v_mfma_f32_16x16x128_f8f6f4 v[232:235], v[152:159], v[80:87], v[16:19]
	v_mfma_f32_16x16x128_f8f6f4 v[164:167], v[144:151], v[88:95], v[4:7]
	v_mfma_f32_16x16x128_f8f6f4 v[168:171], v[152:159], v[88:95], v[0:3]
	s_setprio 0
	s_barrier
; #define PG8_STAGE(bufoff, rs_, soff_, voff) do { _Pragma("unroll") for (int _i = 0; _i < 2; ++_i) \
;         __builtin_amdgcn_raw_ptr_buffer_load_lds(rs_, (LAS void*)(lds + (bufoff) + ldsw + _i * 8192), 16, (int)(voff)[_i], (int)(soff_), 0, 0); } while (0)
; #define PG8_LDA(dst, b, h) do { _Pragma("unroll") for (int m = 0; m < 4; ++m) dst[m] = PG8_LD2(lds + PG8_SA(b, h) + aoff + m * 2048); } while (0)
; #define PG8_LDB(dst, b, h) do { _Pragma("unroll") for (int n = 0; n < 2; ++n) dst[n] = PG8_LD2(lds + PG8_SB(b, h) + boff + n * 2048); } while (0)
; #define PG8_WAIT_V(n) asm volatile("s_waitcnt vmcnt(" #n ")" ::: "memory")
; #define PG8_WAIT_L(n) asm volatile("s_waitcnt lgkmcnt(" #n ")" ::: "memory")
; #define PG8_BAR __builtin_amdgcn_s_barrier()
; #define PG8_SCHED __builtin_amdgcn_sched_barrier(0)
; template <class Epi, class Sched, bool ALIGN_EPI = false, bool SP2 = false, bool FP8 = false>
; __device__ __forceinline__ void gemm_phase(LAS unsigned char* lds, const Gemm g, const Sched& S, const Epi& E, int wbase) {
;     ...
;             PG8_LDB(B0, 1, 0); PG8_LDB(B1, 1, 1); PG8_SCHED; PG8_LDA(At, 1, 0); PG8_STAGE(PG8_SA(0, 1), rA2, a2 + hstep, voffA);
;             PG8_WAIT_V(8); PG8_WAIT_L(0); PG8_BAR; PG8_MMA(0, 0, At, B0); PG8_MMA(0, 1, At, B1); PG8_BAR; PG8_SCHED;
;             PG8_LDA(At, 1, 1); PG8_STAGE(PG8_SB(1, 0), rB2, b3, voffB); PG8_STAGE(PG8_SB(1, 1), rB2, b3 + hstep, voffB); PG8_STAGE(PG8_SA(1, 0), rA2, a3, voffA);
;             PG8_WAIT_V(8); PG8_WAIT_L(0); PG8_BAR; PG8_MMA(1, 0, At, B0); PG8_MMA(1, 1, At, B1); PG8_BAR; PG8_SCHED;
	s_nop 4
	ds_read_b128 v[0:3], v173
	ds_read_b128 v[4:7], v173 offset:1024
	ds_read_b128 v[16:19], v173 offset:2048
	ds_read_b128 v[20:23], v173 offset:3072
	ds_read_b128 v[128:131], v174
	ds_read_b128 v[132:135], v174 offset:1024
	ds_read_b128 v[136:139], v174 offset:2048
	ds_read_b128 v[140:143], v174 offset:3072
	s_add_i32 s46, s46, s41
	s_mov_b32 m0, s56
	ds_read_b128 v[8:11], v172 offset:32768
	ds_read_b128 v[12:15], v172 offset:33792
	ds_read_b128 v[24:27], v172 offset:34816
	ds_read_b128 v[28:31], v172 offset:35840
	ds_read_b128 v[32:35], v172 offset:36864
	ds_read_b128 v[36:39], v172 offset:37888
	ds_read_b128 v[40:43], v172 offset:38912
	ds_read_b128 v[44:47], v172 offset:39936
	buffer_load_dwordx4 v192, s[36:39], s46 offen lds
	s_mov_b32 m0, s57
	s_nop 0
	buffer_load_dwordx4 v223, s[36:39], s46 offen lds
	s_waitcnt vmcnt(8)
	s_waitcnt lgkmcnt(0)
	s_barrier
	s_setprio 1
	v_mfma_f32_16x16x128_f8f6f4 v[124:127], v[0:7], v[8:15], v[124:127]
	v_mfma_f32_16x16x128_f8f6f4 v[120:123], v[16:23], v[8:15], v[120:123]
	v_mfma_f32_16x16x128_f8f6f4 v[108:111], v[0:7], v[24:31], v[108:111]
	v_mfma_f32_16x16x128_f8f6f4 v[104:107], v[16:23], v[24:31], v[104:107]
	v_mfma_f32_16x16x128_f8f6f4 v[92:95], v[0:7], v[32:39], v[160:163]
	v_mfma_f32_16x16x128_f8f6f4 v[88:91], v[16:23], v[32:39], v[210:213]
	v_mfma_f32_16x16x128_f8f6f4 v[76:79], v[0:7], v[40:47], v[214:217]
	v_mfma_f32_16x16x128_f8f6f4 v[72:75], v[16:23], v[40:47], v[218:221]
	s_setprio 0
	s_setprio 1
	v_mfma_f32_16x16x128_f8f6f4 v[116:119], v[128:135], v[8:15], v[116:119]
	v_mfma_f32_16x16x128_f8f6f4 v[112:115], v[136:143], v[8:15], v[112:115]
	v_mfma_f32_16x16x128_f8f6f4 v[100:103], v[128:135], v[24:31], v[100:103]
	v_mfma_f32_16x16x128_f8f6f4 v[96:99], v[136:143], v[24:31], v[96:99]
	v_mfma_f32_16x16x128_f8f6f4 v[84:87], v[128:135], v[32:39], v[176:179]
	v_mfma_f32_16x16x128_f8f6f4 v[80:83], v[136:143], v[32:39], v[180:183]
	v_mfma_f32_16x16x128_f8f6f4 v[68:71], v[128:135], v[40:47], v[184:187]
	v_mfma_f32_16x16x128_f8f6f4 v[64:67], v[136:143], v[40:47], v[188:191]
	s_setprio 0
	s_barrier
	s_mov_b32 m0, s58
	s_bitset1_b32 s31, 7
	ds_read_b128 v[32:35], v172 offset:49152
	ds_read_b128 v[36:39], v172 offset:50176
	ds_read_b128 v[144:147], v172 offset:51200
	ds_read_b128 v[148:151], v172 offset:52224
	ds_read_b128 v[152:155], v172 offset:53248
	ds_read_b128 v[156:159], v172 offset:54272
	ds_read_b128 v[176:179], v172 offset:55296
	ds_read_b128 v[180:183], v172 offset:56320
	buffer_load_dwordx4 v222, s[4:7], s31 offen lds
	s_mov_b32 m0, s59
	s_nop 0
	buffer_load_dwordx4 v193, s[4:7], s31 offen lds
	s_add_i32 s31, s31, s41
	s_mov_b32 m0, s65
	s_nop 0
	buffer_load_dwordx4 v222, s[4:7], s31 offen lds
	s_mov_b32 m0, s33
	s_nop 0
	buffer_load_dwordx4 v193, s[4:7], s31 offen lds
	s_mov_b32 m0, s12
	s_nop 0
	buffer_load_dwordx4 v192, s[36:39], s30 offen lds
	s_mov_b32 m0, s13
	s_nop 0
	buffer_load_dwordx4 v223, s[36:39], s30 offen lds
	s_waitcnt vmcnt(8)
	s_waitcnt lgkmcnt(0)
	s_barrier
	s_setprio 1
	v_mfma_f32_16x16x128_f8f6f4 v[60:63], v[0:7], v[32:39], v[60:63]
	v_mfma_f32_16x16x128_f8f6f4 v[56:59], v[16:23], v[32:39], v[56:59]
	v_mfma_f32_16x16x128_f8f6f4 v[44:47], v[0:7], v[144:151], v[194:197]
	v_mfma_f32_16x16x128_f8f6f4 v[40:43], v[16:23], v[144:151], v[198:201]
	v_mfma_f32_16x16x128_f8f6f4 v[28:31], v[0:7], v[152:159], v[202:205]
	v_mfma_f32_16x16x128_f8f6f4 v[24:27], v[16:23], v[152:159], v[206:209]
	v_mfma_f32_16x16x128_f8f6f4 v[12:15], v[0:7], v[176:183], v[236:239]
	v_mfma_f32_16x16x128_f8f6f4 v[8:11], v[16:23], v[176:183], v[240:243]
	s_setprio 0
	s_setprio 1
	v_mfma_f32_16x16x128_f8f6f4 v[52:55], v[128:135], v[32:39], v[52:55]
	v_mfma_f32_16x16x128_f8f6f4 v[48:51], v[136:143], v[32:39], v[48:51]
	v_mfma_f32_16x16x128_f8f6f4 v[36:39], v[128:135], v[144:151], v[244:247]
	v_mfma_f32_16x16x128_f8f6f4 v[32:35], v[136:143], v[144:151], v[248:251]
	v_mfma_f32_16x16x128_f8f6f4 v[20:23], v[128:135], v[152:159], v[226:229]
	v_mfma_f32_16x16x128_f8f6f4 v[16:19], v[136:143], v[152:159], v[232:235]
	v_mfma_f32_16x16x128_f8f6f4 v[4:7], v[128:135], v[176:183], v[164:167]
	v_mfma_f32_16x16x128_f8f6f4 v[0:3], v[136:143], v[176:183], v[168:171]
	s_setprio 0
	s_barrier
	s_add_i32 s29, s29, 2
	s_addk_i32 s16, 0x100
	s_addk_i32 s28, 0x100
	s_cmp_ge_i32 s29, s77
	s_cbranch_scc0 .LBB0_258
	v_mov_b32_e32 v233, v175
	v_mov_b32_e32 v234, v230
	v_mov_b32_e32 v164, v231
	v_mov_b32_e32 v231, 1
	v_mov_b32_e32 v230, 0x358637bd
	s_and_b64 vcc, exec, s[78:79]
	s_cbranch_vccnz .LBB0_261
	s_branch .LBB0_262

; #define PG8_STAGE(bufoff, rs_, soff_, voff) do { _Pragma("unroll") for (int _i = 0; _i < 2; ++_i) \
;         __builtin_amdgcn_raw_ptr_buffer_load_lds(rs_, (LAS void*)(lds + (bufoff) + ldsw + _i * 8192), 16, (int)(voff)[_i], (int)(soff_), 0, 0); } while (0)
; #define PG8_LDA(dst, b, h) do { _Pragma("unroll") for (int m = 0; m < 4; ++m) dst[m] = PG8_LD2(lds + PG8_SA(b, h) + aoff + m * 2048); } while (0)
; #define PG8_LDB(dst, b, h) do { _Pragma("unroll") for (int n = 0; n < 2; ++n) dst[n] = PG8_LD2(lds + PG8_SB(b, h) + boff + n * 2048); } while (0)
; #define PG8_WAIT_V(n) asm volatile("s_waitcnt vmcnt(" #n ")" ::: "memory")
; #define PG8_WAIT_L(n) asm volatile("s_waitcnt lgkmcnt(" #n ")" ::: "memory")
; #define PG8_BAR __builtin_amdgcn_s_barrier()
; #define PG8_SCHED __builtin_amdgcn_sched_barrier(0)
; template <class Epi, class Sched, bool ALIGN_EPI = false, bool SP2 = false, bool FP8 = false>
; __device__ __forceinline__ void gemm_phase(LAS unsigned char* lds, const Gemm g, const Sched& S, const Epi& E, int wbase) {
;     ...
;             PG8_LDB(B0, 0, 0); PG8_LDB(B1, 0, 1); PG8_SCHED; PG8_LDA(At, 0, 0); PG8_STAGE(PG8_SA(1, 1), rAc, a1 + hstep, voffA);
;             PG8_WAIT_V(8); PG8_WAIT_L(0); PG8_BAR; PG8_MMA(0, 0, At, B0); PG8_MMA(0, 1, At, B1); PG8_BAR; PG8_SCHED;
;             PG8_LDA(At, 0, 1); PG8_STAGE(PG8_SB(0, 0), rB2, b2, voffB); PG8_STAGE(PG8_SB(0, 1), rB2, b2 + hstep, voffB); PG8_STAGE(PG8_SA(0, 0), rA2, a2, voffA);
;             PG8_WAIT_V(8); PG8_WAIT_L(0); PG8_BAR; PG8_MMA(1, 0, At, B0); PG8_MMA(1, 1, At, B1); PG8_BAR; PG8_SCHED;
.LBB0_352:
	v_add_u32_e32 v140, 0x10000, v170
	v_add_u32_e32 v156, 0x14000, v170
	ds_read_b128 v[128:131], v140
	ds_read_b128 v[132:135], v140 offset:1024
	ds_read_b128 v[136:139], v140 offset:2048
	ds_read_b128 v[140:143], v140 offset:3072
	ds_read_b128 v[144:147], v156
	ds_read_b128 v[148:151], v156 offset:1024
	ds_read_b128 v[152:155], v156 offset:2048
	ds_read_b128 v[156:159], v156 offset:3072
	s_add_i32 s6, s16, 0x80
	s_cmp_eq_u32 s12, s29
	s_cselect_b32 s46, s2, s6
	s_cselect_b32 s31, s3, s28
	s_or_b32 s30, s46, 0x80
	s_add_i32 s6, s33, s16
	s_mov_b32 m0, s13
	ds_read_b128 v[160:163], v171
	ds_read_b128 v[172:175], v171 offset:1024
	ds_read_b128 v[176:179], v171 offset:2048
	ds_read_b128 v[180:183], v171 offset:3072
	ds_read_b128 v[184:187], v171 offset:4096
	ds_read_b128 v[188:191], v171 offset:5120
	ds_read_b128 v[194:197], v171 offset:6144
	ds_read_b128 v[198:201], v171 offset:7168
	buffer_load_dwordx4 v164, s[36:39], s6 offen lds
	s_mov_b32 m0, s83
	s_nop 0
	buffer_load_dwordx4 v166, s[36:39], s6 offen lds
	s_waitcnt vmcnt(8)
	s_waitcnt lgkmcnt(0)
	s_barrier
	s_setprio 1
	v_mfma_f32_16x16x32_bf16 v[124:127], v[128:131], v[160:163], v[124:127]
	v_mfma_f32_16x16x32_bf16 v[120:123], v[136:139], v[160:163], v[120:123]
	v_mfma_f32_16x16x32_bf16 v[108:111], v[128:131], v[176:179], v[108:111]
	v_mfma_f32_16x16x32_bf16 v[104:107], v[136:139], v[176:179], v[104:107]
	v_mfma_f32_16x16x32_bf16 v[92:95], v[128:131], v[184:187], v[92:95]
	v_mfma_f32_16x16x32_bf16 v[88:91], v[136:139], v[184:187], v[88:91]
	v_mfma_f32_16x16x32_bf16 v[76:79], v[128:131], v[194:197], v[76:79]
	v_mfma_f32_16x16x32_bf16 v[72:75], v[136:139], v[194:197], v[72:75]
	v_mfma_f32_16x16x32_bf16 v[124:127], v[132:135], v[172:175], v[124:127]
	v_mfma_f32_16x16x32_bf16 v[120:123], v[140:143], v[172:175], v[120:123]
	v_mfma_f32_16x16x32_bf16 v[108:111], v[132:135], v[180:183], v[108:111]
	v_mfma_f32_16x16x32_bf16 v[104:107], v[140:143], v[180:183], v[104:107]
	v_mfma_f32_16x16x32_bf16 v[92:95], v[132:135], v[188:191], v[92:95]
	v_mfma_f32_16x16x32_bf16 v[88:91], v[140:143], v[188:191], v[88:91]
	v_mfma_f32_16x16x32_bf16 v[76:79], v[132:135], v[198:201], v[76:79]
	v_mfma_f32_16x16x32_bf16 v[72:75], v[140:143], v[198:201], v[72:75]
	s_setprio 0
	s_setprio 1
	v_mfma_f32_16x16x32_bf16 v[116:119], v[144:147], v[160:163], v[116:119]
	v_mfma_f32_16x16x32_bf16 v[112:115], v[152:155], v[160:163], v[112:115]
	v_mfma_f32_16x16x32_bf16 v[100:103], v[144:147], v[176:179], v[100:103]
	v_mfma_f32_16x16x32_bf16 v[96:99], v[152:155], v[176:179], v[96:99]
	v_mfma_f32_16x16x32_bf16 v[84:87], v[144:147], v[184:187], v[84:87]
	v_mfma_f32_16x16x32_bf16 v[80:83], v[152:155], v[184:187], v[80:83]
	v_mfma_f32_16x16x32_bf16 v[68:71], v[144:147], v[194:197], v[68:71]
	v_mfma_f32_16x16x32_bf16 v[64:67], v[152:155], v[194:197], v[64:67]
	v_mfma_f32_16x16x32_bf16 v[116:119], v[148:151], v[172:175], v[116:119]
	v_mfma_f32_16x16x32_bf16 v[112:115], v[156:159], v[172:175], v[112:115]
	v_mfma_f32_16x16x32_bf16 v[100:103], v[148:151], v[180:183], v[100:103]
	v_mfma_f32_16x16x32_bf16 v[96:99], v[156:159], v[180:183], v[96:99]
	v_mfma_f32_16x16x32_bf16 v[84:87], v[148:151], v[188:191], v[84:87]
	v_mfma_f32_16x16x32_bf16 v[80:83], v[156:159], v[188:191], v[80:83]
	v_mfma_f32_16x16x32_bf16 v[68:71], v[148:151], v[198:201], v[68:71]
	v_mfma_f32_16x16x32_bf16 v[64:67], v[156:159], v[198:201], v[64:67]
	s_setprio 0
	s_barrier
	s_mov_b32 m0, s42
	s_mov_b32 s6, s38
	s_mov_b32 s7, s39
	ds_read_b128 v[160:163], v171 offset:16384
	ds_read_b128 v[172:175], v171 offset:17408
	ds_read_b128 v[176:179], v171 offset:18432
	ds_read_b128 v[180:183], v171 offset:19456
	ds_read_b128 v[184:187], v171 offset:20480
	ds_read_b128 v[188:191], v171 offset:21504
	ds_read_b128 v[194:197], v171 offset:22528
	ds_read_b128 v[198:201], v171 offset:23552
	buffer_load_dwordx4 v165, s[4:7], s31 offen lds
	s_mov_b32 m0, s43
	s_add_i32 s47, s31, s33
	buffer_load_dwordx4 v167, s[4:7], s31 offen lds
	s_mov_b32 m0, s44
	s_nop 0
	buffer_load_dwordx4 v165, s[4:7], s47 offen lds
	s_mov_b32 m0, s45
	s_nop 0
	buffer_load_dwordx4 v167, s[4:7], s47 offen lds
	s_mov_b32 m0, s41
	s_nop 0
	buffer_load_dwordx4 v164, s[36:39], s46 offen lds
	s_mov_b32 m0, s52
	s_nop 0
	buffer_load_dwordx4 v166, s[36:39], s46 offen lds
	s_waitcnt vmcnt(8)
	s_waitcnt lgkmcnt(0)
	s_barrier
	s_setprio 1
	v_mfma_f32_16x16x32_bf16 v[60:63], v[128:131], v[160:163], v[60:63]
	v_mfma_f32_16x16x32_bf16 v[56:59], v[136:139], v[160:163], v[56:59]
	v_mfma_f32_16x16x32_bf16 v[44:47], v[128:131], v[176:179], v[44:47]
	v_mfma_f32_16x16x32_bf16 v[40:43], v[136:139], v[176:179], v[40:43]
	v_mfma_f32_16x16x32_bf16 v[28:31], v[128:131], v[184:187], v[28:31]
	v_mfma_f32_16x16x32_bf16 v[24:27], v[136:139], v[184:187], v[24:27]
	v_mfma_f32_16x16x32_bf16 v[12:15], v[128:131], v[194:197], v[12:15]
	v_mfma_f32_16x16x32_bf16 v[8:11], v[136:139], v[194:197], v[8:11]
	v_mfma_f32_16x16x32_bf16 v[60:63], v[132:135], v[172:175], v[60:63]
	v_mfma_f32_16x16x32_bf16 v[56:59], v[140:143], v[172:175], v[56:59]
	v_mfma_f32_16x16x32_bf16 v[44:47], v[132:135], v[180:183], v[44:47]
	v_mfma_f32_16x16x32_bf16 v[40:43], v[140:143], v[180:183], v[40:43]
	v_mfma_f32_16x16x32_bf16 v[28:31], v[132:135], v[188:191], v[28:31]
	v_mfma_f32_16x16x32_bf16 v[24:27], v[140:143], v[188:191], v[24:27]
	v_mfma_f32_16x16x32_bf16 v[12:15], v[132:135], v[198:201], v[12:15]
	v_mfma_f32_16x16x32_bf16 v[8:11], v[140:143], v[198:201], v[8:11]
	s_setprio 0
	s_setprio 1
	v_mfma_f32_16x16x32_bf16 v[52:55], v[144:147], v[160:163], v[52:55]
	v_mfma_f32_16x16x32_bf16 v[48:51], v[152:155], v[160:163], v[48:51]
	v_mfma_f32_16x16x32_bf16 v[36:39], v[144:147], v[176:179], v[36:39]
	v_mfma_f32_16x16x32_bf16 v[32:35], v[152:155], v[176:179], v[32:35]
	v_mfma_f32_16x16x32_bf16 v[20:23], v[144:147], v[184:187], v[20:23]
	v_mfma_f32_16x16x32_bf16 v[16:19], v[152:155], v[184:187], v[16:19]
	v_mfma_f32_16x16x32_bf16 v[4:7], v[144:147], v[194:197], v[4:7]
	v_mfma_f32_16x16x32_bf16 v[0:3], v[152:155], v[194:197], v[0:3]
	v_mfma_f32_16x16x32_bf16 v[52:55], v[148:151], v[172:175], v[52:55]
	v_mfma_f32_16x16x32_bf16 v[48:51], v[156:159], v[172:175], v[48:51]
	v_mfma_f32_16x16x32_bf16 v[36:39], v[148:151], v[180:183], v[36:39]
	v_mfma_f32_16x16x32_bf16 v[32:35], v[156:159], v[180:183], v[32:35]
	v_mfma_f32_16x16x32_bf16 v[20:23], v[148:151], v[188:191], v[20:23]
	v_mfma_f32_16x16x32_bf16 v[16:19], v[156:159], v[188:191], v[16:19]
	v_mfma_f32_16x16x32_bf16 v[4:7], v[148:151], v[198:201], v[4:7]
	v_mfma_f32_16x16x32_bf16 v[0:3], v[156:159], v[198:201], v[0:3]
	s_setprio 0
	s_barrier
; #define PG8_STAGE(bufoff, rs_, soff_, voff) do { _Pragma("unroll") for (int _i = 0; _i < 2; ++_i) \
;         __builtin_amdgcn_raw_ptr_buffer_load_lds(rs_, (LAS void*)(lds + (bufoff) + ldsw + _i * 8192), 16, (int)(voff)[_i], (int)(soff_), 0, 0); } while (0)
; #define PG8_LDA(dst, b, h) do { _Pragma("unroll") for (int m = 0; m < 4; ++m) dst[m] = PG8_LD2(lds + PG8_SA(b, h) + aoff + m * 2048); } while (0)
; #define PG8_LDB(dst, b, h) do { _Pragma("unroll") for (int n = 0; n < 2; ++n) dst[n] = PG8_LD2(lds + PG8_SB(b, h) + boff + n * 2048); } while (0)
; #define PG8_WAIT_V(n) asm volatile("s_waitcnt vmcnt(" #n ")" ::: "memory")
; #define PG8_WAIT_L(n) asm volatile("s_waitcnt lgkmcnt(" #n ")" ::: "memory")
; #define PG8_BAR __builtin_amdgcn_s_barrier()
; #define PG8_SCHED __builtin_amdgcn_sched_barrier(0)
; template <class Epi, class Sched, bool ALIGN_EPI = false, bool SP2 = false, bool FP8 = false>
; __device__ __forceinline__ void gemm_phase(LAS unsigned char* lds, const Gemm g, const Sched& S, const Epi& E, int wbase) {
;     ...
;             PG8_LDB(B0, 1, 0); PG8_LDB(B1, 1, 1); PG8_SCHED; PG8_LDA(At, 1, 0); PG8_STAGE(PG8_SA(0, 1), rA2, a2 + hstep, voffA);
;             PG8_WAIT_V(8); PG8_WAIT_L(0); PG8_BAR; PG8_MMA(0, 0, At, B0); PG8_MMA(0, 1, At, B1); PG8_BAR; PG8_SCHED;
;             PG8_LDA(At, 1, 1); PG8_STAGE(PG8_SB(1, 0), rB2, b3, voffB); PG8_STAGE(PG8_SB(1, 1), rB2, b3 + hstep, voffB); PG8_STAGE(PG8_SA(1, 0), rA2, a3, voffA);
;             PG8_WAIT_V(8); PG8_WAIT_L(0); PG8_BAR; PG8_MMA(1, 0, At, B0); PG8_MMA(1, 1, At, B1); PG8_BAR; PG8_SCHED;
	v_add_u32_e32 v140, 0x18000, v170
	v_add_u32_e32 v156, 0x1c000, v170
	ds_read_b128 v[128:131], v140
	ds_read_b128 v[132:135], v140 offset:1024
	ds_read_b128 v[136:139], v140 offset:2048
	ds_read_b128 v[140:143], v140 offset:3072
	ds_read_b128 v[144:147], v156
	ds_read_b128 v[148:151], v156 offset:1024
	ds_read_b128 v[152:155], v156 offset:2048
	ds_read_b128 v[156:159], v156 offset:3072
	s_add_i32 s46, s46, s33
	s_mov_b32 m0, s53
	ds_read_b128 v[160:163], v171 offset:32768
	ds_read_b128 v[172:175], v171 offset:33792
	ds_read_b128 v[176:179], v171 offset:34816
	ds_read_b128 v[180:183], v171 offset:35840
	ds_read_b128 v[184:187], v171 offset:36864
	ds_read_b128 v[188:191], v171 offset:37888
	ds_read_b128 v[194:197], v171 offset:38912
	ds_read_b128 v[198:201], v171 offset:39936
	buffer_load_dwordx4 v164, s[36:39], s46 offen lds
	s_mov_b32 m0, s1
	s_nop 0
	buffer_load_dwordx4 v166, s[36:39], s46 offen lds
	s_waitcnt vmcnt(8)
	s_waitcnt lgkmcnt(0)
	s_barrier
	s_setprio 1
	v_mfma_f32_16x16x32_bf16 v[124:127], v[128:131], v[160:163], v[124:127]
	v_mfma_f32_16x16x32_bf16 v[120:123], v[136:139], v[160:163], v[120:123]
	v_mfma_f32_16x16x32_bf16 v[108:111], v[128:131], v[176:179], v[108:111]
	v_mfma_f32_16x16x32_bf16 v[104:107], v[136:139], v[176:179], v[104:107]
	v_mfma_f32_16x16x32_bf16 v[92:95], v[128:131], v[184:187], v[92:95]
	v_mfma_f32_16x16x32_bf16 v[88:91], v[136:139], v[184:187], v[88:91]
	v_mfma_f32_16x16x32_bf16 v[76:79], v[128:131], v[194:197], v[76:79]
	v_mfma_f32_16x16x32_bf16 v[72:75], v[136:139], v[194:197], v[72:75]
	v_mfma_f32_16x16x32_bf16 v[124:127], v[132:135], v[172:175], v[124:127]
	v_mfma_f32_16x16x32_bf16 v[120:123], v[140:143], v[172:175], v[120:123]
	v_mfma_f32_16x16x32_bf16 v[108:111], v[132:135], v[180:183], v[108:111]
	v_mfma_f32_16x16x32_bf16 v[104:107], v[140:143], v[180:183], v[104:107]
	v_mfma_f32_16x16x32_bf16 v[92:95], v[132:135], v[188:191], v[92:95]
	v_mfma_f32_16x16x32_bf16 v[88:91], v[140:143], v[188:191], v[88:91]
	v_mfma_f32_16x16x32_bf16 v[76:79], v[132:135], v[198:201], v[76:79]
	v_mfma_f32_16x16x32_bf16 v[72:75], v[140:143], v[198:201], v[72:75]
	s_setprio 0
	s_setprio 1
	v_mfma_f32_16x16x32_bf16 v[116:119], v[144:147], v[160:163], v[116:119]
	v_mfma_f32_16x16x32_bf16 v[112:115], v[152:155], v[160:163], v[112:115]
	v_mfma_f32_16x16x32_bf16 v[100:103], v[144:147], v[176:179], v[100:103]
	v_mfma_f32_16x16x32_bf16 v[96:99], v[152:155], v[176:179], v[96:99]
	v_mfma_f32_16x16x32_bf16 v[84:87], v[144:147], v[184:187], v[84:87]
	v_mfma_f32_16x16x32_bf16 v[80:83], v[152:155], v[184:187], v[80:83]
	v_mfma_f32_16x16x32_bf16 v[68:71], v[144:147], v[194:197], v[68:71]
	v_mfma_f32_16x16x32_bf16 v[64:67], v[152:155], v[194:197], v[64:67]
	v_mfma_f32_16x16x32_bf16 v[116:119], v[148:151], v[172:175], v[116:119]
	v_mfma_f32_16x16x32_bf16 v[112:115], v[156:159], v[172:175], v[112:115]
	v_mfma_f32_16x16x32_bf16 v[100:103], v[148:151], v[180:183], v[100:103]
	v_mfma_f32_16x16x32_bf16 v[96:99], v[156:159], v[180:183], v[96:99]
	v_mfma_f32_16x16x32_bf16 v[84:87], v[148:151], v[188:191], v[84:87]
	v_mfma_f32_16x16x32_bf16 v[80:83], v[156:159], v[188:191], v[80:83]
	v_mfma_f32_16x16x32_bf16 v[68:71], v[148:151], v[198:201], v[68:71]
	v_mfma_f32_16x16x32_bf16 v[64:67], v[156:159], v[198:201], v[64:67]
	s_setprio 0
	s_barrier
	s_mov_b32 m0, s56
	s_bitset1_b32 s31, 7
	ds_read_b128 v[160:163], v171 offset:49152
	ds_read_b128 v[172:175], v171 offset:50176
	ds_read_b128 v[176:179], v171 offset:51200
	ds_read_b128 v[180:183], v171 offset:52224
	ds_read_b128 v[184:187], v171 offset:53248
	ds_read_b128 v[188:191], v171 offset:54272
	ds_read_b128 v[194:197], v171 offset:55296
	ds_read_b128 v[198:201], v171 offset:56320
	buffer_load_dwordx4 v165, s[4:7], s31 offen lds
	s_mov_b32 m0, s57
	s_nop 0
	buffer_load_dwordx4 v167, s[4:7], s31 offen lds
	s_add_i32 s31, s31, s33
	s_mov_b32 m0, s65
	s_nop 0
	buffer_load_dwordx4 v165, s[4:7], s31 offen lds
	s_mov_b32 m0, s76
	s_nop 0
	buffer_load_dwordx4 v167, s[4:7], s31 offen lds
	s_mov_b32 m0, s58
	s_nop 0
	buffer_load_dwordx4 v164, s[36:39], s30 offen lds
	s_mov_b32 m0, s59
	s_nop 0
	buffer_load_dwordx4 v166, s[36:39], s30 offen lds
	s_waitcnt vmcnt(8)
	s_waitcnt lgkmcnt(0)
	s_barrier
	s_setprio 1
	v_mfma_f32_16x16x32_bf16 v[60:63], v[128:131], v[160:163], v[60:63]
	v_mfma_f32_16x16x32_bf16 v[56:59], v[136:139], v[160:163], v[56:59]
	v_mfma_f32_16x16x32_bf16 v[44:47], v[128:131], v[176:179], v[44:47]
	v_mfma_f32_16x16x32_bf16 v[40:43], v[136:139], v[176:179], v[40:43]
	v_mfma_f32_16x16x32_bf16 v[28:31], v[128:131], v[184:187], v[28:31]
	v_mfma_f32_16x16x32_bf16 v[24:27], v[136:139], v[184:187], v[24:27]
	v_mfma_f32_16x16x32_bf16 v[12:15], v[128:131], v[194:197], v[12:15]
	v_mfma_f32_16x16x32_bf16 v[8:11], v[136:139], v[194:197], v[8:11]
	v_mfma_f32_16x16x32_bf16 v[60:63], v[132:135], v[172:175], v[60:63]
	v_mfma_f32_16x16x32_bf16 v[56:59], v[140:143], v[172:175], v[56:59]
	v_mfma_f32_16x16x32_bf16 v[44:47], v[132:135], v[180:183], v[44:47]
	v_mfma_f32_16x16x32_bf16 v[40:43], v[140:143], v[180:183], v[40:43]
	v_mfma_f32_16x16x32_bf16 v[28:31], v[132:135], v[188:191], v[28:31]
	v_mfma_f32_16x16x32_bf16 v[24:27], v[140:143], v[188:191], v[24:27]
	v_mfma_f32_16x16x32_bf16 v[12:15], v[132:135], v[198:201], v[12:15]
	v_mfma_f32_16x16x32_bf16 v[8:11], v[140:143], v[198:201], v[8:11]
	s_setprio 0
	s_setprio 1
	v_mfma_f32_16x16x32_bf16 v[52:55], v[144:147], v[160:163], v[52:55]
	v_mfma_f32_16x16x32_bf16 v[48:51], v[152:155], v[160:163], v[48:51]
	v_mfma_f32_16x16x32_bf16 v[36:39], v[144:147], v[176:179], v[36:39]
	v_mfma_f32_16x16x32_bf16 v[32:35], v[152:155], v[176:179], v[32:35]
	v_mfma_f32_16x16x32_bf16 v[20:23], v[144:147], v[184:187], v[20:23]
	v_mfma_f32_16x16x32_bf16 v[16:19], v[152:155], v[184:187], v[16:19]
	v_mfma_f32_16x16x32_bf16 v[4:7], v[144:147], v[194:197], v[4:7]
	v_mfma_f32_16x16x32_bf16 v[0:3], v[152:155], v[194:197], v[0:3]
	v_mfma_f32_16x16x32_bf16 v[52:55], v[148:151], v[172:175], v[52:55]
	v_mfma_f32_16x16x32_bf16 v[48:51], v[156:159], v[172:175], v[48:51]
	v_mfma_f32_16x16x32_bf16 v[36:39], v[148:151], v[180:183], v[36:39]
	v_mfma_f32_16x16x32_bf16 v[32:35], v[156:159], v[180:183], v[32:35]
	v_mfma_f32_16x16x32_bf16 v[20:23], v[148:151], v[188:191], v[20:23]
	v_mfma_f32_16x16x32_bf16 v[16:19], v[156:159], v[188:191], v[16:19]
	v_mfma_f32_16x16x32_bf16 v[4:7], v[148:151], v[198:201], v[4:7]
	v_mfma_f32_16x16x32_bf16 v[0:3], v[156:159], v[198:201], v[0:3]
	s_setprio 0
	s_barrier
	s_add_i32 s29, s29, 2
	s_addk_i32 s16, 0x100
	s_addk_i32 s28, 0x100
	s_cmp_ge_i32 s29, s82
	s_cbranch_scc0 .LBB0_352
	s_and_b64 vcc, exec, s[78:79]
	s_cbranch_vccz .LBB0_355

; #define PG8_STAGE(bufoff, rs_, soff_, voff) do { _Pragma("unroll") for (int _i = 0; _i < 2; ++_i) \
;         __builtin_amdgcn_raw_ptr_buffer_load_lds(rs_, (LAS void*)(lds + (bufoff) + ldsw + _i * 8192), 16, (int)(voff)[_i], (int)(soff_), 0, 0); } while (0)
; #define PG8_LDA(dst, b, h) do { _Pragma("unroll") for (int m = 0; m < 4; ++m) dst[m] = PG8_LD2(lds + PG8_SA(b, h) + aoff + m * 2048); } while (0)
; #define PG8_LDB(dst, b, h) do { _Pragma("unroll") for (int n = 0; n < 2; ++n) dst[n] = PG8_LD2(lds + PG8_SB(b, h) + boff + n * 2048); } while (0)
; #define PG8_WAIT_V(n) asm volatile("s_waitcnt vmcnt(" #n ")" ::: "memory")
; #define PG8_WAIT_L(n) asm volatile("s_waitcnt lgkmcnt(" #n ")" ::: "memory")
; #define PG8_BAR __builtin_amdgcn_s_barrier()
; #define PG8_SCHED __builtin_amdgcn_sched_barrier(0)
; template <class Epi, class Sched, bool ALIGN_EPI = false, bool SP2 = false, bool FP8 = false>
; __device__ __forceinline__ void gemm_phase(LAS unsigned char* lds, const Gemm g, const Sched& S, const Epi& E, int wbase) {
;     ...
;             PG8_LDB(B0, 0, 0); PG8_LDB(B1, 0, 1); PG8_SCHED; PG8_LDA(At, 0, 0); PG8_STAGE(PG8_SA(1, 1), rAc, a1 + hstep, voffA);
;             PG8_WAIT_V(8); PG8_WAIT_L(0); PG8_BAR; PG8_MMA(0, 0, At, B0); PG8_MMA(0, 1, At, B1); PG8_BAR; PG8_SCHED;
;             PG8_LDA(At, 0, 1); PG8_STAGE(PG8_SB(0, 0), rB2, b2, voffB); PG8_STAGE(PG8_SB(0, 1), rB2, b2 + hstep, voffB); PG8_STAGE(PG8_SA(0, 0), rA2, a2, voffA);
;             PG8_WAIT_V(8); PG8_WAIT_L(0); PG8_BAR; PG8_MMA(1, 0, At, B0); PG8_MMA(1, 1, At, B1); PG8_BAR; PG8_SCHED;
.LBB0_450:
	v_add_u32_e32 v148, 0x10000, v138
	v_add_u32_e32 v164, 0x14000, v138
	ds_read_b128 v[128:131], v148
	ds_read_b128 v[140:143], v148 offset:1024
	ds_read_b128 v[144:147], v148 offset:2048
	ds_read_b128 v[148:151], v148 offset:3072
	ds_read_b128 v[152:155], v164
	ds_read_b128 v[156:159], v164 offset:1024
	ds_read_b128 v[160:163], v164 offset:2048
	ds_read_b128 v[164:167], v164 offset:3072
	s_add_i32 s6, s58, 0x80
	s_cmp_eq_u32 s42, s60
	s_cselect_b32 s61, s56, s6
	s_cselect_b32 s55, s57, s59
	s_or_b32 s54, s61, 0x80
	s_add_i32 s6, s19, s58
	s_mov_b32 m0, s43
	ds_read_b128 v[168:171], v139
	ds_read_b128 v[172:175], v139 offset:1024
	ds_read_b128 v[176:179], v139 offset:2048
	ds_read_b128 v[180:183], v139 offset:3072
	ds_read_b128 v[184:187], v139 offset:4096
	ds_read_b128 v[188:191], v139 offset:5120
	ds_read_b128 v[194:197], v139 offset:6144
	ds_read_b128 v[198:201], v139 offset:7168
	buffer_load_dwordx4 v132, s[36:39], s6 offen lds
	s_mov_b32 m0, s44
	s_nop 0
	buffer_load_dwordx4 v134, s[36:39], s6 offen lds
	s_waitcnt vmcnt(8)
	s_waitcnt lgkmcnt(0)
	s_barrier
	s_setprio 1
	v_mfma_f32_16x16x32_bf16 v[124:127], v[128:131], v[168:171], v[124:127]
	v_mfma_f32_16x16x32_bf16 v[120:123], v[144:147], v[168:171], v[120:123]
	v_mfma_f32_16x16x32_bf16 v[108:111], v[128:131], v[176:179], v[108:111]
	v_mfma_f32_16x16x32_bf16 v[104:107], v[144:147], v[176:179], v[104:107]
	v_mfma_f32_16x16x32_bf16 v[92:95], v[128:131], v[184:187], v[92:95]
	v_mfma_f32_16x16x32_bf16 v[88:91], v[144:147], v[184:187], v[88:91]
	v_mfma_f32_16x16x32_bf16 v[76:79], v[128:131], v[194:197], v[76:79]
	v_mfma_f32_16x16x32_bf16 v[72:75], v[144:147], v[194:197], v[72:75]
	v_mfma_f32_16x16x32_bf16 v[124:127], v[140:143], v[172:175], v[124:127]
	v_mfma_f32_16x16x32_bf16 v[120:123], v[148:151], v[172:175], v[120:123]
	v_mfma_f32_16x16x32_bf16 v[108:111], v[140:143], v[180:183], v[108:111]
	v_mfma_f32_16x16x32_bf16 v[104:107], v[148:151], v[180:183], v[104:107]
	v_mfma_f32_16x16x32_bf16 v[92:95], v[140:143], v[188:191], v[92:95]
	v_mfma_f32_16x16x32_bf16 v[88:91], v[148:151], v[188:191], v[88:91]
	v_mfma_f32_16x16x32_bf16 v[76:79], v[140:143], v[198:201], v[76:79]
	v_mfma_f32_16x16x32_bf16 v[72:75], v[148:151], v[198:201], v[72:75]
	s_setprio 0
	s_setprio 1
	v_mfma_f32_16x16x32_bf16 v[116:119], v[152:155], v[168:171], v[116:119]
	v_mfma_f32_16x16x32_bf16 v[112:115], v[160:163], v[168:171], v[112:115]
	v_mfma_f32_16x16x32_bf16 v[100:103], v[152:155], v[176:179], v[100:103]
	v_mfma_f32_16x16x32_bf16 v[96:99], v[160:163], v[176:179], v[96:99]
	v_mfma_f32_16x16x32_bf16 v[84:87], v[152:155], v[184:187], v[84:87]
	v_mfma_f32_16x16x32_bf16 v[80:83], v[160:163], v[184:187], v[80:83]
	v_mfma_f32_16x16x32_bf16 v[68:71], v[152:155], v[194:197], v[68:71]
	v_mfma_f32_16x16x32_bf16 v[64:67], v[160:163], v[194:197], v[64:67]
	v_mfma_f32_16x16x32_bf16 v[116:119], v[156:159], v[172:175], v[116:119]
	v_mfma_f32_16x16x32_bf16 v[112:115], v[164:167], v[172:175], v[112:115]
	v_mfma_f32_16x16x32_bf16 v[100:103], v[156:159], v[180:183], v[100:103]
	v_mfma_f32_16x16x32_bf16 v[96:99], v[164:167], v[180:183], v[96:99]
	v_mfma_f32_16x16x32_bf16 v[84:87], v[156:159], v[188:191], v[84:87]
	v_mfma_f32_16x16x32_bf16 v[80:83], v[164:167], v[188:191], v[80:83]
	v_mfma_f32_16x16x32_bf16 v[68:71], v[156:159], v[198:201], v[68:71]
	v_mfma_f32_16x16x32_bf16 v[64:67], v[164:167], v[198:201], v[64:67]
	s_setprio 0
	s_barrier
	s_mov_b32 m0, s21
	s_mov_b32 s6, s38
	s_mov_b32 s7, s39
	ds_read_b128 v[168:171], v139 offset:16384
	ds_read_b128 v[172:175], v139 offset:17408
	ds_read_b128 v[176:179], v139 offset:18432
	ds_read_b128 v[180:183], v139 offset:19456
	ds_read_b128 v[184:187], v139 offset:20480
	ds_read_b128 v[188:191], v139 offset:21504
	ds_read_b128 v[194:197], v139 offset:22528
	ds_read_b128 v[198:201], v139 offset:23552
	buffer_load_dwordx4 v133, s[4:7], s55 offen lds
	s_mov_b32 m0, s22
	s_add_i32 s62, s55, s19
	buffer_load_dwordx4 v135, s[4:7], s55 offen lds
	s_mov_b32 m0, s23
	s_nop 0
	buffer_load_dwordx4 v133, s[4:7], s62 offen lds
	s_mov_b32 m0, s24
	s_nop 0
	buffer_load_dwordx4 v135, s[4:7], s62 offen lds
	s_mov_b32 m0, s20
	s_nop 0
	buffer_load_dwordx4 v132, s[36:39], s61 offen lds
	s_mov_b32 m0, s25
	s_nop 0
	buffer_load_dwordx4 v134, s[36:39], s61 offen lds
	s_waitcnt vmcnt(8)
	s_waitcnt lgkmcnt(0)
	s_barrier
	s_setprio 1
	v_mfma_f32_16x16x32_bf16 v[60:63], v[128:131], v[168:171], v[60:63]
	v_mfma_f32_16x16x32_bf16 v[56:59], v[144:147], v[168:171], v[56:59]
	v_mfma_f32_16x16x32_bf16 v[44:47], v[128:131], v[176:179], v[44:47]
	v_mfma_f32_16x16x32_bf16 v[40:43], v[144:147], v[176:179], v[40:43]
	v_mfma_f32_16x16x32_bf16 v[28:31], v[128:131], v[184:187], v[28:31]
	v_mfma_f32_16x16x32_bf16 v[24:27], v[144:147], v[184:187], v[24:27]
	v_mfma_f32_16x16x32_bf16 v[12:15], v[128:131], v[194:197], v[12:15]
	v_mfma_f32_16x16x32_bf16 v[8:11], v[144:147], v[194:197], v[8:11]
	v_mfma_f32_16x16x32_bf16 v[60:63], v[140:143], v[172:175], v[60:63]
	v_mfma_f32_16x16x32_bf16 v[56:59], v[148:151], v[172:175], v[56:59]
	v_mfma_f32_16x16x32_bf16 v[44:47], v[140:143], v[180:183], v[44:47]
	v_mfma_f32_16x16x32_bf16 v[40:43], v[148:151], v[180:183], v[40:43]
	v_mfma_f32_16x16x32_bf16 v[28:31], v[140:143], v[188:191], v[28:31]
	v_mfma_f32_16x16x32_bf16 v[24:27], v[148:151], v[188:191], v[24:27]
	v_mfma_f32_16x16x32_bf16 v[12:15], v[140:143], v[198:201], v[12:15]
	v_mfma_f32_16x16x32_bf16 v[8:11], v[148:151], v[198:201], v[8:11]
	s_setprio 0
	s_setprio 1
	v_mfma_f32_16x16x32_bf16 v[52:55], v[152:155], v[168:171], v[52:55]
	v_mfma_f32_16x16x32_bf16 v[48:51], v[160:163], v[168:171], v[48:51]
	v_mfma_f32_16x16x32_bf16 v[36:39], v[152:155], v[176:179], v[36:39]
	v_mfma_f32_16x16x32_bf16 v[32:35], v[160:163], v[176:179], v[32:35]
	v_mfma_f32_16x16x32_bf16 v[20:23], v[152:155], v[184:187], v[20:23]
	v_mfma_f32_16x16x32_bf16 v[16:19], v[160:163], v[184:187], v[16:19]
	v_mfma_f32_16x16x32_bf16 v[4:7], v[152:155], v[194:197], v[4:7]
	v_mfma_f32_16x16x32_bf16 v[0:3], v[160:163], v[194:197], v[0:3]
	v_mfma_f32_16x16x32_bf16 v[52:55], v[156:159], v[172:175], v[52:55]
	v_mfma_f32_16x16x32_bf16 v[48:51], v[164:167], v[172:175], v[48:51]
	v_mfma_f32_16x16x32_bf16 v[36:39], v[156:159], v[180:183], v[36:39]
	v_mfma_f32_16x16x32_bf16 v[32:35], v[164:167], v[180:183], v[32:35]
	v_mfma_f32_16x16x32_bf16 v[20:23], v[156:159], v[188:191], v[20:23]
	v_mfma_f32_16x16x32_bf16 v[16:19], v[164:167], v[188:191], v[16:19]
	v_mfma_f32_16x16x32_bf16 v[4:7], v[156:159], v[198:201], v[4:7]
	v_mfma_f32_16x16x32_bf16 v[0:3], v[164:167], v[198:201], v[0:3]
	s_setprio 0
	s_barrier
; #define PG8_STAGE(bufoff, rs_, soff_, voff) do { _Pragma("unroll") for (int _i = 0; _i < 2; ++_i) \
;         __builtin_amdgcn_raw_ptr_buffer_load_lds(rs_, (LAS void*)(lds + (bufoff) + ldsw + _i * 8192), 16, (int)(voff)[_i], (int)(soff_), 0, 0); } while (0)
; #define PG8_LDA(dst, b, h) do { _Pragma("unroll") for (int m = 0; m < 4; ++m) dst[m] = PG8_LD2(lds + PG8_SA(b, h) + aoff + m * 2048); } while (0)
; #define PG8_LDB(dst, b, h) do { _Pragma("unroll") for (int n = 0; n < 2; ++n) dst[n] = PG8_LD2(lds + PG8_SB(b, h) + boff + n * 2048); } while (0)
; #define PG8_WAIT_V(n) asm volatile("s_waitcnt vmcnt(" #n ")" ::: "memory")
; #define PG8_WAIT_L(n) asm volatile("s_waitcnt lgkmcnt(" #n ")" ::: "memory")
; #define PG8_BAR __builtin_amdgcn_s_barrier()
; #define PG8_SCHED __builtin_amdgcn_sched_barrier(0)
; template <class Epi, class Sched, bool ALIGN_EPI = false, bool SP2 = false, bool FP8 = false>
; __device__ __forceinline__ void gemm_phase(LAS unsigned char* lds, const Gemm g, const Sched& S, const Epi& E, int wbase) {
;     ...
;         for (int t = 0; t < nt; t += 2) {
;             const bool last = (t == nt - 2);
;             const unsigned a1 = cA + (unsigned)(t + 1) * kstep;
;             const unsigned a2 = last ? nA : cA + (unsigned)(t + 2) * kstep, b2 = last ? nB : cB + (unsigned)(t + 2) * kstep; const rsrc_t rA2 = (Sched::TWO && last) ? rAn : rAc, rB2 = (Sched::TWO && last) ? rBn : rBc;
;             const unsigned a3 = a2 + kstep, b3 = b2 + kstep;
;             if (last && has_next) S.a_ready(nxt);
;     ...
;             PG8_LDB(B0, 1, 0); PG8_LDB(B1, 1, 1); PG8_SCHED; PG8_LDA(At, 1, 0); PG8_STAGE(PG8_SA(0, 1), rA2, a2 + hstep, voffA);
;             PG8_WAIT_V(8); PG8_WAIT_L(0); PG8_BAR; PG8_MMA(0, 0, At, B0); PG8_MMA(0, 1, At, B1); PG8_BAR; PG8_SCHED;
;             PG8_LDA(At, 1, 1); PG8_STAGE(PG8_SB(1, 0), rB2, b3, voffB); PG8_STAGE(PG8_SB(1, 1), rB2, b3 + hstep, voffB); PG8_STAGE(PG8_SA(1, 0), rA2, a3, voffA);
;             PG8_WAIT_V(8); PG8_WAIT_L(0); PG8_BAR; PG8_MMA(1, 0, At, B0); PG8_MMA(1, 1, At, B1); PG8_BAR; PG8_SCHED;
	v_add_u32_e32 v148, 0x18000, v138
	v_add_u32_e32 v164, 0x1c000, v138
	ds_read_b128 v[128:131], v148
	ds_read_b128 v[140:143], v148 offset:1024
	ds_read_b128 v[144:147], v148 offset:2048
	ds_read_b128 v[148:151], v148 offset:3072
	ds_read_b128 v[152:155], v164
	ds_read_b128 v[156:159], v164 offset:1024
	ds_read_b128 v[160:163], v164 offset:2048
	ds_read_b128 v[164:167], v164 offset:3072
	s_add_i32 s61, s61, s19
	s_mov_b32 m0, s26
	ds_read_b128 v[168:171], v139 offset:32768
	ds_read_b128 v[172:175], v139 offset:33792
	ds_read_b128 v[176:179], v139 offset:34816
	ds_read_b128 v[180:183], v139 offset:35840
	ds_read_b128 v[184:187], v139 offset:36864
	ds_read_b128 v[188:191], v139 offset:37888
	ds_read_b128 v[194:197], v139 offset:38912
	ds_read_b128 v[198:201], v139 offset:39936
	buffer_load_dwordx4 v132, s[36:39], s61 offen lds
	s_mov_b32 m0, s27
	s_nop 0
	buffer_load_dwordx4 v134, s[36:39], s61 offen lds
	s_waitcnt vmcnt(8)
	s_waitcnt lgkmcnt(0)
	s_barrier
	s_setprio 1
	v_mfma_f32_16x16x32_bf16 v[124:127], v[128:131], v[168:171], v[124:127]
	v_mfma_f32_16x16x32_bf16 v[120:123], v[144:147], v[168:171], v[120:123]
	v_mfma_f32_16x16x32_bf16 v[108:111], v[128:131], v[176:179], v[108:111]
	v_mfma_f32_16x16x32_bf16 v[104:107], v[144:147], v[176:179], v[104:107]
	v_mfma_f32_16x16x32_bf16 v[92:95], v[128:131], v[184:187], v[92:95]
	v_mfma_f32_16x16x32_bf16 v[88:91], v[144:147], v[184:187], v[88:91]
	v_mfma_f32_16x16x32_bf16 v[76:79], v[128:131], v[194:197], v[76:79]
	v_mfma_f32_16x16x32_bf16 v[72:75], v[144:147], v[194:197], v[72:75]
	v_mfma_f32_16x16x32_bf16 v[124:127], v[140:143], v[172:175], v[124:127]
	v_mfma_f32_16x16x32_bf16 v[120:123], v[148:151], v[172:175], v[120:123]
	v_mfma_f32_16x16x32_bf16 v[108:111], v[140:143], v[180:183], v[108:111]
	v_mfma_f32_16x16x32_bf16 v[104:107], v[148:151], v[180:183], v[104:107]
	v_mfma_f32_16x16x32_bf16 v[92:95], v[140:143], v[188:191], v[92:95]
	v_mfma_f32_16x16x32_bf16 v[88:91], v[148:151], v[188:191], v[88:91]
	v_mfma_f32_16x16x32_bf16 v[76:79], v[140:143], v[198:201], v[76:79]
	v_mfma_f32_16x16x32_bf16 v[72:75], v[148:151], v[198:201], v[72:75]
	s_setprio 0
	s_setprio 1
	v_mfma_f32_16x16x32_bf16 v[116:119], v[152:155], v[168:171], v[116:119]
	v_mfma_f32_16x16x32_bf16 v[112:115], v[160:163], v[168:171], v[112:115]
	v_mfma_f32_16x16x32_bf16 v[100:103], v[152:155], v[176:179], v[100:103]
	v_mfma_f32_16x16x32_bf16 v[96:99], v[160:163], v[176:179], v[96:99]
	v_mfma_f32_16x16x32_bf16 v[84:87], v[152:155], v[184:187], v[84:87]
	v_mfma_f32_16x16x32_bf16 v[80:83], v[160:163], v[184:187], v[80:83]
	v_mfma_f32_16x16x32_bf16 v[68:71], v[152:155], v[194:197], v[68:71]
	v_mfma_f32_16x16x32_bf16 v[64:67], v[160:163], v[194:197], v[64:67]
	v_mfma_f32_16x16x32_bf16 v[116:119], v[156:159], v[172:175], v[116:119]
	v_mfma_f32_16x16x32_bf16 v[112:115], v[164:167], v[172:175], v[112:115]
	v_mfma_f32_16x16x32_bf16 v[100:103], v[156:159], v[180:183], v[100:103]
	v_mfma_f32_16x16x32_bf16 v[96:99], v[164:167], v[180:183], v[96:99]
	v_mfma_f32_16x16x32_bf16 v[84:87], v[156:159], v[188:191], v[84:87]
	v_mfma_f32_16x16x32_bf16 v[80:83], v[164:167], v[188:191], v[80:83]
	v_mfma_f32_16x16x32_bf16 v[68:71], v[156:159], v[198:201], v[68:71]
	v_mfma_f32_16x16x32_bf16 v[64:67], v[164:167], v[198:201], v[64:67]
	s_setprio 0
	s_barrier
	s_mov_b32 m0, s28
	s_bitset1_b32 s55, 7
	ds_read_b128 v[168:171], v139 offset:49152
	ds_read_b128 v[172:175], v139 offset:50176
	ds_read_b128 v[176:179], v139 offset:51200
	ds_read_b128 v[180:183], v139 offset:52224
	ds_read_b128 v[184:187], v139 offset:53248
	ds_read_b128 v[188:191], v139 offset:54272
	ds_read_b128 v[194:197], v139 offset:55296
	ds_read_b128 v[198:201], v139 offset:56320
	buffer_load_dwordx4 v133, s[4:7], s55 offen lds
	s_mov_b32 m0, s29
	s_nop 0
	buffer_load_dwordx4 v135, s[4:7], s55 offen lds
	s_add_i32 s55, s55, s19
	s_mov_b32 m0, s33
	s_nop 0
	buffer_load_dwordx4 v133, s[4:7], s55 offen lds
	s_mov_b32 m0, s34
	s_nop 0
	buffer_load_dwordx4 v135, s[4:7], s55 offen lds
	s_mov_b32 m0, s30
	s_nop 0
	buffer_load_dwordx4 v132, s[36:39], s54 offen lds
	s_mov_b32 m0, s31
	s_nop 0
	buffer_load_dwordx4 v134, s[36:39], s54 offen lds
	s_waitcnt vmcnt(8)
	s_waitcnt lgkmcnt(0)
	s_barrier
	s_setprio 1
	v_mfma_f32_16x16x32_bf16 v[60:63], v[128:131], v[168:171], v[60:63]
	v_mfma_f32_16x16x32_bf16 v[56:59], v[144:147], v[168:171], v[56:59]
	v_mfma_f32_16x16x32_bf16 v[44:47], v[128:131], v[176:179], v[44:47]
	v_mfma_f32_16x16x32_bf16 v[40:43], v[144:147], v[176:179], v[40:43]
	v_mfma_f32_16x16x32_bf16 v[28:31], v[128:131], v[184:187], v[28:31]
	v_mfma_f32_16x16x32_bf16 v[24:27], v[144:147], v[184:187], v[24:27]
	v_mfma_f32_16x16x32_bf16 v[12:15], v[128:131], v[194:197], v[12:15]
	v_mfma_f32_16x16x32_bf16 v[8:11], v[144:147], v[194:197], v[8:11]
	v_mfma_f32_16x16x32_bf16 v[60:63], v[140:143], v[172:175], v[60:63]
	v_mfma_f32_16x16x32_bf16 v[56:59], v[148:151], v[172:175], v[56:59]
	v_mfma_f32_16x16x32_bf16 v[44:47], v[140:143], v[180:183], v[44:47]
	v_mfma_f32_16x16x32_bf16 v[40:43], v[148:151], v[180:183], v[40:43]
	v_mfma_f32_16x16x32_bf16 v[28:31], v[140:143], v[188:191], v[28:31]
	v_mfma_f32_16x16x32_bf16 v[24:27], v[148:151], v[188:191], v[24:27]
	v_mfma_f32_16x16x32_bf16 v[12:15], v[140:143], v[198:201], v[12:15]
	v_mfma_f32_16x16x32_bf16 v[8:11], v[148:151], v[198:201], v[8:11]
	s_setprio 0
	s_setprio 1
	v_mfma_f32_16x16x32_bf16 v[52:55], v[152:155], v[168:171], v[52:55]
	v_mfma_f32_16x16x32_bf16 v[48:51], v[160:163], v[168:171], v[48:51]
	v_mfma_f32_16x16x32_bf16 v[36:39], v[152:155], v[176:179], v[36:39]
	v_mfma_f32_16x16x32_bf16 v[32:35], v[160:163], v[176:179], v[32:35]
	v_mfma_f32_16x16x32_bf16 v[20:23], v[152:155], v[184:187], v[20:23]
	v_mfma_f32_16x16x32_bf16 v[16:19], v[160:163], v[184:187], v[16:19]
	v_mfma_f32_16x16x32_bf16 v[4:7], v[152:155], v[194:197], v[4:7]
	v_mfma_f32_16x16x32_bf16 v[0:3], v[160:163], v[194:197], v[0:3]
	v_mfma_f32_16x16x32_bf16 v[52:55], v[156:159], v[172:175], v[52:55]
	v_mfma_f32_16x16x32_bf16 v[48:51], v[164:167], v[172:175], v[48:51]
	v_mfma_f32_16x16x32_bf16 v[36:39], v[156:159], v[180:183], v[36:39]
	v_mfma_f32_16x16x32_bf16 v[32:35], v[164:167], v[180:183], v[32:35]
	v_mfma_f32_16x16x32_bf16 v[20:23], v[156:159], v[188:191], v[20:23]
	v_mfma_f32_16x16x32_bf16 v[16:19], v[164:167], v[188:191], v[16:19]
	v_mfma_f32_16x16x32_bf16 v[4:7], v[156:159], v[198:201], v[4:7]
	v_mfma_f32_16x16x32_bf16 v[0:3], v[164:167], v[198:201], v[0:3]
	s_setprio 0
	s_barrier
	s_add_i32 s60, s60, 2
	s_addk_i32 s58, 0x100
	s_addk_i32 s59, 0x100
	s_cmp_ge_i32 s60, s35
	s_cbranch_scc0 .LBB0_450
	s_and_b64 vcc, exec, s[12:13]
	s_cbranch_vccz .LBB0_453

; #define PG8_STAGE(bufoff, rs_, soff_, voff) do { _Pragma("unroll") for (int _i = 0; _i < 2; ++_i) \
;         __builtin_amdgcn_raw_ptr_buffer_load_lds(rs_, (LAS void*)(lds + (bufoff) + ldsw + _i * 8192), 16, (int)(voff)[_i], (int)(soff_), 0, 0); } while (0)
; #define PG8_LDA(dst, b, h) do { _Pragma("unroll") for (int m = 0; m < 4; ++m) dst[m] = PG8_LD2(lds + PG8_SA(b, h) + aoff + m * 2048); } while (0)
; #define PG8_LDB(dst, b, h) do { _Pragma("unroll") for (int n = 0; n < 2; ++n) dst[n] = PG8_LD2(lds + PG8_SB(b, h) + boff + n * 2048); } while (0)
; #define PG8_BAR __builtin_amdgcn_s_barrier()
; template <class Epi, class Sched, bool ALIGN_EPI = false, bool SP2 = false, bool FP8 = false>
; __device__ __forceinline__ void gemm_phase(LAS unsigned char* lds, const Gemm g, const Sched& S, const Epi& E, int wbase) {
;     ...
;             const bool last = (t == nt - 2);
;             const unsigned a1 = cA + (unsigned)(t + 1) * kstep;
;             const unsigned a2 = last ? nA : cA + (unsigned)(t + 2) * kstep, b2 = last ? nB : cB + (unsigned)(t + 2) * kstep; const rsrc_t rA2 = (Sched::TWO && last) ? rAn : rAc, rB2 = (Sched::TWO && last) ? rBn : rBc;
;             const unsigned a3 = a2 + kstep, b3 = b2 + kstep;
;             if (last && has_next) S.a_ready(nxt);
;             if constexpr (SP2) {
;             PG8_LDB(B0, 0, 0); PG8_LDB(B1, 0, 1); PG8_SCHED; PG8_LDA(At, 0, 0); PG8_STAGE(PG8_SA(1, 1), rAc, a1 + hstep, voffA);
;             PG8_WAIT_V(8); PG8_WAIT_L(0); PG8_BAR; PG8_MMA(0, 0, At, B0); PG8_MMA(0, 1, At, B1); PG8_BAR; PG8_SCHED;
;             PG8_LDA(At, 0, 1); PG8_STAGE(PG8_SB(0, 0), rB2, b2, voffB); PG8_STAGE(PG8_SB(0, 1), rB2, b2 + hstep, voffB); PG8_STAGE(PG8_SA(0, 0), rA2, a2, voffA);
;             PG8_WAIT_V(8); PG8_WAIT_L(0); PG8_BAR; PG8_MMA(1, 0, At, B0); PG8_MMA(1, 1, At, B1); PG8_BAR; PG8_SCHED;
;             PG8_LDB(B0, 1, 0); PG8_LDB(B1, 1, 1); PG8_SCHED; PG8_LDA(At, 1, 0); PG8_STAGE(PG8_SA(0, 1), rA2, a2 + hstep, voffA);
;             PG8_WAIT_V(8); PG8_WAIT_L(0); PG8_BAR; PG8_MMA(0, 0, At, B0); PG8_MMA(0, 1, At, B1); PG8_BAR; PG8_SCHED;
;             PG8_LDA(At, 1, 1); PG8_STAGE(PG8_SB(1, 0), rB2, b3, voffB); PG8_STAGE(PG8_SB(1, 1), rB2, b3 + hstep, voffB); PG8_STAGE(PG8_SA(1, 0), rA2, a3, voffA);
;             PG8_WAIT_V(8); PG8_WAIT_L(0); PG8_BAR; PG8_MMA(1, 0, At, B0); PG8_MMA(1, 1, At, B1); PG8_BAR; PG8_SCHED;
.LBB0_813:
	s_add_i32 s20, vcc_hi, 0x80
	v_add_u32_e32 v140, 0x10000, v240
	v_add_u32_e32 v156, 0x14000, v240
	s_cmp_eq_u32 s41, s78
	ds_read_b128 v[128:131], v140
	ds_read_b128 v[132:135], v140 offset:1024
	ds_read_b128 v[136:139], v140 offset:2048
	ds_read_b128 v[140:143], v140 offset:3072
	ds_read_b128 v[144:147], v156
	ds_read_b128 v[148:151], v156 offset:1024
	ds_read_b128 v[152:155], v156 offset:2048
	ds_read_b128 v[156:159], v156 offset:3072
	s_cselect_b64 s[16:17], -1, 0
	s_and_b64 s[18:19], s[16:17], exec
	s_cselect_b32 s68, s67, s20
	s_cselect_b32 s54, vcc_lo, s3
	s_and_b64 s[20:21], s[44:45], s[16:17]
	s_and_b64 s[16:17], s[20:21], exec
	s_cselect_b32 s18, s52, s14
	s_cselect_b32 s19, s53, s15
	s_cselect_b32 s17, s35, s13
	s_cselect_b32 s16, s34, s12
	s_or_b32 s55, s68, 0x80
	s_and_b64 s[20:21], s[20:21], exec
	s_cselect_b32 s23, s53, s31
	s_cselect_b32 s22, s52, s30
	s_cselect_b32 s21, s11, s59
	s_cselect_b32 s20, s10, s58
	s_add_i32 s69, s46, vcc_hi
	s_mov_b32 m0, s61
	ds_read_b128 v[160:163], v241
	ds_read_b128 v[164:167], v241 offset:1024
	ds_read_b128 v[168:171], v241 offset:2048
	ds_read_b128 v[172:175], v241 offset:3072
	ds_read_b128 v[176:179], v241 offset:4096
	ds_read_b128 v[180:183], v241 offset:5120
	ds_read_b128 v[184:187], v241 offset:6144
	ds_read_b128 v[188:191], v241 offset:7168
	buffer_load_dwordx4 v192, s[12:15], s69 offen lds
	s_mov_b32 m0, s62
	s_nop 0
	buffer_load_dwordx4 v236, s[12:15], s69 offen lds
	s_waitcnt vmcnt(8)
	s_waitcnt lgkmcnt(0)
	s_barrier
	s_setprio 1
	v_mfma_f32_16x16x128_f8f6f4 v[124:127], v[128:135], v[160:167], v[124:127]
	v_mfma_f32_16x16x128_f8f6f4 v[120:123], v[136:143], v[160:167], v[120:123]
	v_mfma_f32_16x16x128_f8f6f4 v[116:119], v[128:135], v[168:175], v[116:119]
	v_mfma_f32_16x16x128_f8f6f4 v[112:115], v[136:143], v[168:175], v[112:115]
	v_mfma_f32_16x16x128_f8f6f4 v[108:111], v[128:135], v[176:183], v[108:111]
	v_mfma_f32_16x16x128_f8f6f4 v[104:107], v[136:143], v[176:183], v[104:107]
	v_mfma_f32_16x16x128_f8f6f4 v[100:103], v[128:135], v[184:191], v[100:103]
	v_mfma_f32_16x16x128_f8f6f4 v[96:99], v[136:143], v[184:191], v[96:99]
	s_setprio 0
	s_setprio 1
	v_mfma_f32_16x16x128_f8f6f4 v[194:197], v[144:151], v[160:167], v[92:95]
	v_mfma_f32_16x16x128_f8f6f4 v[160:163], v[152:159], v[160:167], v[88:91]
	v_mfma_f32_16x16x128_f8f6f4 v[164:167], v[144:151], v[168:175], v[84:87]
	v_mfma_f32_16x16x128_f8f6f4 v[168:171], v[152:159], v[168:175], v[80:83]
	v_mfma_f32_16x16x128_f8f6f4 v[172:175], v[144:151], v[176:183], v[76:79]
	v_mfma_f32_16x16x128_f8f6f4 v[176:179], v[152:159], v[176:183], v[72:75]
	v_mfma_f32_16x16x128_f8f6f4 v[180:183], v[144:151], v[184:191], v[68:71]
	v_mfma_f32_16x16x128_f8f6f4 v[184:187], v[152:159], v[184:191], v[64:67]
	s_setprio 0
	s_barrier
	s_mov_b32 m0, s48
	s_nop 3
	ds_read_b128 v[64:67], v241 offset:16384
	ds_read_b128 v[68:71], v241 offset:17408
	ds_read_b128 v[72:75], v241 offset:18432
	ds_read_b128 v[76:79], v241 offset:19456
	ds_read_b128 v[80:83], v241 offset:20480
	ds_read_b128 v[84:87], v241 offset:21504
	ds_read_b128 v[88:91], v241 offset:22528
	ds_read_b128 v[92:95], v241 offset:23552
	buffer_load_dwordx4 v235, s[20:23], s54 offen lds
	s_mov_b32 m0, s56
	s_add_i32 s69, s54, s46
	buffer_load_dwordx4 v237, s[20:23], s54 offen lds
	s_mov_b32 m0, s57
	s_nop 0
	buffer_load_dwordx4 v235, s[20:23], s69 offen lds
	s_mov_b32 m0, s65
	s_nop 0
	buffer_load_dwordx4 v237, s[20:23], s69 offen lds
	s_mov_b32 m0, s47
	s_nop 0
	buffer_load_dwordx4 v192, s[16:19], s68 offen lds
	s_mov_b32 m0, s76
	s_nop 0
	buffer_load_dwordx4 v236, s[16:19], s68 offen lds
	s_waitcnt vmcnt(8)
	s_waitcnt lgkmcnt(0)
	s_barrier
	s_setprio 1
	v_mfma_f32_16x16x128_f8f6f4 v[60:63], v[128:135], v[64:71], v[60:63]
	v_mfma_f32_16x16x128_f8f6f4 v[56:59], v[136:143], v[64:71], v[56:59]
	v_mfma_f32_16x16x128_f8f6f4 v[52:55], v[128:135], v[72:79], v[52:55]
	v_mfma_f32_16x16x128_f8f6f4 v[48:51], v[136:143], v[72:79], v[48:51]
	v_mfma_f32_16x16x128_f8f6f4 v[188:191], v[128:135], v[80:87], v[44:47]
	v_mfma_f32_16x16x128_f8f6f4 v[198:201], v[136:143], v[80:87], v[40:43]
	v_mfma_f32_16x16x128_f8f6f4 v[202:205], v[128:135], v[88:95], v[36:39]
	v_mfma_f32_16x16x128_f8f6f4 v[206:209], v[136:143], v[88:95], v[32:35]
	s_setprio 0
	s_setprio 1
	v_mfma_f32_16x16x128_f8f6f4 v[210:213], v[144:151], v[64:71], v[28:31]
	v_mfma_f32_16x16x128_f8f6f4 v[214:217], v[152:159], v[64:71], v[24:27]
	v_mfma_f32_16x16x128_f8f6f4 v[218:221], v[144:151], v[72:79], v[20:23]
	v_mfma_f32_16x16x128_f8f6f4 v[226:229], v[152:159], v[72:79], v[16:19]
	v_mfma_f32_16x16x128_f8f6f4 v[242:245], v[144:151], v[80:87], v[12:15]
	v_mfma_f32_16x16x128_f8f6f4 v[246:249], v[152:159], v[80:87], v[8:11]
	v_mfma_f32_16x16x128_f8f6f4 v[250:253], v[144:151], v[88:95], v[4:7]
	v_mfma_f32_16x16x128_f8f6f4 v[230:233], v[152:159], v[88:95], v[0:3]
	s_setprio 0
	s_barrier
; #define PG8_STAGE(bufoff, rs_, soff_, voff) do { _Pragma("unroll") for (int _i = 0; _i < 2; ++_i) \
;         __builtin_amdgcn_raw_ptr_buffer_load_lds(rs_, (LAS void*)(lds + (bufoff) + ldsw + _i * 8192), 16, (int)(voff)[_i], (int)(soff_), 0, 0); } while (0)
; #define PG8_LDA(dst, b, h) do { _Pragma("unroll") for (int m = 0; m < 4; ++m) dst[m] = PG8_LD2(lds + PG8_SA(b, h) + aoff + m * 2048); } while (0)
; #define PG8_LDB(dst, b, h) do { _Pragma("unroll") for (int n = 0; n < 2; ++n) dst[n] = PG8_LD2(lds + PG8_SB(b, h) + boff + n * 2048); } while (0)
; #define PG8_WAIT_V(n) asm volatile("s_waitcnt vmcnt(" #n ")" ::: "memory")
; #define PG8_WAIT_L(n) asm volatile("s_waitcnt lgkmcnt(" #n ")" ::: "memory")
; #define PG8_BAR __builtin_amdgcn_s_barrier()
; #define PG8_SCHED __builtin_amdgcn_sched_barrier(0)
; template <class Epi, class Sched, bool ALIGN_EPI = false, bool SP2 = false, bool FP8 = false>
; __device__ __forceinline__ void gemm_phase(LAS unsigned char* lds, const Gemm g, const Sched& S, const Epi& E, int wbase) {
;     ...
;         for (int t = 0; t < nt; t += 2) {
;             const bool last = (t == nt - 2);
;             const unsigned a1 = cA + (unsigned)(t + 1) * kstep;
;             const unsigned a2 = last ? nA : cA + (unsigned)(t + 2) * kstep, b2 = last ? nB : cB + (unsigned)(t + 2) * kstep; const rsrc_t rA2 = (Sched::TWO && last) ? rAn : rAc, rB2 = (Sched::TWO && last) ? rBn : rBc;
;             const unsigned a3 = a2 + kstep, b3 = b2 + kstep;
;             if (last && has_next) S.a_ready(nxt);
;     ...
;             PG8_LDB(B0, 1, 0); PG8_LDB(B1, 1, 1); PG8_SCHED; PG8_LDA(At, 1, 0); PG8_STAGE(PG8_SA(0, 1), rA2, a2 + hstep, voffA);
;             PG8_WAIT_V(8); PG8_WAIT_L(0); PG8_BAR; PG8_MMA(0, 0, At, B0); PG8_MMA(0, 1, At, B1); PG8_BAR; PG8_SCHED;
;             PG8_LDA(At, 1, 1); PG8_STAGE(PG8_SB(1, 0), rB2, b3, voffB); PG8_STAGE(PG8_SB(1, 1), rB2, b3 + hstep, voffB); PG8_STAGE(PG8_SA(1, 0), rA2, a3, voffA);
;             PG8_WAIT_V(8); PG8_WAIT_L(0); PG8_BAR; PG8_MMA(1, 0, At, B0); PG8_MMA(1, 1, At, B1); PG8_BAR; PG8_SCHED;
	s_nop 1
	v_add_u32_e32 v12, 0x18000, v240
	v_add_u32_e32 v16, 0x1c000, v240
	s_nop 0
	ds_read_b128 v[0:3], v12
	ds_read_b128 v[4:7], v12 offset:1024
	ds_read_b128 v[8:11], v12 offset:2048
	ds_read_b128 v[12:15], v12 offset:3072
	ds_read_b128 v[128:131], v16
	ds_read_b128 v[132:135], v16 offset:1024
	ds_read_b128 v[136:139], v16 offset:2048
	ds_read_b128 v[140:143], v16 offset:3072
	s_add_i32 s68, s68, s46
	s_mov_b32 m0, s77
	ds_read_b128 v[16:19], v241 offset:32768
	ds_read_b128 v[20:23], v241 offset:33792
	ds_read_b128 v[24:27], v241 offset:34816
	ds_read_b128 v[28:31], v241 offset:35840
	ds_read_b128 v[32:35], v241 offset:36864
	ds_read_b128 v[36:39], v241 offset:37888
	ds_read_b128 v[40:43], v241 offset:38912
	ds_read_b128 v[44:47], v241 offset:39936
	buffer_load_dwordx4 v192, s[16:19], s68 offen lds
	s_mov_b32 m0, s79
	s_nop 0
	buffer_load_dwordx4 v236, s[16:19], s68 offen lds
	s_waitcnt vmcnt(8)
	s_waitcnt lgkmcnt(0)
	s_barrier
	s_setprio 1
	v_mfma_f32_16x16x128_f8f6f4 v[124:127], v[0:7], v[16:23], v[124:127]
	v_mfma_f32_16x16x128_f8f6f4 v[120:123], v[8:15], v[16:23], v[120:123]
	v_mfma_f32_16x16x128_f8f6f4 v[116:119], v[0:7], v[24:31], v[116:119]
	v_mfma_f32_16x16x128_f8f6f4 v[112:115], v[8:15], v[24:31], v[112:115]
	v_mfma_f32_16x16x128_f8f6f4 v[108:111], v[0:7], v[32:39], v[108:111]
	v_mfma_f32_16x16x128_f8f6f4 v[104:107], v[8:15], v[32:39], v[104:107]
	v_mfma_f32_16x16x128_f8f6f4 v[100:103], v[0:7], v[40:47], v[100:103]
	v_mfma_f32_16x16x128_f8f6f4 v[96:99], v[8:15], v[40:47], v[96:99]
	s_setprio 0
	s_setprio 1
	v_mfma_f32_16x16x128_f8f6f4 v[92:95], v[128:135], v[16:23], v[194:197]
	v_mfma_f32_16x16x128_f8f6f4 v[88:91], v[136:143], v[16:23], v[160:163]
	v_mfma_f32_16x16x128_f8f6f4 v[84:87], v[128:135], v[24:31], v[164:167]
	v_mfma_f32_16x16x128_f8f6f4 v[80:83], v[136:143], v[24:31], v[168:171]
	v_mfma_f32_16x16x128_f8f6f4 v[76:79], v[128:135], v[32:39], v[172:175]
	v_mfma_f32_16x16x128_f8f6f4 v[72:75], v[136:143], v[32:39], v[176:179]
	v_mfma_f32_16x16x128_f8f6f4 v[68:71], v[128:135], v[40:47], v[180:183]
	v_mfma_f32_16x16x128_f8f6f4 v[64:67], v[136:143], v[40:47], v[184:187]
	s_setprio 0
	s_barrier
	s_mov_b32 m0, s84
	s_bitset1_b32 s54, 7
	ds_read_b128 v[16:19], v241 offset:49152
	ds_read_b128 v[20:23], v241 offset:50176
	ds_read_b128 v[144:147], v241 offset:51200
	ds_read_b128 v[148:151], v241 offset:52224
	ds_read_b128 v[152:155], v241 offset:53248
	ds_read_b128 v[156:159], v241 offset:54272
	ds_read_b128 v[160:163], v241 offset:55296
	ds_read_b128 v[164:167], v241 offset:56320
	buffer_load_dwordx4 v235, s[20:23], s54 offen lds
	s_mov_b32 m0, s85
	s_nop 0
	buffer_load_dwordx4 v237, s[20:23], s54 offen lds
	s_add_i32 s54, s54, s46
	s_mov_b32 m0, s96
	s_nop 0
	buffer_load_dwordx4 v235, s[20:23], s54 offen lds
	s_mov_b32 m0, s97
	s_nop 0
	buffer_load_dwordx4 v237, s[20:23], s54 offen lds
	s_mov_b32 m0, s94
	s_nop 0
	buffer_load_dwordx4 v192, s[16:19], s55 offen lds
	s_mov_b32 m0, s95
	s_nop 0
	buffer_load_dwordx4 v236, s[16:19], s55 offen lds
	s_waitcnt vmcnt(8)
	s_waitcnt lgkmcnt(0)
	s_barrier
	s_setprio 1
	v_mfma_f32_16x16x128_f8f6f4 v[60:63], v[0:7], v[16:23], v[60:63]
	v_mfma_f32_16x16x128_f8f6f4 v[56:59], v[8:15], v[16:23], v[56:59]
	v_mfma_f32_16x16x128_f8f6f4 v[52:55], v[0:7], v[144:151], v[52:55]
	v_mfma_f32_16x16x128_f8f6f4 v[48:51], v[8:15], v[144:151], v[48:51]
	v_mfma_f32_16x16x128_f8f6f4 v[44:47], v[0:7], v[152:159], v[188:191]
	v_mfma_f32_16x16x128_f8f6f4 v[40:43], v[8:15], v[152:159], v[198:201]
	v_mfma_f32_16x16x128_f8f6f4 v[36:39], v[0:7], v[160:167], v[202:205]
	v_mfma_f32_16x16x128_f8f6f4 v[32:35], v[8:15], v[160:167], v[206:209]
	s_setprio 0
	s_setprio 1
	v_mfma_f32_16x16x128_f8f6f4 v[28:31], v[128:135], v[16:23], v[210:213]
	v_mfma_f32_16x16x128_f8f6f4 v[24:27], v[136:143], v[16:23], v[214:217]
	v_mfma_f32_16x16x128_f8f6f4 v[20:23], v[128:135], v[144:151], v[218:221]
	v_mfma_f32_16x16x128_f8f6f4 v[16:19], v[136:143], v[144:151], v[226:229]
	v_mfma_f32_16x16x128_f8f6f4 v[12:15], v[128:135], v[152:159], v[242:245]
	v_mfma_f32_16x16x128_f8f6f4 v[8:11], v[136:143], v[152:159], v[246:249]
	v_mfma_f32_16x16x128_f8f6f4 v[4:7], v[128:135], v[160:167], v[250:253]
	v_mfma_f32_16x16x128_f8f6f4 v[0:3], v[136:143], v[160:167], v[230:233]
	s_setprio 0
	s_barrier
	s_add_i32 s78, s78, 2
	s_addk_i32 vcc_hi, 0x100
	s_addk_i32 s3, 0x100
	s_cmp_ge_i32 s78, s60
	s_cbranch_scc0 .LBB0_813
	v_readlane_b32 s68, v255, 22
	v_readlane_b32 s54, v255, 25
	v_readlane_b32 s69, v255, 23
	v_readlane_b32 s55, v255, 26
	v_mov_b32_e32 v230, v193
	v_mov_b32_e32 v231, v222

; #define PG8_STAGE(bufoff, rs_, soff_, voff) do { _Pragma("unroll") for (int _i = 0; _i < 2; ++_i) \
;         __builtin_amdgcn_raw_ptr_buffer_load_lds(rs_, (LAS void*)(lds + (bufoff) + ldsw + _i * 8192), 16, (int)(voff)[_i], (int)(soff_), 0, 0); } while (0)
; #define PG8_LDA(dst, b, h) do { _Pragma("unroll") for (int m = 0; m < 4; ++m) dst[m] = PG8_LD2(lds + PG8_SA(b, h) + aoff + m * 2048); } while (0)
; #define PG8_LDB(dst, b, h) do { _Pragma("unroll") for (int n = 0; n < 2; ++n) dst[n] = PG8_LD2(lds + PG8_SB(b, h) + boff + n * 2048); } while (0)
; #define PG8_BAR __builtin_amdgcn_s_barrier()
; template <class Epi, class Sched, bool ALIGN_EPI = false, bool SP2 = false, bool FP8 = false>
; __device__ __forceinline__ void gemm_phase(LAS unsigned char* lds, const Gemm g, const Sched& S, const Epi& E, int wbase) {
;     ...
;             const bool last = (t == nt - 2);
;             const unsigned a1 = cA + (unsigned)(t + 1) * kstep;
;             const unsigned a2 = last ? nA : cA + (unsigned)(t + 2) * kstep, b2 = last ? nB : cB + (unsigned)(t + 2) * kstep; const rsrc_t rA2 = (Sched::TWO && last) ? rAn : rAc, rB2 = (Sched::TWO && last) ? rBn : rBc;
;             const unsigned a3 = a2 + kstep, b3 = b2 + kstep;
;             if (last && has_next) S.a_ready(nxt);
;             if constexpr (SP2) {
;             PG8_LDB(B0, 0, 0); PG8_LDB(B1, 0, 1); PG8_SCHED; PG8_LDA(At, 0, 0); PG8_STAGE(PG8_SA(1, 1), rAc, a1 + hstep, voffA);
;             PG8_WAIT_V(8); PG8_WAIT_L(0); PG8_BAR; PG8_MMA(0, 0, At, B0); PG8_MMA(0, 1, At, B1); PG8_BAR; PG8_SCHED;
;             PG8_LDA(At, 0, 1); PG8_STAGE(PG8_SB(0, 0), rB2, b2, voffB); PG8_STAGE(PG8_SB(0, 1), rB2, b2 + hstep, voffB); PG8_STAGE(PG8_SA(0, 0), rA2, a2, voffA);
;             PG8_WAIT_V(8); PG8_WAIT_L(0); PG8_BAR; PG8_MMA(1, 0, At, B0); PG8_MMA(1, 1, At, B1); PG8_BAR; PG8_SCHED;
;             PG8_LDB(B0, 1, 0); PG8_LDB(B1, 1, 1); PG8_SCHED; PG8_LDA(At, 1, 0); PG8_STAGE(PG8_SA(0, 1), rA2, a2 + hstep, voffA);
;             PG8_WAIT_V(8); PG8_WAIT_L(0); PG8_BAR; PG8_MMA(0, 0, At, B0); PG8_MMA(0, 1, At, B1); PG8_BAR; PG8_SCHED;
;             PG8_LDA(At, 1, 1); PG8_STAGE(PG8_SB(1, 0), rB2, b3, voffB); PG8_STAGE(PG8_SB(1, 1), rB2, b3 + hstep, voffB); PG8_STAGE(PG8_SA(1, 0), rA2, a3, voffA);
;             PG8_WAIT_V(8); PG8_WAIT_L(0); PG8_BAR; PG8_MMA(1, 0, At, B0); PG8_MMA(1, 1, At, B1); PG8_BAR; PG8_SCHED;
.LBB0_847:
	s_add_i32 s20, vcc_lo, 0x80
	v_add_u32_e32 v140, 0x10000, v238
	v_add_u32_e32 v156, 0x14000, v238
	s_cmp_eq_u32 s88, s85
	ds_read_b128 v[128:131], v140
	ds_read_b128 v[132:135], v140 offset:1024
	ds_read_b128 v[136:139], v140 offset:2048
	ds_read_b128 v[140:143], v140 offset:3072
	ds_read_b128 v[144:147], v156
	ds_read_b128 v[148:151], v156 offset:1024
	ds_read_b128 v[152:155], v156 offset:2048
	ds_read_b128 v[156:159], v156 offset:3072
	s_cselect_b64 s[16:17], -1, 0
	s_and_b64 s[18:19], s[16:17], exec
	s_cselect_b32 s68, s67, s20
	s_cselect_b32 s54, s78, vcc_hi
	s_and_b64 s[20:21], s[58:59], s[16:17]
	s_and_b64 s[16:17], s[20:21], exec
	s_cselect_b32 s18, s30, s14
	s_cselect_b32 s19, s31, s15
	s_cselect_b32 s17, s35, s13
	s_cselect_b32 s16, s34, s12
	s_or_b32 s55, s68, 0x80
	s_and_b64 s[20:21], s[20:21], exec
	s_cselect_b32 s23, s31, s53
	s_cselect_b32 s22, s30, s52
	s_cselect_b32 s21, s45, s11
	s_cselect_b32 s20, s44, s10
	s_add_i32 s69, s41, vcc_lo
	s_mov_b32 m0, s89
	ds_read_b128 v[160:163], v239
	ds_read_b128 v[164:167], v239 offset:1024
	ds_read_b128 v[168:171], v239 offset:2048
	ds_read_b128 v[172:175], v239 offset:3072
	ds_read_b128 v[176:179], v239 offset:4096
	ds_read_b128 v[180:183], v239 offset:5120
	ds_read_b128 v[184:187], v239 offset:6144
	ds_read_b128 v[188:191], v239 offset:7168
	buffer_load_dwordx4 v192, s[12:15], s69 offen lds
	s_mov_b32 m0, s92
	s_nop 0
	buffer_load_dwordx4 v223, s[12:15], s69 offen lds
	s_waitcnt vmcnt(8)
	s_waitcnt lgkmcnt(0)
	s_barrier
	s_setprio 1
	v_mfma_f32_16x16x32_bf16 v[124:127], v[128:131], v[160:163], v[124:127]
	v_mfma_f32_16x16x32_bf16 v[120:123], v[136:139], v[160:163], v[120:123]
	v_mfma_f32_16x16x32_bf16 v[116:119], v[128:131], v[168:171], v[116:119]
	v_mfma_f32_16x16x32_bf16 v[112:115], v[136:139], v[168:171], v[112:115]
	v_mfma_f32_16x16x32_bf16 v[108:111], v[128:131], v[176:179], v[108:111]
	v_mfma_f32_16x16x32_bf16 v[104:107], v[136:139], v[176:179], v[104:107]
	v_mfma_f32_16x16x32_bf16 v[100:103], v[128:131], v[184:187], v[100:103]
	v_mfma_f32_16x16x32_bf16 v[96:99], v[136:139], v[184:187], v[96:99]
	v_mfma_f32_16x16x32_bf16 v[124:127], v[132:135], v[164:167], v[124:127]
	v_mfma_f32_16x16x32_bf16 v[120:123], v[140:143], v[164:167], v[120:123]
	v_mfma_f32_16x16x32_bf16 v[116:119], v[132:135], v[172:175], v[116:119]
	v_mfma_f32_16x16x32_bf16 v[112:115], v[140:143], v[172:175], v[112:115]
	v_mfma_f32_16x16x32_bf16 v[108:111], v[132:135], v[180:183], v[108:111]
	v_mfma_f32_16x16x32_bf16 v[104:107], v[140:143], v[180:183], v[104:107]
	v_mfma_f32_16x16x32_bf16 v[100:103], v[132:135], v[188:191], v[100:103]
	v_mfma_f32_16x16x32_bf16 v[96:99], v[140:143], v[188:191], v[96:99]
	s_setprio 0
	s_setprio 1
	v_mfma_f32_16x16x32_bf16 v[92:95], v[144:147], v[160:163], v[92:95]
	v_mfma_f32_16x16x32_bf16 v[88:91], v[152:155], v[160:163], v[88:91]
	v_mfma_f32_16x16x32_bf16 v[84:87], v[144:147], v[168:171], v[84:87]
	v_mfma_f32_16x16x32_bf16 v[80:83], v[152:155], v[168:171], v[80:83]
	v_mfma_f32_16x16x32_bf16 v[76:79], v[144:147], v[176:179], v[76:79]
	v_mfma_f32_16x16x32_bf16 v[72:75], v[152:155], v[176:179], v[72:75]
	v_mfma_f32_16x16x32_bf16 v[68:71], v[144:147], v[184:187], v[68:71]
	v_mfma_f32_16x16x32_bf16 v[64:67], v[152:155], v[184:187], v[64:67]
	v_mfma_f32_16x16x32_bf16 v[92:95], v[148:151], v[164:167], v[92:95]
	v_mfma_f32_16x16x32_bf16 v[88:91], v[156:159], v[164:167], v[88:91]
	v_mfma_f32_16x16x32_bf16 v[84:87], v[148:151], v[172:175], v[84:87]
	v_mfma_f32_16x16x32_bf16 v[80:83], v[156:159], v[172:175], v[80:83]
	v_mfma_f32_16x16x32_bf16 v[76:79], v[148:151], v[180:183], v[76:79]
	v_mfma_f32_16x16x32_bf16 v[72:75], v[156:159], v[180:183], v[72:75]
	v_mfma_f32_16x16x32_bf16 v[68:71], v[148:151], v[188:191], v[68:71]
	v_mfma_f32_16x16x32_bf16 v[64:67], v[156:159], v[188:191], v[64:67]
	s_setprio 0
	s_barrier
	s_mov_b32 m0, s43
	ds_read_b128 v[160:163], v239 offset:16384
	ds_read_b128 v[164:167], v239 offset:17408
	ds_read_b128 v[168:171], v239 offset:18432
	ds_read_b128 v[172:175], v239 offset:19456
	ds_read_b128 v[176:179], v239 offset:20480
	ds_read_b128 v[180:183], v239 offset:21504
	ds_read_b128 v[184:187], v239 offset:22528
	ds_read_b128 v[188:191], v239 offset:23552
	buffer_load_dwordx4 v222, s[20:23], s54 offen lds
	s_mov_b32 m0, s46
	s_add_i32 s69, s54, s41
	buffer_load_dwordx4 v235, s[20:23], s54 offen lds
	s_mov_b32 m0, s47
	s_nop 0
	buffer_load_dwordx4 v222, s[20:23], s69 offen lds
	s_mov_b32 m0, s48
	s_nop 0
	buffer_load_dwordx4 v235, s[20:23], s69 offen lds
	s_mov_b32 m0, s42
	s_nop 0
	buffer_load_dwordx4 v192, s[16:19], s68 offen lds
	s_mov_b32 m0, s56
	s_nop 0
	buffer_load_dwordx4 v223, s[16:19], s68 offen lds
	s_waitcnt vmcnt(8)
	s_waitcnt lgkmcnt(0)
	s_barrier
; #define PG8_STAGE(bufoff, rs_, soff_, voff) do { _Pragma("unroll") for (int _i = 0; _i < 2; ++_i) \
;         __builtin_amdgcn_raw_ptr_buffer_load_lds(rs_, (LAS void*)(lds + (bufoff) + ldsw + _i * 8192), 16, (int)(voff)[_i], (int)(soff_), 0, 0); } while (0)
; #define PG8_LDA(dst, b, h) do { _Pragma("unroll") for (int m = 0; m < 4; ++m) dst[m] = PG8_LD2(lds + PG8_SA(b, h) + aoff + m * 2048); } while (0)
; #define PG8_LDB(dst, b, h) do { _Pragma("unroll") for (int n = 0; n < 2; ++n) dst[n] = PG8_LD2(lds + PG8_SB(b, h) + boff + n * 2048); } while (0)
; #define PG8_WAIT_V(n) asm volatile("s_waitcnt vmcnt(" #n ")" ::: "memory")
; #define PG8_WAIT_L(n) asm volatile("s_waitcnt lgkmcnt(" #n ")" ::: "memory")
; #define PG8_BAR __builtin_amdgcn_s_barrier()
; #define PG8_SCHED __builtin_amdgcn_sched_barrier(0)
; template <class Epi, class Sched, bool ALIGN_EPI = false, bool SP2 = false, bool FP8 = false>
; __device__ __forceinline__ void gemm_phase(LAS unsigned char* lds, const Gemm g, const Sched& S, const Epi& E, int wbase) {
;     ...
;             PG8_LDB(B0, 0, 0); PG8_LDB(B1, 0, 1); PG8_SCHED; PG8_LDA(At, 0, 0); PG8_STAGE(PG8_SA(1, 1), rAc, a1 + hstep, voffA);
;             PG8_WAIT_V(8); PG8_WAIT_L(0); PG8_BAR; PG8_MMA(0, 0, At, B0); PG8_MMA(0, 1, At, B1); PG8_BAR; PG8_SCHED;
;             PG8_LDA(At, 0, 1); PG8_STAGE(PG8_SB(0, 0), rB2, b2, voffB); PG8_STAGE(PG8_SB(0, 1), rB2, b2 + hstep, voffB); PG8_STAGE(PG8_SA(0, 0), rA2, a2, voffA);
;             PG8_WAIT_V(8); PG8_WAIT_L(0); PG8_BAR; PG8_MMA(1, 0, At, B0); PG8_MMA(1, 1, At, B1); PG8_BAR; PG8_SCHED;
;             PG8_LDB(B0, 1, 0); PG8_LDB(B1, 1, 1); PG8_SCHED; PG8_LDA(At, 1, 0); PG8_STAGE(PG8_SA(0, 1), rA2, a2 + hstep, voffA);
;             PG8_WAIT_V(8); PG8_WAIT_L(0); PG8_BAR; PG8_MMA(0, 0, At, B0); PG8_MMA(0, 1, At, B1); PG8_BAR; PG8_SCHED;
;             PG8_LDA(At, 1, 1); PG8_STAGE(PG8_SB(1, 0), rB2, b3, voffB); PG8_STAGE(PG8_SB(1, 1), rB2, b3 + hstep, voffB); PG8_STAGE(PG8_SA(1, 0), rA2, a3, voffA);
;             PG8_WAIT_V(8); PG8_WAIT_L(0); PG8_BAR; PG8_MMA(1, 0, At, B0); PG8_MMA(1, 1, At, B1); PG8_BAR; PG8_SCHED;
	s_setprio 1
	v_mfma_f32_16x16x32_bf16 v[60:63], v[128:131], v[160:163], v[60:63]
	v_mfma_f32_16x16x32_bf16 v[56:59], v[136:139], v[160:163], v[56:59]
	v_mfma_f32_16x16x32_bf16 v[52:55], v[128:131], v[168:171], v[52:55]
	v_mfma_f32_16x16x32_bf16 v[48:51], v[136:139], v[168:171], v[48:51]
	v_mfma_f32_16x16x32_bf16 v[44:47], v[128:131], v[176:179], v[44:47]
	v_mfma_f32_16x16x32_bf16 v[40:43], v[136:139], v[176:179], v[40:43]
	v_mfma_f32_16x16x32_bf16 v[36:39], v[128:131], v[184:187], v[36:39]
	v_mfma_f32_16x16x32_bf16 v[32:35], v[136:139], v[184:187], v[32:35]
	v_mfma_f32_16x16x32_bf16 v[60:63], v[132:135], v[164:167], v[60:63]
	v_mfma_f32_16x16x32_bf16 v[56:59], v[140:143], v[164:167], v[56:59]
	v_mfma_f32_16x16x32_bf16 v[52:55], v[132:135], v[172:175], v[52:55]
	v_mfma_f32_16x16x32_bf16 v[48:51], v[140:143], v[172:175], v[48:51]
	v_mfma_f32_16x16x32_bf16 v[44:47], v[132:135], v[180:183], v[44:47]
	v_mfma_f32_16x16x32_bf16 v[40:43], v[140:143], v[180:183], v[40:43]
	v_mfma_f32_16x16x32_bf16 v[36:39], v[132:135], v[188:191], v[36:39]
	v_mfma_f32_16x16x32_bf16 v[32:35], v[140:143], v[188:191], v[32:35]
	s_setprio 0
	s_setprio 1
	v_mfma_f32_16x16x32_bf16 v[28:31], v[144:147], v[160:163], v[28:31]
	v_mfma_f32_16x16x32_bf16 v[24:27], v[152:155], v[160:163], v[24:27]
	v_mfma_f32_16x16x32_bf16 v[20:23], v[144:147], v[168:171], v[20:23]
	v_mfma_f32_16x16x32_bf16 v[16:19], v[152:155], v[168:171], v[16:19]
	v_mfma_f32_16x16x32_bf16 v[12:15], v[144:147], v[176:179], v[12:15]
	v_mfma_f32_16x16x32_bf16 v[8:11], v[152:155], v[176:179], v[8:11]
	v_mfma_f32_16x16x32_bf16 v[4:7], v[144:147], v[184:187], v[4:7]
	v_mfma_f32_16x16x32_bf16 v[0:3], v[152:155], v[184:187], v[0:3]
	v_mfma_f32_16x16x32_bf16 v[28:31], v[148:151], v[164:167], v[28:31]
	v_mfma_f32_16x16x32_bf16 v[24:27], v[156:159], v[164:167], v[24:27]
	v_mfma_f32_16x16x32_bf16 v[20:23], v[148:151], v[172:175], v[20:23]
	v_mfma_f32_16x16x32_bf16 v[16:19], v[156:159], v[172:175], v[16:19]
	v_mfma_f32_16x16x32_bf16 v[12:15], v[148:151], v[180:183], v[12:15]
	v_mfma_f32_16x16x32_bf16 v[8:11], v[156:159], v[180:183], v[8:11]
	v_mfma_f32_16x16x32_bf16 v[4:7], v[148:151], v[188:191], v[4:7]
	v_mfma_f32_16x16x32_bf16 v[0:3], v[156:159], v[188:191], v[0:3]
	s_setprio 0
	s_barrier
	v_add_u32_e32 v140, 0x18000, v238
	v_add_u32_e32 v156, 0x1c000, v238
	ds_read_b128 v[128:131], v140
	ds_read_b128 v[132:135], v140 offset:1024
	ds_read_b128 v[136:139], v140 offset:2048
	ds_read_b128 v[140:143], v140 offset:3072
	ds_read_b128 v[144:147], v156
	ds_read_b128 v[148:151], v156 offset:1024
	ds_read_b128 v[152:155], v156 offset:2048
	ds_read_b128 v[156:159], v156 offset:3072
	s_add_i32 s68, s68, s41
	s_mov_b32 m0, s57
	ds_read_b128 v[160:163], v239 offset:32768
	ds_read_b128 v[164:167], v239 offset:33792
	ds_read_b128 v[168:171], v239 offset:34816
	ds_read_b128 v[172:175], v239 offset:35840
	ds_read_b128 v[176:179], v239 offset:36864
	ds_read_b128 v[180:183], v239 offset:37888
	ds_read_b128 v[184:187], v239 offset:38912
	ds_read_b128 v[188:191], v239 offset:39936
	buffer_load_dwordx4 v192, s[16:19], s68 offen lds
	s_mov_b32 m0, s60
	s_nop 0
	buffer_load_dwordx4 v223, s[16:19], s68 offen lds
	s_waitcnt vmcnt(8)
	s_waitcnt lgkmcnt(0)
	s_barrier
	s_setprio 1
	v_mfma_f32_16x16x32_bf16 v[124:127], v[128:131], v[160:163], v[124:127]
	v_mfma_f32_16x16x32_bf16 v[120:123], v[136:139], v[160:163], v[120:123]
	v_mfma_f32_16x16x32_bf16 v[116:119], v[128:131], v[168:171], v[116:119]
	v_mfma_f32_16x16x32_bf16 v[112:115], v[136:139], v[168:171], v[112:115]
	v_mfma_f32_16x16x32_bf16 v[108:111], v[128:131], v[176:179], v[108:111]
	v_mfma_f32_16x16x32_bf16 v[104:107], v[136:139], v[176:179], v[104:107]
	v_mfma_f32_16x16x32_bf16 v[100:103], v[128:131], v[184:187], v[100:103]
	v_mfma_f32_16x16x32_bf16 v[96:99], v[136:139], v[184:187], v[96:99]
	v_mfma_f32_16x16x32_bf16 v[124:127], v[132:135], v[164:167], v[124:127]
	v_mfma_f32_16x16x32_bf16 v[120:123], v[140:143], v[164:167], v[120:123]
	v_mfma_f32_16x16x32_bf16 v[116:119], v[132:135], v[172:175], v[116:119]
	v_mfma_f32_16x16x32_bf16 v[112:115], v[140:143], v[172:175], v[112:115]
	v_mfma_f32_16x16x32_bf16 v[108:111], v[132:135], v[180:183], v[108:111]
	v_mfma_f32_16x16x32_bf16 v[104:107], v[140:143], v[180:183], v[104:107]
	v_mfma_f32_16x16x32_bf16 v[100:103], v[132:135], v[188:191], v[100:103]
	v_mfma_f32_16x16x32_bf16 v[96:99], v[140:143], v[188:191], v[96:99]
	s_setprio 0
	s_setprio 1
	v_mfma_f32_16x16x32_bf16 v[92:95], v[144:147], v[160:163], v[92:95]
	v_mfma_f32_16x16x32_bf16 v[88:91], v[152:155], v[160:163], v[88:91]
	v_mfma_f32_16x16x32_bf16 v[84:87], v[144:147], v[168:171], v[84:87]
	v_mfma_f32_16x16x32_bf16 v[80:83], v[152:155], v[168:171], v[80:83]
	v_mfma_f32_16x16x32_bf16 v[76:79], v[144:147], v[176:179], v[76:79]
	v_mfma_f32_16x16x32_bf16 v[72:75], v[152:155], v[176:179], v[72:75]
	v_mfma_f32_16x16x32_bf16 v[68:71], v[144:147], v[184:187], v[68:71]
	v_mfma_f32_16x16x32_bf16 v[64:67], v[152:155], v[184:187], v[64:67]
	v_mfma_f32_16x16x32_bf16 v[92:95], v[148:151], v[164:167], v[92:95]
	v_mfma_f32_16x16x32_bf16 v[88:91], v[156:159], v[164:167], v[88:91]
	v_mfma_f32_16x16x32_bf16 v[84:87], v[148:151], v[172:175], v[84:87]
	v_mfma_f32_16x16x32_bf16 v[80:83], v[156:159], v[172:175], v[80:83]
	v_mfma_f32_16x16x32_bf16 v[76:79], v[148:151], v[180:183], v[76:79]
	v_mfma_f32_16x16x32_bf16 v[72:75], v[156:159], v[180:183], v[72:75]
	v_mfma_f32_16x16x32_bf16 v[68:71], v[148:151], v[188:191], v[68:71]
	v_mfma_f32_16x16x32_bf16 v[64:67], v[156:159], v[188:191], v[64:67]
	s_setprio 0
	s_barrier
; #define PG8_STAGE(bufoff, rs_, soff_, voff) do { _Pragma("unroll") for (int _i = 0; _i < 2; ++_i) \
;         __builtin_amdgcn_raw_ptr_buffer_load_lds(rs_, (LAS void*)(lds + (bufoff) + ldsw + _i * 8192), 16, (int)(voff)[_i], (int)(soff_), 0, 0); } while (0)
; #define PG8_LDA(dst, b, h) do { _Pragma("unroll") for (int m = 0; m < 4; ++m) dst[m] = PG8_LD2(lds + PG8_SA(b, h) + aoff + m * 2048); } while (0)
; #define PG8_WAIT_V(n) asm volatile("s_waitcnt vmcnt(" #n ")" ::: "memory")
; #define PG8_WAIT_L(n) asm volatile("s_waitcnt lgkmcnt(" #n ")" ::: "memory")
; #define PG8_BAR __builtin_amdgcn_s_barrier()
; #define PG8_SCHED __builtin_amdgcn_sched_barrier(0)
; template <class Epi, class Sched, bool ALIGN_EPI = false, bool SP2 = false, bool FP8 = false>
; __device__ __forceinline__ void gemm_phase(LAS unsigned char* lds, const Gemm g, const Sched& S, const Epi& E, int wbase) {
;     ...
;         for (int t = 0; t < nt; t += 2) {
;             const bool last = (t == nt - 2);
;             const unsigned a1 = cA + (unsigned)(t + 1) * kstep;
;             const unsigned a2 = last ? nA : cA + (unsigned)(t + 2) * kstep, b2 = last ? nB : cB + (unsigned)(t + 2) * kstep; const rsrc_t rA2 = (Sched::TWO && last) ? rAn : rAc, rB2 = (Sched::TWO && last) ? rBn : rBc;
;             const unsigned a3 = a2 + kstep, b3 = b2 + kstep;
;             if (last && has_next) S.a_ready(nxt);
;     ...
;             PG8_LDA(At, 1, 1); PG8_STAGE(PG8_SB(1, 0), rB2, b3, voffB); PG8_STAGE(PG8_SB(1, 1), rB2, b3 + hstep, voffB); PG8_STAGE(PG8_SA(1, 0), rA2, a3, voffA);
;             PG8_WAIT_V(8); PG8_WAIT_L(0); PG8_BAR; PG8_MMA(1, 0, At, B0); PG8_MMA(1, 1, At, B1); PG8_BAR; PG8_SCHED;
	s_mov_b32 m0, s63
	s_bitset1_b32 s54, 7
	ds_read_b128 v[160:163], v239 offset:49152
	ds_read_b128 v[164:167], v239 offset:50176
	ds_read_b128 v[168:171], v239 offset:51200
	ds_read_b128 v[172:175], v239 offset:52224
	ds_read_b128 v[176:179], v239 offset:53248
	ds_read_b128 v[180:183], v239 offset:54272
	ds_read_b128 v[184:187], v239 offset:55296
	ds_read_b128 v[188:191], v239 offset:56320
	buffer_load_dwordx4 v222, s[20:23], s54 offen lds
	s_mov_b32 m0, s65
	s_nop 0
	buffer_load_dwordx4 v235, s[20:23], s54 offen lds
	s_add_i32 s54, s54, s41
	s_mov_b32 m0, s79
	s_nop 0
	buffer_load_dwordx4 v222, s[20:23], s54 offen lds
	s_mov_b32 m0, s80
	s_nop 0
	buffer_load_dwordx4 v235, s[20:23], s54 offen lds
	s_mov_b32 m0, s76
	s_nop 0
	buffer_load_dwordx4 v192, s[16:19], s55 offen lds
	s_mov_b32 m0, s77
	s_nop 0
	buffer_load_dwordx4 v223, s[16:19], s55 offen lds
	s_waitcnt vmcnt(8)
	s_waitcnt lgkmcnt(0)
	s_barrier
	s_setprio 1
	v_mfma_f32_16x16x32_bf16 v[60:63], v[128:131], v[160:163], v[60:63]
	v_mfma_f32_16x16x32_bf16 v[56:59], v[136:139], v[160:163], v[56:59]
	v_mfma_f32_16x16x32_bf16 v[52:55], v[128:131], v[168:171], v[52:55]
	v_mfma_f32_16x16x32_bf16 v[48:51], v[136:139], v[168:171], v[48:51]
	v_mfma_f32_16x16x32_bf16 v[44:47], v[128:131], v[176:179], v[44:47]
	v_mfma_f32_16x16x32_bf16 v[40:43], v[136:139], v[176:179], v[40:43]
	v_mfma_f32_16x16x32_bf16 v[36:39], v[128:131], v[184:187], v[36:39]
	v_mfma_f32_16x16x32_bf16 v[32:35], v[136:139], v[184:187], v[32:35]
	v_mfma_f32_16x16x32_bf16 v[60:63], v[132:135], v[164:167], v[60:63]
	v_mfma_f32_16x16x32_bf16 v[56:59], v[140:143], v[164:167], v[56:59]
	v_mfma_f32_16x16x32_bf16 v[52:55], v[132:135], v[172:175], v[52:55]
	v_mfma_f32_16x16x32_bf16 v[48:51], v[140:143], v[172:175], v[48:51]
	v_mfma_f32_16x16x32_bf16 v[44:47], v[132:135], v[180:183], v[44:47]
	v_mfma_f32_16x16x32_bf16 v[40:43], v[140:143], v[180:183], v[40:43]
	v_mfma_f32_16x16x32_bf16 v[36:39], v[132:135], v[188:191], v[36:39]
	v_mfma_f32_16x16x32_bf16 v[32:35], v[140:143], v[188:191], v[32:35]
	s_setprio 0
	s_setprio 1
	v_mfma_f32_16x16x32_bf16 v[28:31], v[144:147], v[160:163], v[28:31]
	v_mfma_f32_16x16x32_bf16 v[24:27], v[152:155], v[160:163], v[24:27]
	v_mfma_f32_16x16x32_bf16 v[20:23], v[144:147], v[168:171], v[20:23]
	v_mfma_f32_16x16x32_bf16 v[16:19], v[152:155], v[168:171], v[16:19]
	v_mfma_f32_16x16x32_bf16 v[12:15], v[144:147], v[176:179], v[12:15]
	v_mfma_f32_16x16x32_bf16 v[8:11], v[152:155], v[176:179], v[8:11]
	v_mfma_f32_16x16x32_bf16 v[4:7], v[144:147], v[184:187], v[4:7]
	v_mfma_f32_16x16x32_bf16 v[0:3], v[152:155], v[184:187], v[0:3]
	v_mfma_f32_16x16x32_bf16 v[28:31], v[148:151], v[164:167], v[28:31]
	v_mfma_f32_16x16x32_bf16 v[24:27], v[156:159], v[164:167], v[24:27]
	v_mfma_f32_16x16x32_bf16 v[20:23], v[148:151], v[172:175], v[20:23]
	v_mfma_f32_16x16x32_bf16 v[16:19], v[156:159], v[172:175], v[16:19]
	v_mfma_f32_16x16x32_bf16 v[12:15], v[148:151], v[180:183], v[12:15]
	v_mfma_f32_16x16x32_bf16 v[8:11], v[156:159], v[180:183], v[8:11]
	v_mfma_f32_16x16x32_bf16 v[4:7], v[148:151], v[188:191], v[4:7]
	v_mfma_f32_16x16x32_bf16 v[0:3], v[156:159], v[188:191], v[0:3]
	s_setprio 0
	s_barrier
	s_add_i32 s85, s85, 2
	s_addk_i32 vcc_lo, 0x100
	s_addk_i32 vcc_hi, 0x100
	s_cmp_ge_i32 s85, s81
	s_cbranch_scc0 .LBB0_847
	v_readlane_b32 s68, v255, 22
	v_readlane_b32 s54, v255, 25
	v_readlane_b32 s69, v255, 23
	v_readlane_b32 s55, v255, 26

; #define PG8_STAGE(bufoff, rs_, soff_, voff) do { _Pragma("unroll") for (int _i = 0; _i < 2; ++_i) \
;         __builtin_amdgcn_raw_ptr_buffer_load_lds(rs_, (LAS void*)(lds + (bufoff) + ldsw + _i * 8192), 16, (int)(voff)[_i], (int)(soff_), 0, 0); } while (0)
; #define PG8_LDA(dst, b, h) do { _Pragma("unroll") for (int m = 0; m < 4; ++m) dst[m] = PG8_LD2(lds + PG8_SA(b, h) + aoff + m * 2048); } while (0)
; #define PG8_LDB(dst, b, h) do { _Pragma("unroll") for (int n = 0; n < 2; ++n) dst[n] = PG8_LD2(lds + PG8_SB(b, h) + boff + n * 2048); } while (0)
; #define PG8_BAR __builtin_amdgcn_s_barrier()
; template <class Epi, class Sched, bool ALIGN_EPI = false, bool SP2 = false, bool FP8 = false>
; __device__ __forceinline__ void gemm_phase(LAS unsigned char* lds, const Gemm g, const Sched& S, const Epi& E, int wbase) {
;     ...
;             const bool last = (t == nt - 2);
;             const unsigned a1 = cA + (unsigned)(t + 1) * kstep;
;             const unsigned a2 = last ? nA : cA + (unsigned)(t + 2) * kstep, b2 = last ? nB : cB + (unsigned)(t + 2) * kstep; const rsrc_t rA2 = (Sched::TWO && last) ? rAn : rAc, rB2 = (Sched::TWO && last) ? rBn : rBc;
;             const unsigned a3 = a2 + kstep, b3 = b2 + kstep;
;             if (last && has_next) S.a_ready(nxt);
;             if constexpr (SP2) {
;             PG8_LDB(B0, 0, 0); PG8_LDB(B1, 0, 1); PG8_SCHED; PG8_LDA(At, 0, 0); PG8_STAGE(PG8_SA(1, 1), rAc, a1 + hstep, voffA);
;             PG8_WAIT_V(8); PG8_WAIT_L(0); PG8_BAR; PG8_MMA(0, 0, At, B0); PG8_MMA(0, 1, At, B1); PG8_BAR; PG8_SCHED;
;             PG8_LDA(At, 0, 1); PG8_STAGE(PG8_SB(0, 0), rB2, b2, voffB); PG8_STAGE(PG8_SB(0, 1), rB2, b2 + hstep, voffB); PG8_STAGE(PG8_SA(0, 0), rA2, a2, voffA);
;             PG8_WAIT_V(8); PG8_WAIT_L(0); PG8_BAR; PG8_MMA(1, 0, At, B0); PG8_MMA(1, 1, At, B1); PG8_BAR; PG8_SCHED;
;             PG8_LDB(B0, 1, 0); PG8_LDB(B1, 1, 1); PG8_SCHED; PG8_LDA(At, 1, 0); PG8_STAGE(PG8_SA(0, 1), rA2, a2 + hstep, voffA);
;             PG8_WAIT_V(8); PG8_WAIT_L(0); PG8_BAR; PG8_MMA(0, 0, At, B0); PG8_MMA(0, 1, At, B1); PG8_BAR; PG8_SCHED;
;             PG8_LDA(At, 1, 1); PG8_STAGE(PG8_SB(1, 0), rB2, b3, voffB); PG8_STAGE(PG8_SB(1, 1), rB2, b3 + hstep, voffB); PG8_STAGE(PG8_SA(1, 0), rA2, a3, voffA);
;             PG8_WAIT_V(8); PG8_WAIT_L(0); PG8_BAR; PG8_MMA(1, 0, At, B0); PG8_MMA(1, 1, At, B1); PG8_BAR; PG8_SCHED;
.LBB0_926:
	v_add_u32_e32 v120, 0x10000, v160
	ds_read_b128 v[132:135], v120
	ds_read_b128 v[136:139], v120 offset:1024
	ds_read_b128 v[140:143], v120 offset:2048
	ds_read_b128 v[144:147], v120 offset:3072
	v_add_u32_e32 v120, 0x14000, v160
	ds_read_b128 v[162:165], v120
	ds_read_b128 v[166:169], v120 offset:1024
	ds_read_b128 v[170:173], v120 offset:2048
	ds_read_b128 v[174:177], v120 offset:3072
	s_add_i32 s14, s4, 0x80
	s_cmp_eq_u32 s60, s11
	s_cselect_b32 s66, s2, s14
	s_cselect_b32 s55, s3, s5
	s_or_b32 s54, s66, 0x80
	s_add_i32 s14, s30, s4
	s_mov_b32 m0, s61
	ds_read_b128 v[178:181], v161
	ds_read_b128 v[182:185], v161 offset:1024
	ds_read_b128 v[194:197], v161 offset:2048
	ds_read_b128 v[198:201], v161 offset:3072
	ds_read_b128 v[202:205], v161 offset:4096
	ds_read_b128 v[206:209], v161 offset:5120
	ds_read_b128 v[210:213], v161 offset:6144
	ds_read_b128 v[214:217], v161 offset:7168
	buffer_load_dwordx4 v222, s[36:39], s14 offen lds
	s_mov_b32 m0, s62
	s_nop 0
	buffer_load_dwordx4 v156, s[36:39], s14 offen lds
	s_waitcnt vmcnt(8)
	s_waitcnt lgkmcnt(0)
	s_barrier
	s_setprio 1
	v_mfma_f32_16x16x128_f8f6f4 v[124:127], v[140:147], v[178:185], v[124:127]
	v_mfma_f32_16x16x128_f8f6f4 v[108:111], v[132:139], v[194:201], v[108:111]
	v_mfma_f32_16x16x128_f8f6f4 v[104:107], v[140:147], v[194:201], v[104:107]
	v_mfma_f32_16x16x128_f8f6f4 v[120:123], v[132:139], v[178:185], v[128:131]
	v_mfma_f32_16x16x128_f8f6f4 v[148:151], v[132:139], v[202:209], v[92:95]
	v_mfma_f32_16x16x128_f8f6f4 v[186:189], v[140:147], v[202:209], v[88:91]
	v_mfma_f32_16x16x128_f8f6f4 v[218:221], v[132:139], v[210:217], v[76:79]
	v_mfma_f32_16x16x128_f8f6f4 v[226:229], v[140:147], v[210:217], v[72:75]
	s_setprio 0
	s_setprio 1
	v_mfma_f32_16x16x128_f8f6f4 v[116:119], v[162:169], v[178:185], v[116:119]
	v_mfma_f32_16x16x128_f8f6f4 v[112:115], v[170:177], v[178:185], v[112:115]
	v_mfma_f32_16x16x128_f8f6f4 v[100:103], v[162:169], v[194:201], v[100:103]
	v_mfma_f32_16x16x128_f8f6f4 v[96:99], v[170:177], v[194:201], v[96:99]
	v_mfma_f32_16x16x128_f8f6f4 v[178:181], v[162:169], v[202:209], v[84:87]
	v_mfma_f32_16x16x128_f8f6f4 v[182:185], v[170:177], v[202:209], v[80:83]
	v_mfma_f32_16x16x128_f8f6f4 v[194:197], v[162:169], v[210:217], v[68:71]
	v_mfma_f32_16x16x128_f8f6f4 v[198:201], v[170:177], v[210:217], v[64:67]
	s_setprio 0
	s_barrier
	s_mov_b32 m0, s33
	s_mov_b32 s14, s38
	s_mov_b32 s15, s39
	s_nop 1
	ds_read_b128 v[64:67], v161 offset:16384
	ds_read_b128 v[68:71], v161 offset:17408
	ds_read_b128 v[72:75], v161 offset:18432
	ds_read_b128 v[76:79], v161 offset:19456
	ds_read_b128 v[80:83], v161 offset:20480
	ds_read_b128 v[84:87], v161 offset:21504
	ds_read_b128 v[88:91], v161 offset:22528
	ds_read_b128 v[92:95], v161 offset:23552
	buffer_load_dwordx4 v223, s[12:15], s55 offen lds
	s_mov_b32 m0, s34
	s_add_i32 s67, s55, s30
	buffer_load_dwordx4 v157, s[12:15], s55 offen lds
	s_mov_b32 m0, s35
	s_nop 0
	buffer_load_dwordx4 v223, s[12:15], s67 offen lds
	s_mov_b32 m0, s41
	s_nop 0
	buffer_load_dwordx4 v157, s[12:15], s67 offen lds
	s_mov_b32 m0, s31
	s_nop 0
	buffer_load_dwordx4 v222, s[36:39], s66 offen lds
	s_mov_b32 m0, s42
	s_nop 0
	buffer_load_dwordx4 v156, s[36:39], s66 offen lds
	s_waitcnt vmcnt(8)
	s_waitcnt lgkmcnt(0)
	s_barrier
	s_setprio 1
	v_mfma_f32_16x16x128_f8f6f4 v[60:63], v[132:139], v[64:71], v[60:63]
	v_mfma_f32_16x16x128_f8f6f4 v[56:59], v[140:147], v[64:71], v[56:59]
	v_mfma_f32_16x16x128_f8f6f4 v[202:205], v[132:139], v[72:79], v[44:47]
	v_mfma_f32_16x16x128_f8f6f4 v[206:209], v[140:147], v[72:79], v[40:43]
	v_mfma_f32_16x16x128_f8f6f4 v[210:213], v[132:139], v[80:87], v[28:31]
	v_mfma_f32_16x16x128_f8f6f4 v[214:217], v[140:147], v[80:87], v[24:27]
	v_mfma_f32_16x16x128_f8f6f4 v[230:233], v[132:139], v[88:95], v[12:15]
	v_mfma_f32_16x16x128_f8f6f4 v[234:237], v[140:147], v[88:95], v[8:11]
	s_setprio 0
	s_setprio 1
	v_mfma_f32_16x16x128_f8f6f4 v[52:55], v[162:169], v[64:71], v[52:55]
	v_mfma_f32_16x16x128_f8f6f4 v[48:51], v[170:177], v[64:71], v[48:51]
	v_mfma_f32_16x16x128_f8f6f4 v[238:241], v[162:169], v[72:79], v[36:39]
	v_mfma_f32_16x16x128_f8f6f4 v[242:245], v[170:177], v[72:79], v[32:35]
	v_mfma_f32_16x16x128_f8f6f4 v[246:249], v[162:169], v[80:87], v[20:23]
	v_mfma_f32_16x16x128_f8f6f4 v[250:253], v[170:177], v[80:87], v[16:19]
	v_mfma_f32_16x16x128_f8f6f4 v[190:193], v[162:169], v[88:95], v[4:7]
	v_mfma_f32_16x16x128_f8f6f4 v[152:155], v[170:177], v[88:95], v[0:3]
	s_setprio 0
	s_barrier
; #define PG8_STAGE(bufoff, rs_, soff_, voff) do { _Pragma("unroll") for (int _i = 0; _i < 2; ++_i) \
;         __builtin_amdgcn_raw_ptr_buffer_load_lds(rs_, (LAS void*)(lds + (bufoff) + ldsw + _i * 8192), 16, (int)(voff)[_i], (int)(soff_), 0, 0); } while (0)
; #define PG8_LDA(dst, b, h) do { _Pragma("unroll") for (int m = 0; m < 4; ++m) dst[m] = PG8_LD2(lds + PG8_SA(b, h) + aoff + m * 2048); } while (0)
; #define PG8_LDB(dst, b, h) do { _Pragma("unroll") for (int n = 0; n < 2; ++n) dst[n] = PG8_LD2(lds + PG8_SB(b, h) + boff + n * 2048); } while (0)
; #define PG8_WAIT_V(n) asm volatile("s_waitcnt vmcnt(" #n ")" ::: "memory")
; #define PG8_WAIT_L(n) asm volatile("s_waitcnt lgkmcnt(" #n ")" ::: "memory")
; #define PG8_BAR __builtin_amdgcn_s_barrier()
; #define PG8_SCHED __builtin_amdgcn_sched_barrier(0)
; template <class Epi, class Sched, bool ALIGN_EPI = false, bool SP2 = false, bool FP8 = false>
; __device__ __forceinline__ void gemm_phase(LAS unsigned char* lds, const Gemm g, const Sched& S, const Epi& E, int wbase) {
;     ...
;         for (int t = 0; t < nt; t += 2) {
;             const bool last = (t == nt - 2);
;             const unsigned a1 = cA + (unsigned)(t + 1) * kstep;
;             const unsigned a2 = last ? nA : cA + (unsigned)(t + 2) * kstep, b2 = last ? nB : cB + (unsigned)(t + 2) * kstep; const rsrc_t rA2 = (Sched::TWO && last) ? rAn : rAc, rB2 = (Sched::TWO && last) ? rBn : rBc;
;             const unsigned a3 = a2 + kstep, b3 = b2 + kstep;
;             if (last && has_next) S.a_ready(nxt);
;     ...
;             PG8_LDB(B0, 1, 0); PG8_LDB(B1, 1, 1); PG8_SCHED; PG8_LDA(At, 1, 0); PG8_STAGE(PG8_SA(0, 1), rA2, a2 + hstep, voffA);
;             PG8_WAIT_V(8); PG8_WAIT_L(0); PG8_BAR; PG8_MMA(0, 0, At, B0); PG8_MMA(0, 1, At, B1); PG8_BAR; PG8_SCHED;
;             PG8_LDA(At, 1, 1); PG8_STAGE(PG8_SB(1, 0), rB2, b3, voffB); PG8_STAGE(PG8_SB(1, 1), rB2, b3 + hstep, voffB); PG8_STAGE(PG8_SA(1, 0), rA2, a3, voffA);
;             PG8_WAIT_V(8); PG8_WAIT_L(0); PG8_BAR; PG8_MMA(1, 0, At, B0); PG8_MMA(1, 1, At, B1); PG8_BAR; PG8_SCHED;
	v_add_u32_e32 v8, 0x18000, v160
	s_nop 3
	ds_read_b128 v[0:3], v8
	ds_read_b128 v[4:7], v8 offset:1024
	ds_read_b128 v[16:19], v8 offset:2048
	ds_read_b128 v[20:23], v8 offset:3072
	v_add_u32_e32 v8, 0x1c000, v160
	ds_read_b128 v[132:135], v8
	ds_read_b128 v[136:139], v8 offset:1024
	ds_read_b128 v[140:143], v8 offset:2048
	ds_read_b128 v[144:147], v8 offset:3072
	s_add_i32 s66, s66, s30
	s_mov_b32 m0, s43
	ds_read_b128 v[8:11], v161 offset:32768
	ds_read_b128 v[12:15], v161 offset:33792
	ds_read_b128 v[24:27], v161 offset:34816
	ds_read_b128 v[28:31], v161 offset:35840
	ds_read_b128 v[32:35], v161 offset:36864
	ds_read_b128 v[36:39], v161 offset:37888
	ds_read_b128 v[40:43], v161 offset:38912
	ds_read_b128 v[44:47], v161 offset:39936
	buffer_load_dwordx4 v222, s[36:39], s66 offen lds
	s_mov_b32 m0, s44
	s_nop 0
	buffer_load_dwordx4 v156, s[36:39], s66 offen lds
	s_waitcnt vmcnt(8)
	s_waitcnt lgkmcnt(0)
	s_barrier
	s_setprio 1
	v_mfma_f32_16x16x128_f8f6f4 v[128:131], v[0:7], v[8:15], v[120:123]
	v_mfma_f32_16x16x128_f8f6f4 v[124:127], v[16:23], v[8:15], v[124:127]
	v_mfma_f32_16x16x128_f8f6f4 v[108:111], v[0:7], v[24:31], v[108:111]
	v_mfma_f32_16x16x128_f8f6f4 v[104:107], v[16:23], v[24:31], v[104:107]
	v_mfma_f32_16x16x128_f8f6f4 v[92:95], v[0:7], v[32:39], v[148:151]
	v_mfma_f32_16x16x128_f8f6f4 v[88:91], v[16:23], v[32:39], v[186:189]
	v_mfma_f32_16x16x128_f8f6f4 v[76:79], v[0:7], v[40:47], v[218:221]
	v_mfma_f32_16x16x128_f8f6f4 v[72:75], v[16:23], v[40:47], v[226:229]
	s_setprio 0
	s_setprio 1
	v_mfma_f32_16x16x128_f8f6f4 v[116:119], v[132:139], v[8:15], v[116:119]
	v_mfma_f32_16x16x128_f8f6f4 v[112:115], v[140:147], v[8:15], v[112:115]
	v_mfma_f32_16x16x128_f8f6f4 v[100:103], v[132:139], v[24:31], v[100:103]
	v_mfma_f32_16x16x128_f8f6f4 v[96:99], v[140:147], v[24:31], v[96:99]
	v_mfma_f32_16x16x128_f8f6f4 v[84:87], v[132:139], v[32:39], v[178:181]
	v_mfma_f32_16x16x128_f8f6f4 v[80:83], v[140:147], v[32:39], v[182:185]
	v_mfma_f32_16x16x128_f8f6f4 v[68:71], v[132:139], v[40:47], v[194:197]
	v_mfma_f32_16x16x128_f8f6f4 v[64:67], v[140:147], v[40:47], v[198:201]
	s_setprio 0
	s_barrier
	s_mov_b32 m0, s45
	s_bitset1_b32 s55, 7
	ds_read_b128 v[32:35], v161 offset:49152
	ds_read_b128 v[36:39], v161 offset:50176
	ds_read_b128 v[162:165], v161 offset:51200
	ds_read_b128 v[166:169], v161 offset:52224
	ds_read_b128 v[170:173], v161 offset:53248
	ds_read_b128 v[174:177], v161 offset:54272
	ds_read_b128 v[178:181], v161 offset:55296
	ds_read_b128 v[182:185], v161 offset:56320
	buffer_load_dwordx4 v223, s[12:15], s55 offen lds
	s_mov_b32 m0, s46
	s_nop 0
	buffer_load_dwordx4 v157, s[12:15], s55 offen lds
	s_add_i32 s55, s55, s30
	s_mov_b32 m0, s52
	s_nop 0
	buffer_load_dwordx4 v223, s[12:15], s55 offen lds
	s_mov_b32 m0, s53
	s_nop 0
	buffer_load_dwordx4 v157, s[12:15], s55 offen lds
	s_mov_b32 m0, s47
	s_nop 0
	buffer_load_dwordx4 v222, s[36:39], s54 offen lds
	s_mov_b32 m0, s48
	s_nop 0
	buffer_load_dwordx4 v156, s[36:39], s54 offen lds
	s_waitcnt vmcnt(8)
	s_waitcnt lgkmcnt(0)
	s_barrier
	s_setprio 1
	v_mfma_f32_16x16x128_f8f6f4 v[60:63], v[0:7], v[32:39], v[60:63]
	v_mfma_f32_16x16x128_f8f6f4 v[56:59], v[16:23], v[32:39], v[56:59]
	v_mfma_f32_16x16x128_f8f6f4 v[44:47], v[0:7], v[162:169], v[202:205]
	v_mfma_f32_16x16x128_f8f6f4 v[40:43], v[16:23], v[162:169], v[206:209]
	v_mfma_f32_16x16x128_f8f6f4 v[28:31], v[0:7], v[170:177], v[210:213]
	v_mfma_f32_16x16x128_f8f6f4 v[24:27], v[16:23], v[170:177], v[214:217]
	v_mfma_f32_16x16x128_f8f6f4 v[12:15], v[0:7], v[178:185], v[230:233]
	v_mfma_f32_16x16x128_f8f6f4 v[8:11], v[16:23], v[178:185], v[234:237]
	s_setprio 0
	s_setprio 1
	v_mfma_f32_16x16x128_f8f6f4 v[52:55], v[132:139], v[32:39], v[52:55]
	v_mfma_f32_16x16x128_f8f6f4 v[48:51], v[140:147], v[32:39], v[48:51]
	v_mfma_f32_16x16x128_f8f6f4 v[36:39], v[132:139], v[162:169], v[238:241]
	v_mfma_f32_16x16x128_f8f6f4 v[32:35], v[140:147], v[162:169], v[242:245]
	v_mfma_f32_16x16x128_f8f6f4 v[20:23], v[132:139], v[170:177], v[246:249]
	v_mfma_f32_16x16x128_f8f6f4 v[16:19], v[140:147], v[170:177], v[250:253]
	v_mfma_f32_16x16x128_f8f6f4 v[4:7], v[132:139], v[178:185], v[190:193]
	v_mfma_f32_16x16x128_f8f6f4 v[0:3], v[140:147], v[178:185], v[152:155]
	s_setprio 0
	s_barrier
	s_add_i32 s11, s11, 2
	s_addk_i32 s4, 0x100
	s_addk_i32 s5, 0x100
	s_cmp_ge_i32 s11, s58
	s_cbranch_scc0 .LBB0_926
	v_mov_b32_e32 v230, 0x358637bd
	v_mov_b32_e32 v233, v159
	v_mov_b32_e32 v231, 1
	v_mov_b32_e32 v234, 0xff61b1e6
	s_and_b64 vcc, exec, s[24:25]
	s_cbranch_vccnz .LBB0_929
	s_branch .LBB0_930

; #define PG8_STAGE(bufoff, rs_, soff_, voff) do { _Pragma("unroll") for (int _i = 0; _i < 2; ++_i) \
;         __builtin_amdgcn_raw_ptr_buffer_load_lds(rs_, (LAS void*)(lds + (bufoff) + ldsw + _i * 8192), 16, (int)(voff)[_i], (int)(soff_), 0, 0); } while (0)
; #define PG8_LDA(dst, b, h) do { _Pragma("unroll") for (int m = 0; m < 4; ++m) dst[m] = PG8_LD2(lds + PG8_SA(b, h) + aoff + m * 2048); } while (0)
; #define PG8_LDB(dst, b, h) do { _Pragma("unroll") for (int n = 0; n < 2; ++n) dst[n] = PG8_LD2(lds + PG8_SB(b, h) + boff + n * 2048); } while (0)
; #define PG8_BAR __builtin_amdgcn_s_barrier()
; template <class Epi, class Sched, bool ALIGN_EPI = false, bool SP2 = false, bool FP8 = false>
; __device__ __forceinline__ void gemm_phase(LAS unsigned char* lds, const Gemm g, const Sched& S, const Epi& E, int wbase) {
;     ...
;             const bool last = (t == nt - 2);
;             const unsigned a1 = cA + (unsigned)(t + 1) * kstep;
;             const unsigned a2 = last ? nA : cA + (unsigned)(t + 2) * kstep, b2 = last ? nB : cB + (unsigned)(t + 2) * kstep; const rsrc_t rA2 = (Sched::TWO && last) ? rAn : rAc, rB2 = (Sched::TWO && last) ? rBn : rBc;
;             const unsigned a3 = a2 + kstep, b3 = b2 + kstep;
;             if (last && has_next) S.a_ready(nxt);
;             if constexpr (SP2) {
;             PG8_LDB(B0, 0, 0); PG8_LDB(B1, 0, 1); PG8_SCHED; PG8_LDA(At, 0, 0); PG8_STAGE(PG8_SA(1, 1), rAc, a1 + hstep, voffA);
;             PG8_WAIT_V(8); PG8_WAIT_L(0); PG8_BAR; PG8_MMA(0, 0, At, B0); PG8_MMA(0, 1, At, B1); PG8_BAR; PG8_SCHED;
;             PG8_LDA(At, 0, 1); PG8_STAGE(PG8_SB(0, 0), rB2, b2, voffB); PG8_STAGE(PG8_SB(0, 1), rB2, b2 + hstep, voffB); PG8_STAGE(PG8_SA(0, 0), rA2, a2, voffA);
;             PG8_WAIT_V(8); PG8_WAIT_L(0); PG8_BAR; PG8_MMA(1, 0, At, B0); PG8_MMA(1, 1, At, B1); PG8_BAR; PG8_SCHED;
;             PG8_LDB(B0, 1, 0); PG8_LDB(B1, 1, 1); PG8_SCHED; PG8_LDA(At, 1, 0); PG8_STAGE(PG8_SA(0, 1), rA2, a2 + hstep, voffA);
;             PG8_WAIT_V(8); PG8_WAIT_L(0); PG8_BAR; PG8_MMA(0, 0, At, B0); PG8_MMA(0, 1, At, B1); PG8_BAR; PG8_SCHED;
;             PG8_LDA(At, 1, 1); PG8_STAGE(PG8_SB(1, 0), rB2, b3, voffB); PG8_STAGE(PG8_SB(1, 1), rB2, b3 + hstep, voffB); PG8_STAGE(PG8_SA(1, 0), rA2, a3, voffA);
;             PG8_WAIT_V(8); PG8_WAIT_L(0); PG8_BAR; PG8_MMA(1, 0, At, B0); PG8_MMA(1, 1, At, B1); PG8_BAR; PG8_SCHED;
.LBB0_1004:
	v_add_u32_e32 v132, 0x10000, v180
	v_add_u32_e32 v156, 0x14000, v180
	ds_read_b128 v[96:99], v132
	ds_read_b128 v[108:111], v132 offset:1024
	ds_read_b128 v[120:123], v132 offset:2048
	ds_read_b128 v[132:135], v132 offset:3072
	ds_read_b128 v[136:139], v156
	ds_read_b128 v[144:147], v156 offset:1024
	ds_read_b128 v[152:155], v156 offset:2048
	ds_read_b128 v[156:159], v156 offset:3072
	s_add_i32 s14, s4, 0x80
	s_cmp_eq_u32 s62, s11
	s_cselect_b32 s66, s2, s14
	s_cselect_b32 s55, s3, s5
	s_or_b32 s54, s66, 0x80
	s_add_i32 s14, s33, s4
	s_mov_b32 m0, s63
	ds_read_b128 v[160:163], v181
	ds_read_b128 v[164:167], v181 offset:1024
	ds_read_b128 v[168:171], v181 offset:2048
	ds_read_b128 v[182:185], v181 offset:3072
	ds_read_b128 v[186:189], v181 offset:4096
	ds_read_b128 v[190:193], v181 offset:5120
	ds_read_b128 v[194:197], v181 offset:6144
	ds_read_b128 v[198:201], v181 offset:7168
	buffer_load_dwordx4 v174, s[36:39], s14 offen lds
	s_mov_b32 m0, s65
	s_nop 0
	buffer_load_dwordx4 v176, s[36:39], s14 offen lds
	s_waitcnt vmcnt(8)
	s_waitcnt lgkmcnt(0)
	s_barrier
	s_setprio 1
	v_mfma_f32_16x16x32_bf16 v[148:151], v[96:99], v[160:163], v[148:151]
	v_mfma_f32_16x16x32_bf16 v[140:143], v[120:123], v[160:163], v[140:143]
	v_mfma_f32_16x16x32_bf16 v[116:119], v[96:99], v[168:171], v[116:119]
	v_mfma_f32_16x16x32_bf16 v[112:115], v[120:123], v[168:171], v[112:115]
	v_mfma_f32_16x16x32_bf16 v[92:95], v[96:99], v[186:189], v[92:95]
	v_mfma_f32_16x16x32_bf16 v[88:91], v[120:123], v[186:189], v[88:91]
	v_mfma_f32_16x16x32_bf16 v[76:79], v[96:99], v[194:197], v[76:79]
	v_mfma_f32_16x16x32_bf16 v[72:75], v[120:123], v[194:197], v[72:75]
	v_mfma_f32_16x16x32_bf16 v[148:151], v[108:111], v[164:167], v[148:151]
	v_mfma_f32_16x16x32_bf16 v[140:143], v[132:135], v[164:167], v[140:143]
	v_mfma_f32_16x16x32_bf16 v[116:119], v[108:111], v[182:185], v[116:119]
	v_mfma_f32_16x16x32_bf16 v[112:115], v[132:135], v[182:185], v[112:115]
	v_mfma_f32_16x16x32_bf16 v[92:95], v[108:111], v[190:193], v[92:95]
	v_mfma_f32_16x16x32_bf16 v[88:91], v[132:135], v[190:193], v[88:91]
	v_mfma_f32_16x16x32_bf16 v[76:79], v[108:111], v[198:201], v[76:79]
	v_mfma_f32_16x16x32_bf16 v[72:75], v[132:135], v[198:201], v[72:75]
	s_setprio 0
	s_setprio 1
	v_mfma_f32_16x16x32_bf16 v[128:131], v[136:139], v[160:163], v[128:131]
	v_mfma_f32_16x16x32_bf16 v[124:127], v[152:155], v[160:163], v[124:127]
	v_mfma_f32_16x16x32_bf16 v[104:107], v[136:139], v[168:171], v[104:107]
	v_mfma_f32_16x16x32_bf16 v[100:103], v[152:155], v[168:171], v[100:103]
	v_mfma_f32_16x16x32_bf16 v[84:87], v[136:139], v[186:189], v[84:87]
	v_mfma_f32_16x16x32_bf16 v[80:83], v[152:155], v[186:189], v[80:83]
	v_mfma_f32_16x16x32_bf16 v[68:71], v[136:139], v[194:197], v[68:71]
	v_mfma_f32_16x16x32_bf16 v[64:67], v[152:155], v[194:197], v[64:67]
	v_mfma_f32_16x16x32_bf16 v[128:131], v[144:147], v[164:167], v[128:131]
	v_mfma_f32_16x16x32_bf16 v[124:127], v[156:159], v[164:167], v[124:127]
	v_mfma_f32_16x16x32_bf16 v[104:107], v[144:147], v[182:185], v[104:107]
	v_mfma_f32_16x16x32_bf16 v[100:103], v[156:159], v[182:185], v[100:103]
	v_mfma_f32_16x16x32_bf16 v[84:87], v[144:147], v[190:193], v[84:87]
	v_mfma_f32_16x16x32_bf16 v[80:83], v[156:159], v[190:193], v[80:83]
	v_mfma_f32_16x16x32_bf16 v[68:71], v[144:147], v[198:201], v[68:71]
	v_mfma_f32_16x16x32_bf16 v[64:67], v[156:159], v[198:201], v[64:67]
	s_setprio 0
	s_barrier
	s_mov_b32 m0, s35
	s_mov_b32 s14, s38
	s_mov_b32 s15, s39
	ds_read_b128 v[160:163], v181 offset:16384
	ds_read_b128 v[164:167], v181 offset:17408
	ds_read_b128 v[168:171], v181 offset:18432
	ds_read_b128 v[182:185], v181 offset:19456
	ds_read_b128 v[186:189], v181 offset:20480
	ds_read_b128 v[190:193], v181 offset:21504
	ds_read_b128 v[194:197], v181 offset:22528
	ds_read_b128 v[198:201], v181 offset:23552
	buffer_load_dwordx4 v175, s[12:15], s55 offen lds
	s_mov_b32 m0, s41
	s_add_i32 s67, s55, s33
	buffer_load_dwordx4 v177, s[12:15], s55 offen lds
	s_mov_b32 m0, s42
	s_nop 0
	buffer_load_dwordx4 v175, s[12:15], s67 offen lds
	s_mov_b32 m0, s43
	s_nop 0
	buffer_load_dwordx4 v177, s[12:15], s67 offen lds
	s_mov_b32 m0, s34
	s_nop 0
	buffer_load_dwordx4 v174, s[36:39], s66 offen lds
	s_mov_b32 m0, s44
	s_nop 0
	buffer_load_dwordx4 v176, s[36:39], s66 offen lds
	s_waitcnt vmcnt(8)
	s_waitcnt lgkmcnt(0)
	s_barrier
	s_setprio 1
	v_mfma_f32_16x16x32_bf16 v[60:63], v[96:99], v[160:163], v[60:63]
	v_mfma_f32_16x16x32_bf16 v[56:59], v[120:123], v[160:163], v[56:59]
	v_mfma_f32_16x16x32_bf16 v[44:47], v[96:99], v[168:171], v[44:47]
	v_mfma_f32_16x16x32_bf16 v[40:43], v[120:123], v[168:171], v[40:43]
	v_mfma_f32_16x16x32_bf16 v[28:31], v[96:99], v[186:189], v[28:31]
	v_mfma_f32_16x16x32_bf16 v[24:27], v[120:123], v[186:189], v[24:27]
	v_mfma_f32_16x16x32_bf16 v[12:15], v[96:99], v[194:197], v[12:15]
	v_mfma_f32_16x16x32_bf16 v[8:11], v[120:123], v[194:197], v[8:11]
	v_mfma_f32_16x16x32_bf16 v[60:63], v[108:111], v[164:167], v[60:63]
	v_mfma_f32_16x16x32_bf16 v[56:59], v[132:135], v[164:167], v[56:59]
	v_mfma_f32_16x16x32_bf16 v[44:47], v[108:111], v[182:185], v[44:47]
	v_mfma_f32_16x16x32_bf16 v[40:43], v[132:135], v[182:185], v[40:43]
	v_mfma_f32_16x16x32_bf16 v[28:31], v[108:111], v[190:193], v[28:31]
	v_mfma_f32_16x16x32_bf16 v[24:27], v[132:135], v[190:193], v[24:27]
	v_mfma_f32_16x16x32_bf16 v[12:15], v[108:111], v[198:201], v[12:15]
	v_mfma_f32_16x16x32_bf16 v[8:11], v[132:135], v[198:201], v[8:11]
	s_setprio 0
	s_setprio 1
	v_mfma_f32_16x16x32_bf16 v[52:55], v[136:139], v[160:163], v[52:55]
	v_mfma_f32_16x16x32_bf16 v[48:51], v[152:155], v[160:163], v[48:51]
	v_mfma_f32_16x16x32_bf16 v[36:39], v[136:139], v[168:171], v[36:39]
	v_mfma_f32_16x16x32_bf16 v[32:35], v[152:155], v[168:171], v[32:35]
	v_mfma_f32_16x16x32_bf16 v[20:23], v[136:139], v[186:189], v[20:23]
	v_mfma_f32_16x16x32_bf16 v[16:19], v[152:155], v[186:189], v[16:19]
	v_mfma_f32_16x16x32_bf16 v[4:7], v[136:139], v[194:197], v[4:7]
	v_mfma_f32_16x16x32_bf16 v[0:3], v[152:155], v[194:197], v[0:3]
	v_mfma_f32_16x16x32_bf16 v[52:55], v[144:147], v[164:167], v[52:55]
	v_mfma_f32_16x16x32_bf16 v[48:51], v[156:159], v[164:167], v[48:51]
	v_mfma_f32_16x16x32_bf16 v[36:39], v[144:147], v[182:185], v[36:39]
	v_mfma_f32_16x16x32_bf16 v[32:35], v[156:159], v[182:185], v[32:35]
	v_mfma_f32_16x16x32_bf16 v[20:23], v[144:147], v[190:193], v[20:23]
	v_mfma_f32_16x16x32_bf16 v[16:19], v[156:159], v[190:193], v[16:19]
	v_mfma_f32_16x16x32_bf16 v[4:7], v[144:147], v[198:201], v[4:7]
	v_mfma_f32_16x16x32_bf16 v[0:3], v[156:159], v[198:201], v[0:3]
	s_setprio 0
	s_barrier
; #define PG8_STAGE(bufoff, rs_, soff_, voff) do { _Pragma("unroll") for (int _i = 0; _i < 2; ++_i) \
;         __builtin_amdgcn_raw_ptr_buffer_load_lds(rs_, (LAS void*)(lds + (bufoff) + ldsw + _i * 8192), 16, (int)(voff)[_i], (int)(soff_), 0, 0); } while (0)
; #define PG8_LDA(dst, b, h) do { _Pragma("unroll") for (int m = 0; m < 4; ++m) dst[m] = PG8_LD2(lds + PG8_SA(b, h) + aoff + m * 2048); } while (0)
; #define PG8_LDB(dst, b, h) do { _Pragma("unroll") for (int n = 0; n < 2; ++n) dst[n] = PG8_LD2(lds + PG8_SB(b, h) + boff + n * 2048); } while (0)
; #define PG8_WAIT_V(n) asm volatile("s_waitcnt vmcnt(" #n ")" ::: "memory")
; #define PG8_WAIT_L(n) asm volatile("s_waitcnt lgkmcnt(" #n ")" ::: "memory")
; #define PG8_BAR __builtin_amdgcn_s_barrier()
; #define PG8_SCHED __builtin_amdgcn_sched_barrier(0)
; template <class Epi, class Sched, bool ALIGN_EPI = false, bool SP2 = false, bool FP8 = false>
; __device__ __forceinline__ void gemm_phase(LAS unsigned char* lds, const Gemm g, const Sched& S, const Epi& E, int wbase) {
;     ...
;         for (int t = 0; t < nt; t += 2) {
;             const bool last = (t == nt - 2);
;             const unsigned a1 = cA + (unsigned)(t + 1) * kstep;
;             const unsigned a2 = last ? nA : cA + (unsigned)(t + 2) * kstep, b2 = last ? nB : cB + (unsigned)(t + 2) * kstep; const rsrc_t rA2 = (Sched::TWO && last) ? rAn : rAc, rB2 = (Sched::TWO && last) ? rBn : rBc;
;             const unsigned a3 = a2 + kstep, b3 = b2 + kstep;
;             if (last && has_next) S.a_ready(nxt);
;     ...
;             PG8_LDB(B0, 1, 0); PG8_LDB(B1, 1, 1); PG8_SCHED; PG8_LDA(At, 1, 0); PG8_STAGE(PG8_SA(0, 1), rA2, a2 + hstep, voffA);
;             PG8_WAIT_V(8); PG8_WAIT_L(0); PG8_BAR; PG8_MMA(0, 0, At, B0); PG8_MMA(0, 1, At, B1); PG8_BAR; PG8_SCHED;
;             PG8_LDA(At, 1, 1); PG8_STAGE(PG8_SB(1, 0), rB2, b3, voffB); PG8_STAGE(PG8_SB(1, 1), rB2, b3 + hstep, voffB); PG8_STAGE(PG8_SA(1, 0), rA2, a3, voffA);
;             PG8_WAIT_V(8); PG8_WAIT_L(0); PG8_BAR; PG8_MMA(1, 0, At, B0); PG8_MMA(1, 1, At, B1); PG8_BAR; PG8_SCHED;
	v_add_u32_e32 v132, 0x18000, v180
	v_add_u32_e32 v156, 0x1c000, v180
	ds_read_b128 v[96:99], v132
	ds_read_b128 v[108:111], v132 offset:1024
	ds_read_b128 v[120:123], v132 offset:2048
	ds_read_b128 v[132:135], v132 offset:3072
	ds_read_b128 v[136:139], v156
	ds_read_b128 v[144:147], v156 offset:1024
	ds_read_b128 v[152:155], v156 offset:2048
	ds_read_b128 v[156:159], v156 offset:3072
	s_add_i32 s66, s66, s33
	s_mov_b32 m0, s45
	ds_read_b128 v[160:163], v181 offset:32768
	ds_read_b128 v[164:167], v181 offset:33792
	ds_read_b128 v[168:171], v181 offset:34816
	ds_read_b128 v[182:185], v181 offset:35840
	ds_read_b128 v[186:189], v181 offset:36864
	ds_read_b128 v[190:193], v181 offset:37888
	ds_read_b128 v[194:197], v181 offset:38912
	ds_read_b128 v[198:201], v181 offset:39936
	buffer_load_dwordx4 v174, s[36:39], s66 offen lds
	s_mov_b32 m0, s46
	s_nop 0
	buffer_load_dwordx4 v176, s[36:39], s66 offen lds
	s_waitcnt vmcnt(8)
	s_waitcnt lgkmcnt(0)
	s_barrier
	s_setprio 1
	v_mfma_f32_16x16x32_bf16 v[148:151], v[96:99], v[160:163], v[148:151]
	v_mfma_f32_16x16x32_bf16 v[140:143], v[120:123], v[160:163], v[140:143]
	v_mfma_f32_16x16x32_bf16 v[116:119], v[96:99], v[168:171], v[116:119]
	v_mfma_f32_16x16x32_bf16 v[112:115], v[120:123], v[168:171], v[112:115]
	v_mfma_f32_16x16x32_bf16 v[92:95], v[96:99], v[186:189], v[92:95]
	v_mfma_f32_16x16x32_bf16 v[88:91], v[120:123], v[186:189], v[88:91]
	v_mfma_f32_16x16x32_bf16 v[76:79], v[96:99], v[194:197], v[76:79]
	v_mfma_f32_16x16x32_bf16 v[72:75], v[120:123], v[194:197], v[72:75]
	v_mfma_f32_16x16x32_bf16 v[148:151], v[108:111], v[164:167], v[148:151]
	v_mfma_f32_16x16x32_bf16 v[140:143], v[132:135], v[164:167], v[140:143]
	v_mfma_f32_16x16x32_bf16 v[116:119], v[108:111], v[182:185], v[116:119]
	v_mfma_f32_16x16x32_bf16 v[112:115], v[132:135], v[182:185], v[112:115]
	v_mfma_f32_16x16x32_bf16 v[92:95], v[108:111], v[190:193], v[92:95]
	v_mfma_f32_16x16x32_bf16 v[88:91], v[132:135], v[190:193], v[88:91]
	v_mfma_f32_16x16x32_bf16 v[76:79], v[108:111], v[198:201], v[76:79]
	v_mfma_f32_16x16x32_bf16 v[72:75], v[132:135], v[198:201], v[72:75]
	s_setprio 0
	s_setprio 1
	v_mfma_f32_16x16x32_bf16 v[128:131], v[136:139], v[160:163], v[128:131]
	v_mfma_f32_16x16x32_bf16 v[124:127], v[152:155], v[160:163], v[124:127]
	v_mfma_f32_16x16x32_bf16 v[104:107], v[136:139], v[168:171], v[104:107]
	v_mfma_f32_16x16x32_bf16 v[100:103], v[152:155], v[168:171], v[100:103]
	v_mfma_f32_16x16x32_bf16 v[84:87], v[136:139], v[186:189], v[84:87]
	v_mfma_f32_16x16x32_bf16 v[80:83], v[152:155], v[186:189], v[80:83]
	v_mfma_f32_16x16x32_bf16 v[68:71], v[136:139], v[194:197], v[68:71]
	v_mfma_f32_16x16x32_bf16 v[64:67], v[152:155], v[194:197], v[64:67]
	v_mfma_f32_16x16x32_bf16 v[128:131], v[144:147], v[164:167], v[128:131]
	v_mfma_f32_16x16x32_bf16 v[124:127], v[156:159], v[164:167], v[124:127]
	v_mfma_f32_16x16x32_bf16 v[104:107], v[144:147], v[182:185], v[104:107]
	v_mfma_f32_16x16x32_bf16 v[100:103], v[156:159], v[182:185], v[100:103]
	v_mfma_f32_16x16x32_bf16 v[84:87], v[144:147], v[190:193], v[84:87]
	v_mfma_f32_16x16x32_bf16 v[80:83], v[156:159], v[190:193], v[80:83]
	v_mfma_f32_16x16x32_bf16 v[68:71], v[144:147], v[198:201], v[68:71]
	v_mfma_f32_16x16x32_bf16 v[64:67], v[156:159], v[198:201], v[64:67]
	s_setprio 0
	s_barrier
	s_mov_b32 m0, s47
	s_bitset1_b32 s55, 7
	ds_read_b128 v[160:163], v181 offset:49152
	ds_read_b128 v[164:167], v181 offset:50176
	ds_read_b128 v[168:171], v181 offset:51200
	ds_read_b128 v[182:185], v181 offset:52224
	ds_read_b128 v[186:189], v181 offset:53248
	ds_read_b128 v[190:193], v181 offset:54272
	ds_read_b128 v[194:197], v181 offset:55296
	ds_read_b128 v[198:201], v181 offset:56320
	buffer_load_dwordx4 v175, s[12:15], s55 offen lds
	s_mov_b32 m0, s48
	s_nop 0
	buffer_load_dwordx4 v177, s[12:15], s55 offen lds
	s_add_i32 s55, s55, s33
	s_mov_b32 m0, s56
	s_nop 0
	buffer_load_dwordx4 v175, s[12:15], s55 offen lds
	s_mov_b32 m0, s57
	s_nop 0
	buffer_load_dwordx4 v177, s[12:15], s55 offen lds
	s_mov_b32 m0, s52
	s_nop 0
	buffer_load_dwordx4 v174, s[36:39], s54 offen lds
	s_mov_b32 m0, s53
	s_nop 0
	buffer_load_dwordx4 v176, s[36:39], s54 offen lds
	s_waitcnt vmcnt(8)
	s_waitcnt lgkmcnt(0)
	s_barrier
	s_setprio 1
	v_mfma_f32_16x16x32_bf16 v[60:63], v[96:99], v[160:163], v[60:63]
	v_mfma_f32_16x16x32_bf16 v[56:59], v[120:123], v[160:163], v[56:59]
	v_mfma_f32_16x16x32_bf16 v[44:47], v[96:99], v[168:171], v[44:47]
	v_mfma_f32_16x16x32_bf16 v[40:43], v[120:123], v[168:171], v[40:43]
	v_mfma_f32_16x16x32_bf16 v[28:31], v[96:99], v[186:189], v[28:31]
	v_mfma_f32_16x16x32_bf16 v[24:27], v[120:123], v[186:189], v[24:27]
	v_mfma_f32_16x16x32_bf16 v[12:15], v[96:99], v[194:197], v[12:15]
	v_mfma_f32_16x16x32_bf16 v[8:11], v[120:123], v[194:197], v[8:11]
	v_mfma_f32_16x16x32_bf16 v[60:63], v[108:111], v[164:167], v[60:63]
	v_mfma_f32_16x16x32_bf16 v[56:59], v[132:135], v[164:167], v[56:59]
	v_mfma_f32_16x16x32_bf16 v[44:47], v[108:111], v[182:185], v[44:47]
	v_mfma_f32_16x16x32_bf16 v[40:43], v[132:135], v[182:185], v[40:43]
	v_mfma_f32_16x16x32_bf16 v[28:31], v[108:111], v[190:193], v[28:31]
	v_mfma_f32_16x16x32_bf16 v[24:27], v[132:135], v[190:193], v[24:27]
	v_mfma_f32_16x16x32_bf16 v[12:15], v[108:111], v[198:201], v[12:15]
	v_mfma_f32_16x16x32_bf16 v[8:11], v[132:135], v[198:201], v[8:11]
	s_setprio 0
	s_setprio 1
	v_mfma_f32_16x16x32_bf16 v[52:55], v[136:139], v[160:163], v[52:55]
	v_mfma_f32_16x16x32_bf16 v[48:51], v[152:155], v[160:163], v[48:51]
	v_mfma_f32_16x16x32_bf16 v[36:39], v[136:139], v[168:171], v[36:39]
	v_mfma_f32_16x16x32_bf16 v[32:35], v[152:155], v[168:171], v[32:35]
	v_mfma_f32_16x16x32_bf16 v[20:23], v[136:139], v[186:189], v[20:23]
	v_mfma_f32_16x16x32_bf16 v[16:19], v[152:155], v[186:189], v[16:19]
	v_mfma_f32_16x16x32_bf16 v[4:7], v[136:139], v[194:197], v[4:7]
	v_mfma_f32_16x16x32_bf16 v[0:3], v[152:155], v[194:197], v[0:3]
	v_mfma_f32_16x16x32_bf16 v[52:55], v[144:147], v[164:167], v[52:55]
	v_mfma_f32_16x16x32_bf16 v[48:51], v[156:159], v[164:167], v[48:51]
	v_mfma_f32_16x16x32_bf16 v[36:39], v[144:147], v[182:185], v[36:39]
	v_mfma_f32_16x16x32_bf16 v[32:35], v[156:159], v[182:185], v[32:35]
	v_mfma_f32_16x16x32_bf16 v[20:23], v[144:147], v[190:193], v[20:23]
	v_mfma_f32_16x16x32_bf16 v[16:19], v[156:159], v[190:193], v[16:19]
	v_mfma_f32_16x16x32_bf16 v[4:7], v[144:147], v[198:201], v[4:7]
	v_mfma_f32_16x16x32_bf16 v[0:3], v[156:159], v[198:201], v[0:3]
	s_setprio 0
	s_barrier
	s_add_i32 s11, s11, 2
	s_addk_i32 s4, 0x100
	s_addk_i32 s5, 0x100
	s_cmp_ge_i32 s11, s60
	s_cbranch_scc0 .LBB0_1004
	s_and_b64 vcc, exec, s[26:27]
	s_cbranch_vccz .LBB0_1007

; #define PG8_STAGE(bufoff, rs_, soff_, voff) do { _Pragma("unroll") for (int _i = 0; _i < 2; ++_i) \
;         __builtin_amdgcn_raw_ptr_buffer_load_lds(rs_, (LAS void*)(lds + (bufoff) + ldsw + _i * 8192), 16, (int)(voff)[_i], (int)(soff_), 0, 0); } while (0)
; #define PG8_LDA(dst, b, h) do { _Pragma("unroll") for (int m = 0; m < 4; ++m) dst[m] = PG8_LD2(lds + PG8_SA(b, h) + aoff + m * 2048); } while (0)
; #define PG8_LDB(dst, b, h) do { _Pragma("unroll") for (int n = 0; n < 2; ++n) dst[n] = PG8_LD2(lds + PG8_SB(b, h) + boff + n * 2048); } while (0)
; #define PG8_WAIT_V(n) asm volatile("s_waitcnt vmcnt(" #n ")" ::: "memory")
; #define PG8_WAIT_L(n) asm volatile("s_waitcnt lgkmcnt(" #n ")" ::: "memory")
; #define PG8_BAR __builtin_amdgcn_s_barrier()
; #define PG8_SCHED __builtin_amdgcn_sched_barrier(0)
; template <class Epi, class Sched, bool ALIGN_EPI = false, bool SP2 = false, bool FP8 = false>
; __device__ __forceinline__ void gemm_phase(LAS unsigned char* lds, const Gemm g, const Sched& S, const Epi& E, int wbase) {
;     ...
;             const bool last = (t == nt - 2);
;             const unsigned a1 = cA + (unsigned)(t + 1) * kstep;
;             const unsigned a2 = last ? nA : cA + (unsigned)(t + 2) * kstep, b2 = last ? nB : cB + (unsigned)(t + 2) * kstep; const rsrc_t rA2 = (Sched::TWO && last) ? rAn : rAc, rB2 = (Sched::TWO && last) ? rBn : rBc;
;             const unsigned a3 = a2 + kstep, b3 = b2 + kstep;
;             if (last && has_next) S.a_ready(nxt);
;             if constexpr (SP2) {
;             PG8_LDB(B0, 0, 0); PG8_LDB(B1, 0, 1); PG8_SCHED; PG8_LDA(At, 0, 0); PG8_STAGE(PG8_SA(1, 1), rAc, a1 + hstep, voffA);
;             PG8_WAIT_V(8); PG8_WAIT_L(0); PG8_BAR; PG8_MMA(0, 0, At, B0); PG8_MMA(0, 1, At, B1); PG8_BAR; PG8_SCHED;
.LBB0_1348:
	v_add_u32_e32 v12, 0x10000, v199
	v_add_u32_e32 v28, 0x14000, v199
	ds_read_b128 v[0:3], v12
	ds_read_b128 v[4:7], v12 offset:1024
	ds_read_b128 v[8:11], v12 offset:2048
	ds_read_b128 v[12:15], v12 offset:3072
	ds_read_b128 v[16:19], v28
	ds_read_b128 v[20:23], v28 offset:1024
	ds_read_b128 v[24:27], v28 offset:2048
	ds_read_b128 v[28:31], v28 offset:3072
	s_add_i32 s6, s67, 0x80
	s_cmp_eq_u32 s65, s85
	s_cselect_b32 s54, s66, s6
	s_cselect_b64 vcc, -1, 0
	v_cndmask_b32_e32 v211, v210, v201, vcc
	s_or_b32 s78, s54, 0x80
	s_add_i32 s6, s41, s67
	s_mov_b32 m0, s76
	ds_read_b128 v[32:35], v200
	ds_read_b128 v[36:39], v200 offset:1024
	ds_read_b128 v[40:43], v200 offset:2048
	ds_read_b128 v[44:47], v200 offset:3072
	ds_read_b128 v[48:51], v200 offset:4096
	ds_read_b128 v[52:55], v200 offset:5120
	ds_read_b128 v[56:59], v200 offset:6144
	ds_read_b128 v[60:63], v200 offset:7168
	buffer_load_dwordx4 v192, s[36:39], s6 offen lds
	s_mov_b32 m0, s77
	s_nop 0
	buffer_load_dwordx4 v195, s[36:39], s6 offen lds
	s_waitcnt vmcnt(8)
	s_waitcnt lgkmcnt(0)
	s_barrier
	s_setprio 1
	v_mfma_f32_16x16x128_f8f6f4 v[184:187], v[0:7], v[32:39], v[184:187]
	v_mfma_f32_16x16x128_f8f6f4 v[188:191], v[8:15], v[32:39], v[188:191]
	v_mfma_f32_16x16x128_f8f6f4 v[168:171], v[0:7], v[40:47], v[168:171]
	v_mfma_f32_16x16x128_f8f6f4 v[172:175], v[8:15], v[40:47], v[172:175]
	v_mfma_f32_16x16x128_f8f6f4 v[152:155], v[0:7], v[48:55], v[152:155]
	v_mfma_f32_16x16x128_f8f6f4 v[156:159], v[8:15], v[48:55], v[156:159]
	v_mfma_f32_16x16x128_f8f6f4 v[136:139], v[0:7], v[56:63], v[136:139]
	v_mfma_f32_16x16x128_f8f6f4 v[140:143], v[8:15], v[56:63], v[140:143]
	s_setprio 0
	s_setprio 1
	v_mfma_f32_16x16x128_f8f6f4 v[176:179], v[16:23], v[32:39], v[176:179]
	v_mfma_f32_16x16x128_f8f6f4 v[180:183], v[24:31], v[32:39], v[180:183]
	v_mfma_f32_16x16x128_f8f6f4 v[160:163], v[16:23], v[40:47], v[160:163]
	v_mfma_f32_16x16x128_f8f6f4 v[164:167], v[24:31], v[40:47], v[164:167]
	v_mfma_f32_16x16x128_f8f6f4 v[144:147], v[16:23], v[48:55], v[144:147]
	v_mfma_f32_16x16x128_f8f6f4 v[148:151], v[24:31], v[48:55], v[148:151]
	v_mfma_f32_16x16x128_f8f6f4 v[128:131], v[16:23], v[56:63], v[128:131]
	v_mfma_f32_16x16x128_f8f6f4 v[132:135], v[24:31], v[56:63], v[132:135]
	s_setprio 0
	s_barrier
	ds_read_b128 v[32:35], v200 offset:16384
	ds_read_b128 v[36:39], v200 offset:17408
	ds_read_b128 v[40:43], v200 offset:18432
	ds_read_b128 v[44:47], v200 offset:19456
	ds_read_b128 v[48:51], v200 offset:20480
	ds_read_b128 v[52:55], v200 offset:21504
	ds_read_b128 v[56:59], v200 offset:22528
	ds_read_b128 v[60:63], v200 offset:23552
	s_mov_b32 s6, s38
	s_mov_b32 s7, s39
	s_mov_b64 s[20:21], exec
	s_mov_b32 m0, s43

; #define PG8_STAGE(bufoff, rs_, soff_, voff) do { _Pragma("unroll") for (int _i = 0; _i < 2; ++_i) \
;         __builtin_amdgcn_raw_ptr_buffer_load_lds(rs_, (LAS void*)(lds + (bufoff) + ldsw + _i * 8192), 16, (int)(voff)[_i], (int)(soff_), 0, 0); } while (0)
; #define PG8_LDA(dst, b, h) do { _Pragma("unroll") for (int m = 0; m < 4; ++m) dst[m] = PG8_LD2(lds + PG8_SA(b, h) + aoff + m * 2048); } while (0)
; #define PG8_LDB(dst, b, h) do { _Pragma("unroll") for (int n = 0; n < 2; ++n) dst[n] = PG8_LD2(lds + PG8_SB(b, h) + boff + n * 2048); } while (0)
; #define PG8_WAIT_V(n) asm volatile("s_waitcnt vmcnt(" #n ")" ::: "memory")
; #define PG8_WAIT_L(n) asm volatile("s_waitcnt lgkmcnt(" #n ")" ::: "memory")
; #define PG8_BAR __builtin_amdgcn_s_barrier()
; #define PG8_SCHED __builtin_amdgcn_sched_barrier(0)
; template <class Epi, class Sched, bool ALIGN_EPI = false, bool SP2 = false, bool FP8 = false>
; __device__ __forceinline__ void gemm_phase(LAS unsigned char* lds, const Gemm g, const Sched& S, const Epi& E, int wbase) {
;     ...
;             PG8_LDA(At, 0, 1); PG8_STAGE(PG8_SB(0, 0), rB2, b2, voffB); PG8_STAGE(PG8_SB(0, 1), rB2, b2 + hstep, voffB); PG8_STAGE(PG8_SA(0, 0), rA2, a2, voffA);
;             PG8_WAIT_V(8); PG8_WAIT_L(0); PG8_BAR; PG8_MMA(1, 0, At, B0); PG8_MMA(1, 1, At, B1); PG8_BAR; PG8_SCHED;
;             PG8_LDB(B0, 1, 0); PG8_LDB(B1, 1, 1); PG8_SCHED; PG8_LDA(At, 1, 0); PG8_STAGE(PG8_SA(0, 1), rA2, a2 + hstep, voffA);
;             PG8_WAIT_V(8); PG8_WAIT_L(0); PG8_BAR; PG8_MMA(0, 0, At, B0); PG8_MMA(0, 1, At, B1); PG8_BAR; PG8_SCHED;
.LBB0_1355:
	v_readfirstlane_b32 s55, v212
	s_nop 1
	v_cmp_eq_u32_e32 vcc, s55, v212
	s_and_saveexec_b64 vcc, vcc
	s_nop 0
	buffer_load_dwordx4 v196, s[4:7], s55 offen lds
	s_xor_b64 exec, exec, vcc
	s_cbranch_execnz .LBB0_1355
	s_mov_b64 exec, s[20:21]
	s_mov_b32 m0, s42
	s_nop 0
	buffer_load_dwordx4 v192, s[36:39], s54 offen lds
	s_mov_b32 m0, s47
	s_nop 0
	buffer_load_dwordx4 v195, s[36:39], s54 offen lds
	s_waitcnt vmcnt(8)
	s_waitcnt lgkmcnt(0)
	s_barrier
	s_setprio 1
	v_mfma_f32_16x16x128_f8f6f4 v[120:123], v[0:7], v[32:39], v[120:123]
	v_mfma_f32_16x16x128_f8f6f4 v[124:127], v[8:15], v[32:39], v[124:127]
	v_mfma_f32_16x16x128_f8f6f4 v[104:107], v[0:7], v[40:47], v[104:107]
	v_mfma_f32_16x16x128_f8f6f4 v[108:111], v[8:15], v[40:47], v[108:111]
	v_mfma_f32_16x16x128_f8f6f4 v[88:91], v[0:7], v[48:55], v[88:91]
	v_mfma_f32_16x16x128_f8f6f4 v[92:95], v[8:15], v[48:55], v[92:95]
	v_mfma_f32_16x16x128_f8f6f4 v[72:75], v[0:7], v[56:63], v[72:75]
	v_mfma_f32_16x16x128_f8f6f4 v[76:79], v[8:15], v[56:63], v[76:79]
	s_setprio 0
	s_setprio 1
	v_mfma_f32_16x16x128_f8f6f4 v[112:115], v[16:23], v[32:39], v[112:115]
	v_mfma_f32_16x16x128_f8f6f4 v[116:119], v[24:31], v[32:39], v[116:119]
	v_mfma_f32_16x16x128_f8f6f4 v[96:99], v[16:23], v[40:47], v[96:99]
	v_mfma_f32_16x16x128_f8f6f4 v[100:103], v[24:31], v[40:47], v[100:103]
	v_mfma_f32_16x16x128_f8f6f4 v[80:83], v[16:23], v[48:55], v[80:83]
	v_mfma_f32_16x16x128_f8f6f4 v[84:87], v[24:31], v[48:55], v[84:87]
	v_mfma_f32_16x16x128_f8f6f4 v[68:71], v[16:23], v[56:63], v[68:71]
	v_mfma_f32_16x16x128_f8f6f4 v[64:67], v[24:31], v[56:63], v[64:67]
	s_setprio 0
	s_barrier
	v_add_u32_e32 v12, 0x18000, v199
	v_add_u32_e32 v28, 0x1c000, v199
	ds_read_b128 v[0:3], v12
	ds_read_b128 v[4:7], v12 offset:1024
	ds_read_b128 v[8:11], v12 offset:2048
	ds_read_b128 v[12:15], v12 offset:3072
	ds_read_b128 v[16:19], v28
	ds_read_b128 v[20:23], v28 offset:1024
	ds_read_b128 v[24:27], v28 offset:2048
	ds_read_b128 v[28:31], v28 offset:3072
	s_add_i32 s54, s54, s41
	s_mov_b32 m0, s48
	ds_read_b128 v[32:35], v200 offset:32768
	ds_read_b128 v[36:39], v200 offset:33792
	ds_read_b128 v[40:43], v200 offset:34816
	ds_read_b128 v[44:47], v200 offset:35840
	ds_read_b128 v[48:51], v200 offset:36864
	ds_read_b128 v[52:55], v200 offset:37888
	ds_read_b128 v[56:59], v200 offset:38912
	ds_read_b128 v[60:63], v200 offset:39936
	buffer_load_dwordx4 v192, s[36:39], s54 offen lds
	s_mov_b32 m0, s52
	s_nop 0
	buffer_load_dwordx4 v195, s[36:39], s54 offen lds
	s_waitcnt vmcnt(8)
	s_waitcnt lgkmcnt(0)
	s_barrier
	s_setprio 1
	v_mfma_f32_16x16x128_f8f6f4 v[184:187], v[0:7], v[32:39], v[184:187]
	v_mfma_f32_16x16x128_f8f6f4 v[188:191], v[8:15], v[32:39], v[188:191]
	v_mfma_f32_16x16x128_f8f6f4 v[168:171], v[0:7], v[40:47], v[168:171]
	v_mfma_f32_16x16x128_f8f6f4 v[172:175], v[8:15], v[40:47], v[172:175]
	v_mfma_f32_16x16x128_f8f6f4 v[152:155], v[0:7], v[48:55], v[152:155]
	v_mfma_f32_16x16x128_f8f6f4 v[156:159], v[8:15], v[48:55], v[156:159]
	v_mfma_f32_16x16x128_f8f6f4 v[136:139], v[0:7], v[56:63], v[136:139]
	v_mfma_f32_16x16x128_f8f6f4 v[140:143], v[8:15], v[56:63], v[140:143]
	s_setprio 0
	s_setprio 1
	v_mfma_f32_16x16x128_f8f6f4 v[176:179], v[16:23], v[32:39], v[176:179]
	v_mfma_f32_16x16x128_f8f6f4 v[180:183], v[24:31], v[32:39], v[180:183]
	v_mfma_f32_16x16x128_f8f6f4 v[160:163], v[16:23], v[40:47], v[160:163]
	v_mfma_f32_16x16x128_f8f6f4 v[164:167], v[24:31], v[40:47], v[164:167]
	v_mfma_f32_16x16x128_f8f6f4 v[144:147], v[16:23], v[48:55], v[144:147]
	v_mfma_f32_16x16x128_f8f6f4 v[148:151], v[24:31], v[48:55], v[148:151]
	v_mfma_f32_16x16x128_f8f6f4 v[128:131], v[16:23], v[56:63], v[128:131]
	v_mfma_f32_16x16x128_f8f6f4 v[132:135], v[24:31], v[56:63], v[132:135]
	s_setprio 0
	s_barrier
	ds_read_b128 v[32:35], v200 offset:49152
	ds_read_b128 v[36:39], v200 offset:50176
	ds_read_b128 v[40:43], v200 offset:51200
	ds_read_b128 v[44:47], v200 offset:52224
	ds_read_b128 v[48:51], v200 offset:53248
	ds_read_b128 v[52:55], v200 offset:54272
	ds_read_b128 v[56:59], v200 offset:55296
	ds_read_b128 v[60:63], v200 offset:56320
	v_add_u32_e32 v211, 0x80, v211
	s_mov_b64 s[20:21], exec
	s_mov_b32 m0, s57

; #define PG8_STAGE(bufoff, rs_, soff_, voff) do { _Pragma("unroll") for (int _i = 0; _i < 2; ++_i) \
;         __builtin_amdgcn_raw_ptr_buffer_load_lds(rs_, (LAS void*)(lds + (bufoff) + ldsw + _i * 8192), 16, (int)(voff)[_i], (int)(soff_), 0, 0); } while (0)
; #define PG8_LDA(dst, b, h) do { _Pragma("unroll") for (int m = 0; m < 4; ++m) dst[m] = PG8_LD2(lds + PG8_SA(b, h) + aoff + m * 2048); } while (0)
; #define PG8_WAIT_V(n) asm volatile("s_waitcnt vmcnt(" #n ")" ::: "memory")
; #define PG8_WAIT_L(n) asm volatile("s_waitcnt lgkmcnt(" #n ")" ::: "memory")
; #define PG8_BAR __builtin_amdgcn_s_barrier()
; #define PG8_SCHED __builtin_amdgcn_sched_barrier(0)
; template <class Epi, class Sched, bool ALIGN_EPI = false, bool SP2 = false, bool FP8 = false>
; __device__ __forceinline__ void gemm_phase(LAS unsigned char* lds, const Gemm g, const Sched& S, const Epi& E, int wbase) {
;     ...
;         for (int t = 0; t < nt; t += 2) {
;             const bool last = (t == nt - 2);
;             const unsigned a1 = cA + (unsigned)(t + 1) * kstep;
;             const unsigned a2 = last ? nA : cA + (unsigned)(t + 2) * kstep, b2 = last ? nB : cB + (unsigned)(t + 2) * kstep; const rsrc_t rA2 = (Sched::TWO && last) ? rAn : rAc, rB2 = (Sched::TWO && last) ? rBn : rBc;
;             const unsigned a3 = a2 + kstep, b3 = b2 + kstep;
;             if (last && has_next) S.a_ready(nxt);
;     ...
;             PG8_LDA(At, 1, 1); PG8_STAGE(PG8_SB(1, 0), rB2, b3, voffB); PG8_STAGE(PG8_SB(1, 1), rB2, b3 + hstep, voffB); PG8_STAGE(PG8_SA(1, 0), rA2, a3, voffA);
;             PG8_WAIT_V(8); PG8_WAIT_L(0); PG8_BAR; PG8_MMA(1, 0, At, B0); PG8_MMA(1, 1, At, B1); PG8_BAR; PG8_SCHED;
.LBB0_1363:
	v_readfirstlane_b32 s54, v211
	s_nop 1
	v_cmp_eq_u32_e32 vcc, s54, v211
	s_and_saveexec_b64 vcc, vcc
	s_nop 0
	buffer_load_dwordx4 v196, s[4:7], s54 offen lds
	s_xor_b64 exec, exec, vcc
	s_cbranch_execnz .LBB0_1363
	s_mov_b64 exec, s[20:21]
	s_mov_b32 m0, s59
	s_nop 0
	buffer_load_dwordx4 v192, s[36:39], s78 offen lds
	s_mov_b32 m0, s60
	s_nop 0
	buffer_load_dwordx4 v195, s[36:39], s78 offen lds
	s_waitcnt vmcnt(8)
	s_waitcnt lgkmcnt(0)
	s_barrier
	s_setprio 1
	v_mfma_f32_16x16x128_f8f6f4 v[120:123], v[0:7], v[32:39], v[120:123]
	v_mfma_f32_16x16x128_f8f6f4 v[124:127], v[8:15], v[32:39], v[124:127]
	v_mfma_f32_16x16x128_f8f6f4 v[104:107], v[0:7], v[40:47], v[104:107]
	v_mfma_f32_16x16x128_f8f6f4 v[108:111], v[8:15], v[40:47], v[108:111]
	v_mfma_f32_16x16x128_f8f6f4 v[88:91], v[0:7], v[48:55], v[88:91]
	v_mfma_f32_16x16x128_f8f6f4 v[92:95], v[8:15], v[48:55], v[92:95]
	v_mfma_f32_16x16x128_f8f6f4 v[72:75], v[0:7], v[56:63], v[72:75]
	v_mfma_f32_16x16x128_f8f6f4 v[76:79], v[8:15], v[56:63], v[76:79]
	s_setprio 0
	s_setprio 1
	v_mfma_f32_16x16x128_f8f6f4 v[112:115], v[16:23], v[32:39], v[112:115]
	v_mfma_f32_16x16x128_f8f6f4 v[116:119], v[24:31], v[32:39], v[116:119]
	v_mfma_f32_16x16x128_f8f6f4 v[96:99], v[16:23], v[40:47], v[96:99]
	v_mfma_f32_16x16x128_f8f6f4 v[100:103], v[24:31], v[40:47], v[100:103]
	v_mfma_f32_16x16x128_f8f6f4 v[80:83], v[16:23], v[48:55], v[80:83]
	v_mfma_f32_16x16x128_f8f6f4 v[84:87], v[24:31], v[48:55], v[84:87]
	v_mfma_f32_16x16x128_f8f6f4 v[68:71], v[16:23], v[56:63], v[68:71]
	v_mfma_f32_16x16x128_f8f6f4 v[64:67], v[24:31], v[56:63], v[64:67]
	s_setprio 0
	s_barrier
	s_add_i32 s85, s85, 2
	s_addk_i32 s67, 0x100
	s_cmp_ge_i32 s85, s53
	v_add_u32_e32 v210, 0x100, v210
	s_cbranch_scc0 .LBB0_1348
	v_readlane_b32 s54, v255, 25
	v_readlane_b32 s55, v255, 26
	s_and_b64 vcc, exec, s[18:19]
	s_cbranch_vccnz .LBB0_1367
	s_branch .LBB0_1368

; #define PG8_STAGE(bufoff, rs_, soff_, voff) do { _Pragma("unroll") for (int _i = 0; _i < 2; ++_i) \
;         __builtin_amdgcn_raw_ptr_buffer_load_lds(rs_, (LAS void*)(lds + (bufoff) + ldsw + _i * 8192), 16, (int)(voff)[_i], (int)(soff_), 0, 0); } while (0)
; #define PG8_LDA(dst, b, h) do { _Pragma("unroll") for (int m = 0; m < 4; ++m) dst[m] = PG8_LD2(lds + PG8_SA(b, h) + aoff + m * 2048); } while (0)
; #define PG8_LDB(dst, b, h) do { _Pragma("unroll") for (int n = 0; n < 2; ++n) dst[n] = PG8_LD2(lds + PG8_SB(b, h) + boff + n * 2048); } while (0)
; #define PG8_WAIT_V(n) asm volatile("s_waitcnt vmcnt(" #n ")" ::: "memory")
; #define PG8_WAIT_L(n) asm volatile("s_waitcnt lgkmcnt(" #n ")" ::: "memory")
; #define PG8_BAR __builtin_amdgcn_s_barrier()
; #define PG8_SCHED __builtin_amdgcn_sched_barrier(0)
; template <class Epi, class Sched, bool ALIGN_EPI = false, bool SP2 = false, bool FP8 = false>
; __device__ __forceinline__ void gemm_phase(LAS unsigned char* lds, const Gemm g, const Sched& S, const Epi& E, int wbase) {
;     ...
;             const bool last = (t == nt - 2);
;             const unsigned a1 = cA + (unsigned)(t + 1) * kstep;
;             const unsigned a2 = last ? nA : cA + (unsigned)(t + 2) * kstep, b2 = last ? nB : cB + (unsigned)(t + 2) * kstep; const rsrc_t rA2 = (Sched::TWO && last) ? rAn : rAc, rB2 = (Sched::TWO && last) ? rBn : rBc;
;             const unsigned a3 = a2 + kstep, b3 = b2 + kstep;
;             if (last && has_next) S.a_ready(nxt);
;             if constexpr (SP2) {
;             PG8_LDB(B0, 0, 0); PG8_LDB(B1, 0, 1); PG8_SCHED; PG8_LDA(At, 0, 0); PG8_STAGE(PG8_SA(1, 1), rAc, a1 + hstep, voffA);
;             PG8_WAIT_V(8); PG8_WAIT_L(0); PG8_BAR; PG8_MMA(0, 0, At, B0); PG8_MMA(0, 1, At, B1); PG8_BAR; PG8_SCHED;
.LBB0_1453:
	v_add_u32_e32 v12, 0x10000, v199
	v_add_u32_e32 v28, 0x14000, v199
	ds_read_b128 v[0:3], v12
	ds_read_b128 v[4:7], v12 offset:1024
	ds_read_b128 v[8:11], v12 offset:2048
	ds_read_b128 v[12:15], v12 offset:3072
	ds_read_b128 v[16:19], v28
	ds_read_b128 v[20:23], v28 offset:1024
	ds_read_b128 v[24:27], v28 offset:2048
	ds_read_b128 v[28:31], v28 offset:3072
	s_add_i32 s6, s67, 0x80
	s_cmp_eq_u32 s61, s81
	s_cselect_b32 s54, s66, s6
	s_cselect_b64 vcc, -1, 0
	v_cndmask_b32_e32 v203, v202, v201, vcc
	s_or_b32 s78, s54, 0x80
	s_add_i32 s6, s34, s67
	s_mov_b32 m0, s62
	ds_read_b128 v[32:35], v200
	ds_read_b128 v[36:39], v200 offset:1024
	ds_read_b128 v[40:43], v200 offset:2048
	ds_read_b128 v[44:47], v200 offset:3072
	ds_read_b128 v[48:51], v200 offset:4096
	ds_read_b128 v[52:55], v200 offset:5120
	ds_read_b128 v[56:59], v200 offset:6144
	ds_read_b128 v[60:63], v200 offset:7168
	buffer_load_dwordx4 v192, s[36:39], s6 offen lds
	s_mov_b32 m0, s63
	s_nop 0
	buffer_load_dwordx4 v195, s[36:39], s6 offen lds
	s_waitcnt vmcnt(8)
	s_waitcnt lgkmcnt(0)
	s_barrier
	s_setprio 1
	v_mfma_f32_16x16x128_f8f6f4 v[188:191], v[0:7], v[32:39], v[188:191]
	v_mfma_f32_16x16x128_f8f6f4 v[184:187], v[8:15], v[32:39], v[184:187]
	v_mfma_f32_16x16x128_f8f6f4 v[172:175], v[0:7], v[40:47], v[172:175]
	v_mfma_f32_16x16x128_f8f6f4 v[168:171], v[8:15], v[40:47], v[168:171]
	v_mfma_f32_16x16x128_f8f6f4 v[156:159], v[0:7], v[48:55], v[156:159]
	v_mfma_f32_16x16x128_f8f6f4 v[152:155], v[8:15], v[48:55], v[152:155]
	v_mfma_f32_16x16x128_f8f6f4 v[140:143], v[0:7], v[56:63], v[140:143]
	v_mfma_f32_16x16x128_f8f6f4 v[136:139], v[8:15], v[56:63], v[136:139]
	s_setprio 0
	s_setprio 1
	v_mfma_f32_16x16x128_f8f6f4 v[180:183], v[16:23], v[32:39], v[180:183]
	v_mfma_f32_16x16x128_f8f6f4 v[176:179], v[24:31], v[32:39], v[176:179]
	v_mfma_f32_16x16x128_f8f6f4 v[164:167], v[16:23], v[40:47], v[164:167]
	v_mfma_f32_16x16x128_f8f6f4 v[160:163], v[24:31], v[40:47], v[160:163]
	v_mfma_f32_16x16x128_f8f6f4 v[148:151], v[16:23], v[48:55], v[148:151]
	v_mfma_f32_16x16x128_f8f6f4 v[144:147], v[24:31], v[48:55], v[144:147]
	v_mfma_f32_16x16x128_f8f6f4 v[132:135], v[16:23], v[56:63], v[132:135]
	v_mfma_f32_16x16x128_f8f6f4 v[128:131], v[24:31], v[56:63], v[128:131]
	s_setprio 0
	s_barrier
	ds_read_b128 v[32:35], v200 offset:16384
	ds_read_b128 v[36:39], v200 offset:17408
	ds_read_b128 v[40:43], v200 offset:18432
	ds_read_b128 v[44:47], v200 offset:19456
	ds_read_b128 v[48:51], v200 offset:20480
	ds_read_b128 v[52:55], v200 offset:21504
	ds_read_b128 v[56:59], v200 offset:22528
	ds_read_b128 v[60:63], v200 offset:23552
	s_mov_b32 s6, s38
	s_mov_b32 s7, s39
	s_mov_b64 s[18:19], exec
	s_mov_b32 m0, s41

; #define PG8_STAGE(bufoff, rs_, soff_, voff) do { _Pragma("unroll") for (int _i = 0; _i < 2; ++_i) \
;         __builtin_amdgcn_raw_ptr_buffer_load_lds(rs_, (LAS void*)(lds + (bufoff) + ldsw + _i * 8192), 16, (int)(voff)[_i], (int)(soff_), 0, 0); } while (0)
; #define PG8_LDA(dst, b, h) do { _Pragma("unroll") for (int m = 0; m < 4; ++m) dst[m] = PG8_LD2(lds + PG8_SA(b, h) + aoff + m * 2048); } while (0)
; #define PG8_LDB(dst, b, h) do { _Pragma("unroll") for (int n = 0; n < 2; ++n) dst[n] = PG8_LD2(lds + PG8_SB(b, h) + boff + n * 2048); } while (0)
; #define PG8_WAIT_V(n) asm volatile("s_waitcnt vmcnt(" #n ")" ::: "memory")
; #define PG8_WAIT_L(n) asm volatile("s_waitcnt lgkmcnt(" #n ")" ::: "memory")
; #define PG8_BAR __builtin_amdgcn_s_barrier()
; #define PG8_SCHED __builtin_amdgcn_sched_barrier(0)
; template <class Epi, class Sched, bool ALIGN_EPI = false, bool SP2 = false, bool FP8 = false>
; __device__ __forceinline__ void gemm_phase(LAS unsigned char* lds, const Gemm g, const Sched& S, const Epi& E, int wbase) {
;     ...
;             PG8_LDA(At, 0, 1); PG8_STAGE(PG8_SB(0, 0), rB2, b2, voffB); PG8_STAGE(PG8_SB(0, 1), rB2, b2 + hstep, voffB); PG8_STAGE(PG8_SA(0, 0), rA2, a2, voffA);
;             PG8_WAIT_V(8); PG8_WAIT_L(0); PG8_BAR; PG8_MMA(1, 0, At, B0); PG8_MMA(1, 1, At, B1); PG8_BAR; PG8_SCHED;
;             PG8_LDB(B0, 1, 0); PG8_LDB(B1, 1, 1); PG8_SCHED; PG8_LDA(At, 1, 0); PG8_STAGE(PG8_SA(0, 1), rA2, a2 + hstep, voffA);
;             PG8_WAIT_V(8); PG8_WAIT_L(0); PG8_BAR; PG8_MMA(0, 0, At, B0); PG8_MMA(0, 1, At, B1); PG8_BAR; PG8_SCHED;
.LBB0_1460:
	v_readfirstlane_b32 s55, v204
	s_nop 1
	v_cmp_eq_u32_e32 vcc, s55, v204
	s_and_saveexec_b64 vcc, vcc
	s_nop 0
	buffer_load_dwordx4 v196, s[4:7], s55 offen lds
	s_xor_b64 exec, exec, vcc
	s_cbranch_execnz .LBB0_1460
	s_mov_b64 exec, s[18:19]
	s_mov_b32 m0, s35
	s_nop 0
	buffer_load_dwordx4 v192, s[36:39], s54 offen lds
	s_mov_b32 m0, s45
	s_nop 0
	buffer_load_dwordx4 v195, s[36:39], s54 offen lds
	s_waitcnt vmcnt(8)
	s_waitcnt lgkmcnt(0)
	s_barrier
	s_setprio 1
	v_mfma_f32_16x16x128_f8f6f4 v[124:127], v[0:7], v[32:39], v[124:127]
	v_mfma_f32_16x16x128_f8f6f4 v[120:123], v[8:15], v[32:39], v[120:123]
	v_mfma_f32_16x16x128_f8f6f4 v[108:111], v[0:7], v[40:47], v[108:111]
	v_mfma_f32_16x16x128_f8f6f4 v[104:107], v[8:15], v[40:47], v[104:107]
	v_mfma_f32_16x16x128_f8f6f4 v[92:95], v[0:7], v[48:55], v[92:95]
	v_mfma_f32_16x16x128_f8f6f4 v[88:91], v[8:15], v[48:55], v[88:91]
	v_mfma_f32_16x16x128_f8f6f4 v[76:79], v[0:7], v[56:63], v[76:79]
	v_mfma_f32_16x16x128_f8f6f4 v[72:75], v[8:15], v[56:63], v[72:75]
	s_setprio 0
	s_setprio 1
	v_mfma_f32_16x16x128_f8f6f4 v[116:119], v[16:23], v[32:39], v[116:119]
	v_mfma_f32_16x16x128_f8f6f4 v[112:115], v[24:31], v[32:39], v[112:115]
	v_mfma_f32_16x16x128_f8f6f4 v[100:103], v[16:23], v[40:47], v[100:103]
	v_mfma_f32_16x16x128_f8f6f4 v[96:99], v[24:31], v[40:47], v[96:99]
	v_mfma_f32_16x16x128_f8f6f4 v[84:87], v[16:23], v[48:55], v[84:87]
	v_mfma_f32_16x16x128_f8f6f4 v[80:83], v[24:31], v[48:55], v[80:83]
	v_mfma_f32_16x16x128_f8f6f4 v[68:71], v[16:23], v[56:63], v[68:71]
	v_mfma_f32_16x16x128_f8f6f4 v[64:67], v[24:31], v[56:63], v[64:67]
	s_setprio 0
	s_barrier
	v_add_u32_e32 v12, 0x18000, v199
	v_add_u32_e32 v28, 0x1c000, v199
	ds_read_b128 v[0:3], v12
	ds_read_b128 v[4:7], v12 offset:1024
	ds_read_b128 v[8:11], v12 offset:2048
	ds_read_b128 v[12:15], v12 offset:3072
	ds_read_b128 v[16:19], v28
	ds_read_b128 v[20:23], v28 offset:1024
	ds_read_b128 v[24:27], v28 offset:2048
	ds_read_b128 v[28:31], v28 offset:3072
	s_add_i32 s54, s54, s34
	s_mov_b32 m0, s46
	ds_read_b128 v[32:35], v200 offset:32768
	ds_read_b128 v[36:39], v200 offset:33792
	ds_read_b128 v[40:43], v200 offset:34816
	ds_read_b128 v[44:47], v200 offset:35840
	ds_read_b128 v[48:51], v200 offset:36864
	ds_read_b128 v[52:55], v200 offset:37888
	ds_read_b128 v[56:59], v200 offset:38912
	ds_read_b128 v[60:63], v200 offset:39936
	buffer_load_dwordx4 v192, s[36:39], s54 offen lds
	s_mov_b32 m0, s47
	s_nop 0
	buffer_load_dwordx4 v195, s[36:39], s54 offen lds
	s_waitcnt vmcnt(8)
	s_waitcnt lgkmcnt(0)
	s_barrier
	s_setprio 1
	v_mfma_f32_16x16x128_f8f6f4 v[188:191], v[0:7], v[32:39], v[188:191]
	v_mfma_f32_16x16x128_f8f6f4 v[184:187], v[8:15], v[32:39], v[184:187]
	v_mfma_f32_16x16x128_f8f6f4 v[172:175], v[0:7], v[40:47], v[172:175]
	v_mfma_f32_16x16x128_f8f6f4 v[168:171], v[8:15], v[40:47], v[168:171]
	v_mfma_f32_16x16x128_f8f6f4 v[156:159], v[0:7], v[48:55], v[156:159]
	v_mfma_f32_16x16x128_f8f6f4 v[152:155], v[8:15], v[48:55], v[152:155]
	v_mfma_f32_16x16x128_f8f6f4 v[140:143], v[0:7], v[56:63], v[140:143]
	v_mfma_f32_16x16x128_f8f6f4 v[136:139], v[8:15], v[56:63], v[136:139]
	s_setprio 0
	s_setprio 1
	v_mfma_f32_16x16x128_f8f6f4 v[180:183], v[16:23], v[32:39], v[180:183]
	v_mfma_f32_16x16x128_f8f6f4 v[176:179], v[24:31], v[32:39], v[176:179]
	v_mfma_f32_16x16x128_f8f6f4 v[164:167], v[16:23], v[40:47], v[164:167]
	v_mfma_f32_16x16x128_f8f6f4 v[160:163], v[24:31], v[40:47], v[160:163]
	v_mfma_f32_16x16x128_f8f6f4 v[148:151], v[16:23], v[48:55], v[148:151]
	v_mfma_f32_16x16x128_f8f6f4 v[144:147], v[24:31], v[48:55], v[144:147]
	v_mfma_f32_16x16x128_f8f6f4 v[132:135], v[16:23], v[56:63], v[132:135]
	v_mfma_f32_16x16x128_f8f6f4 v[128:131], v[24:31], v[56:63], v[128:131]
	s_setprio 0
	s_barrier
	ds_read_b128 v[32:35], v200 offset:49152
	ds_read_b128 v[36:39], v200 offset:50176
	ds_read_b128 v[40:43], v200 offset:51200
	ds_read_b128 v[44:47], v200 offset:52224
	ds_read_b128 v[48:51], v200 offset:53248
	ds_read_b128 v[52:55], v200 offset:54272
	ds_read_b128 v[56:59], v200 offset:55296
	ds_read_b128 v[60:63], v200 offset:56320
	v_add_u32_e32 v203, 0x80, v203
	s_mov_b64 s[18:19], exec
	s_mov_b32 m0, s53

; #define PG8_STAGE(bufoff, rs_, soff_, voff) do { _Pragma("unroll") for (int _i = 0; _i < 2; ++_i) \
;         __builtin_amdgcn_raw_ptr_buffer_load_lds(rs_, (LAS void*)(lds + (bufoff) + ldsw + _i * 8192), 16, (int)(voff)[_i], (int)(soff_), 0, 0); } while (0)
; #define PG8_LDA(dst, b, h) do { _Pragma("unroll") for (int m = 0; m < 4; ++m) dst[m] = PG8_LD2(lds + PG8_SA(b, h) + aoff + m * 2048); } while (0)
; #define PG8_WAIT_V(n) asm volatile("s_waitcnt vmcnt(" #n ")" ::: "memory")
; #define PG8_WAIT_L(n) asm volatile("s_waitcnt lgkmcnt(" #n ")" ::: "memory")
; #define PG8_BAR __builtin_amdgcn_s_barrier()
; #define PG8_SCHED __builtin_amdgcn_sched_barrier(0)
; template <class Epi, class Sched, bool ALIGN_EPI = false, bool SP2 = false, bool FP8 = false>
; __device__ __forceinline__ void gemm_phase(LAS unsigned char* lds, const Gemm g, const Sched& S, const Epi& E, int wbase) {
;     ...
;         for (int t = 0; t < nt; t += 2) {
;             const bool last = (t == nt - 2);
;             const unsigned a1 = cA + (unsigned)(t + 1) * kstep;
;             const unsigned a2 = last ? nA : cA + (unsigned)(t + 2) * kstep, b2 = last ? nB : cB + (unsigned)(t + 2) * kstep; const rsrc_t rA2 = (Sched::TWO && last) ? rAn : rAc, rB2 = (Sched::TWO && last) ? rBn : rBc;
;             const unsigned a3 = a2 + kstep, b3 = b2 + kstep;
;             if (last && has_next) S.a_ready(nxt);
;     ...
;             PG8_LDA(At, 1, 1); PG8_STAGE(PG8_SB(1, 0), rB2, b3, voffB); PG8_STAGE(PG8_SB(1, 1), rB2, b3 + hstep, voffB); PG8_STAGE(PG8_SA(1, 0), rA2, a3, voffA);
;             PG8_WAIT_V(8); PG8_WAIT_L(0); PG8_BAR; PG8_MMA(1, 0, At, B0); PG8_MMA(1, 1, At, B1); PG8_BAR; PG8_SCHED;
.LBB0_1468:
	v_readfirstlane_b32 s54, v203
	s_nop 1
	v_cmp_eq_u32_e32 vcc, s54, v203
	s_and_saveexec_b64 vcc, vcc
	s_nop 0
	buffer_load_dwordx4 v196, s[4:7], s54 offen lds
	s_xor_b64 exec, exec, vcc
	s_cbranch_execnz .LBB0_1468
	s_mov_b64 exec, s[18:19]
	s_mov_b32 m0, s57
	s_nop 0
	buffer_load_dwordx4 v192, s[36:39], s78 offen lds
	s_mov_b32 m0, s58
	s_nop 0
	buffer_load_dwordx4 v195, s[36:39], s78 offen lds
	s_waitcnt vmcnt(8)
	s_waitcnt lgkmcnt(0)
	s_barrier
	s_setprio 1
	v_mfma_f32_16x16x128_f8f6f4 v[124:127], v[0:7], v[32:39], v[124:127]
	v_mfma_f32_16x16x128_f8f6f4 v[120:123], v[8:15], v[32:39], v[120:123]
	v_mfma_f32_16x16x128_f8f6f4 v[108:111], v[0:7], v[40:47], v[108:111]
	v_mfma_f32_16x16x128_f8f6f4 v[104:107], v[8:15], v[40:47], v[104:107]
	v_mfma_f32_16x16x128_f8f6f4 v[92:95], v[0:7], v[48:55], v[92:95]
	v_mfma_f32_16x16x128_f8f6f4 v[88:91], v[8:15], v[48:55], v[88:91]
	v_mfma_f32_16x16x128_f8f6f4 v[76:79], v[0:7], v[56:63], v[76:79]
	v_mfma_f32_16x16x128_f8f6f4 v[72:75], v[8:15], v[56:63], v[72:75]
	s_setprio 0
	s_setprio 1
	v_mfma_f32_16x16x128_f8f6f4 v[116:119], v[16:23], v[32:39], v[116:119]
	v_mfma_f32_16x16x128_f8f6f4 v[112:115], v[24:31], v[32:39], v[112:115]
	v_mfma_f32_16x16x128_f8f6f4 v[100:103], v[16:23], v[40:47], v[100:103]
	v_mfma_f32_16x16x128_f8f6f4 v[96:99], v[24:31], v[40:47], v[96:99]
	v_mfma_f32_16x16x128_f8f6f4 v[84:87], v[16:23], v[48:55], v[84:87]
	v_mfma_f32_16x16x128_f8f6f4 v[80:83], v[24:31], v[48:55], v[80:83]
	v_mfma_f32_16x16x128_f8f6f4 v[68:71], v[16:23], v[56:63], v[68:71]
	v_mfma_f32_16x16x128_f8f6f4 v[64:67], v[24:31], v[56:63], v[64:67]
	s_setprio 0
	s_barrier
	s_add_i32 s81, s81, 2
	s_addk_i32 s67, 0x100
	s_cmp_ge_i32 s81, s48
	v_add_u32_e32 v202, 0x100, v202
	s_cbranch_scc0 .LBB0_1453
	v_readlane_b32 s54, v255, 25
	v_readlane_b32 s55, v255, 26
	s_and_b64 vcc, exec, s[14:15]
	s_cbranch_vccnz .LBB0_1472
	s_branch .LBB0_1473

; #define PG8_STAGE(bufoff, rs_, soff_, voff) do { _Pragma("unroll") for (int _i = 0; _i < 2; ++_i) \
;         __builtin_amdgcn_raw_ptr_buffer_load_lds(rs_, (LAS void*)(lds + (bufoff) + ldsw + _i * 8192), 16, (int)(voff)[_i], (int)(soff_), 0, 0); } while (0)
; #define PG8_LDA(dst, b, h) do { _Pragma("unroll") for (int m = 0; m < 4; ++m) dst[m] = PG8_LD2(lds + PG8_SA(b, h) + aoff + m * 2048); } while (0)
; #define PG8_LDB(dst, b, h) do { _Pragma("unroll") for (int n = 0; n < 2; ++n) dst[n] = PG8_LD2(lds + PG8_SB(b, h) + boff + n * 2048); } while (0)
; #define PG8_BAR __builtin_amdgcn_s_barrier()
; template <class Epi, class Sched, bool ALIGN_EPI = false, bool SP2 = false, bool FP8 = false>
; __device__ __forceinline__ void gemm_phase(LAS unsigned char* lds, const Gemm g, const Sched& S, const Epi& E, int wbase) {
;     ...
;             const bool last = (t == nt - 2);
;             const unsigned a1 = cA + (unsigned)(t + 1) * kstep;
;             const unsigned a2 = last ? nA : cA + (unsigned)(t + 2) * kstep, b2 = last ? nB : cB + (unsigned)(t + 2) * kstep; const rsrc_t rA2 = (Sched::TWO && last) ? rAn : rAc, rB2 = (Sched::TWO && last) ? rBn : rBc;
;             const unsigned a3 = a2 + kstep, b3 = b2 + kstep;
;             if (last && has_next) S.a_ready(nxt);
;             if constexpr (SP2) {
;             PG8_LDB(B0, 0, 0); PG8_LDB(B1, 0, 1); PG8_SCHED; PG8_LDA(At, 0, 0); PG8_STAGE(PG8_SA(1, 1), rAc, a1 + hstep, voffA);
;             PG8_WAIT_V(8); PG8_WAIT_L(0); PG8_BAR; PG8_MMA(0, 0, At, B0); PG8_MMA(0, 1, At, B1); PG8_BAR; PG8_SCHED;
;             PG8_LDA(At, 0, 1); PG8_STAGE(PG8_SB(0, 0), rB2, b2, voffB); PG8_STAGE(PG8_SB(0, 1), rB2, b2 + hstep, voffB); PG8_STAGE(PG8_SA(0, 0), rA2, a2, voffA);
;             PG8_WAIT_V(8); PG8_WAIT_L(0); PG8_BAR; PG8_MMA(1, 0, At, B0); PG8_MMA(1, 1, At, B1); PG8_BAR; PG8_SCHED;
;             PG8_LDB(B0, 1, 0); PG8_LDB(B1, 1, 1); PG8_SCHED; PG8_LDA(At, 1, 0); PG8_STAGE(PG8_SA(0, 1), rA2, a2 + hstep, voffA);
;             PG8_WAIT_V(8); PG8_WAIT_L(0); PG8_BAR; PG8_MMA(0, 0, At, B0); PG8_MMA(0, 1, At, B1); PG8_BAR; PG8_SCHED;
;             PG8_LDA(At, 1, 1); PG8_STAGE(PG8_SB(1, 0), rB2, b3, voffB); PG8_STAGE(PG8_SB(1, 1), rB2, b3 + hstep, voffB); PG8_STAGE(PG8_SA(1, 0), rA2, a3, voffA);
;             PG8_WAIT_V(8); PG8_WAIT_L(0); PG8_BAR; PG8_MMA(1, 0, At, B0); PG8_MMA(1, 1, At, B1); PG8_BAR; PG8_SCHED;
.LBB0_1628:
	v_add_u32_e32 v136, 0x10000, v161
	ds_read_b128 v[128:131], v136
	ds_read_b128 v[132:135], v136 offset:1024
	ds_read_b128 v[164:167], v136 offset:2048
	ds_read_b128 v[168:171], v136 offset:3072
	v_add_u32_e32 v136, 0x14000, v161
	ds_read_b128 v[172:175], v136
	ds_read_b128 v[176:179], v136 offset:1024
	ds_read_b128 v[180:183], v136 offset:2048
	ds_read_b128 v[184:187], v136 offset:3072
	s_add_i32 s6, s61, 0x80
	s_cmp_eq_u32 s46, s63
	s_cselect_b32 s65, s59, s6
	s_cselect_b32 s55, s60, s62
	s_or_b32 s54, s65, 0x80
	s_add_i32 s6, s22, s61
	s_mov_b32 m0, s47
	ds_read_b128 v[188:191], v162
	ds_read_b128 v[192:195], v162 offset:1024
	ds_read_b128 v[196:199], v162 offset:2048
	ds_read_b128 v[200:203], v162 offset:3072
	ds_read_b128 v[204:207], v162 offset:4096
	ds_read_b128 v[208:211], v162 offset:5120
	ds_read_b128 v[212:215], v162 offset:6144
	ds_read_b128 v[216:219], v162 offset:7168
	buffer_load_dwordx4 v137, s[36:39], s6 offen lds
	s_mov_b32 m0, s48
	s_nop 0
	buffer_load_dwordx4 v145, s[36:39], s6 offen lds
	s_waitcnt vmcnt(8)
	s_waitcnt lgkmcnt(0)
	s_barrier
	s_setprio 1
	v_mfma_f32_16x16x32_bf16 v[120:123], v[128:131], v[188:191], v[120:123]
	v_mfma_f32_16x16x32_bf16 v[124:127], v[164:167], v[188:191], v[124:127]
	v_mfma_f32_16x16x32_bf16 v[104:107], v[128:131], v[196:199], v[104:107]
	v_mfma_f32_16x16x32_bf16 v[108:111], v[164:167], v[196:199], v[108:111]
	v_mfma_f32_16x16x32_bf16 v[88:91], v[128:131], v[204:207], v[88:91]
	v_mfma_f32_16x16x32_bf16 v[92:95], v[164:167], v[204:207], v[92:95]
	v_mfma_f32_16x16x32_bf16 v[72:75], v[128:131], v[212:215], v[72:75]
	v_mfma_f32_16x16x32_bf16 v[76:79], v[164:167], v[212:215], v[76:79]
	v_mfma_f32_16x16x32_bf16 v[120:123], v[132:135], v[192:195], v[120:123]
	v_mfma_f32_16x16x32_bf16 v[124:127], v[168:171], v[192:195], v[124:127]
	v_mfma_f32_16x16x32_bf16 v[104:107], v[132:135], v[200:203], v[104:107]
	v_mfma_f32_16x16x32_bf16 v[108:111], v[168:171], v[200:203], v[108:111]
	v_mfma_f32_16x16x32_bf16 v[88:91], v[132:135], v[208:211], v[88:91]
	v_mfma_f32_16x16x32_bf16 v[92:95], v[168:171], v[208:211], v[92:95]
	v_mfma_f32_16x16x32_bf16 v[72:75], v[132:135], v[216:219], v[72:75]
	v_mfma_f32_16x16x32_bf16 v[76:79], v[168:171], v[216:219], v[76:79]
	s_setprio 0
	s_setprio 1
	v_mfma_f32_16x16x32_bf16 v[112:115], v[172:175], v[188:191], v[112:115]
	v_mfma_f32_16x16x32_bf16 v[116:119], v[180:183], v[188:191], v[116:119]
	v_mfma_f32_16x16x32_bf16 v[96:99], v[172:175], v[196:199], v[96:99]
	v_mfma_f32_16x16x32_bf16 v[100:103], v[180:183], v[196:199], v[100:103]
	v_mfma_f32_16x16x32_bf16 v[80:83], v[172:175], v[204:207], v[80:83]
	v_mfma_f32_16x16x32_bf16 v[84:87], v[180:183], v[204:207], v[84:87]
	v_mfma_f32_16x16x32_bf16 v[64:67], v[172:175], v[212:215], v[64:67]
	v_mfma_f32_16x16x32_bf16 v[68:71], v[180:183], v[212:215], v[68:71]
	v_mfma_f32_16x16x32_bf16 v[112:115], v[176:179], v[192:195], v[112:115]
	v_mfma_f32_16x16x32_bf16 v[116:119], v[184:187], v[192:195], v[116:119]
	v_mfma_f32_16x16x32_bf16 v[96:99], v[176:179], v[200:203], v[96:99]
	v_mfma_f32_16x16x32_bf16 v[100:103], v[184:187], v[200:203], v[100:103]
	v_mfma_f32_16x16x32_bf16 v[80:83], v[176:179], v[208:211], v[80:83]
	v_mfma_f32_16x16x32_bf16 v[84:87], v[184:187], v[208:211], v[84:87]
	v_mfma_f32_16x16x32_bf16 v[64:67], v[176:179], v[216:219], v[64:67]
	v_mfma_f32_16x16x32_bf16 v[68:71], v[184:187], v[216:219], v[68:71]
	s_setprio 0
	s_barrier
	s_mov_b32 m0, s24
	s_mov_b32 s6, s38
	s_mov_b32 s7, s39
	ds_read_b128 v[188:191], v162 offset:16384
	ds_read_b128 v[192:195], v162 offset:17408
	ds_read_b128 v[196:199], v162 offset:18432
	ds_read_b128 v[200:203], v162 offset:19456
	ds_read_b128 v[204:207], v162 offset:20480
	ds_read_b128 v[208:211], v162 offset:21504
	ds_read_b128 v[212:215], v162 offset:22528
	ds_read_b128 v[216:219], v162 offset:23552
	buffer_load_dwordx4 v141, s[4:7], s55 offen lds
	s_mov_b32 m0, s25
	s_add_i32 s66, s55, s22
	buffer_load_dwordx4 v149, s[4:7], s55 offen lds
	s_mov_b32 m0, s26
	s_nop 0
	buffer_load_dwordx4 v141, s[4:7], s66 offen lds
	s_mov_b32 m0, s27
	s_nop 0
	buffer_load_dwordx4 v149, s[4:7], s66 offen lds
	s_mov_b32 m0, s23
	s_nop 0
	buffer_load_dwordx4 v137, s[36:39], s65 offen lds
	s_mov_b32 m0, s28
	s_nop 0
	buffer_load_dwordx4 v145, s[36:39], s65 offen lds
	s_waitcnt vmcnt(8)
	s_waitcnt lgkmcnt(0)
	s_barrier
	s_setprio 1
	v_mfma_f32_16x16x32_bf16 v[56:59], v[128:131], v[188:191], v[56:59]
	v_mfma_f32_16x16x32_bf16 v[60:63], v[164:167], v[188:191], v[60:63]
	v_mfma_f32_16x16x32_bf16 v[40:43], v[128:131], v[196:199], v[40:43]
	v_mfma_f32_16x16x32_bf16 v[44:47], v[164:167], v[196:199], v[44:47]
	v_mfma_f32_16x16x32_bf16 v[24:27], v[128:131], v[204:207], v[24:27]
	v_mfma_f32_16x16x32_bf16 v[28:31], v[164:167], v[204:207], v[28:31]
	v_mfma_f32_16x16x32_bf16 v[8:11], v[128:131], v[212:215], v[8:11]
	v_mfma_f32_16x16x32_bf16 v[12:15], v[164:167], v[212:215], v[12:15]
	v_mfma_f32_16x16x32_bf16 v[56:59], v[132:135], v[192:195], v[56:59]
	v_mfma_f32_16x16x32_bf16 v[60:63], v[168:171], v[192:195], v[60:63]
	v_mfma_f32_16x16x32_bf16 v[40:43], v[132:135], v[200:203], v[40:43]
	v_mfma_f32_16x16x32_bf16 v[44:47], v[168:171], v[200:203], v[44:47]
	v_mfma_f32_16x16x32_bf16 v[24:27], v[132:135], v[208:211], v[24:27]
	v_mfma_f32_16x16x32_bf16 v[28:31], v[168:171], v[208:211], v[28:31]
	v_mfma_f32_16x16x32_bf16 v[8:11], v[132:135], v[216:219], v[8:11]
	v_mfma_f32_16x16x32_bf16 v[12:15], v[168:171], v[216:219], v[12:15]
	s_setprio 0
	s_setprio 1
	v_mfma_f32_16x16x32_bf16 v[48:51], v[172:175], v[188:191], v[48:51]
	v_mfma_f32_16x16x32_bf16 v[52:55], v[180:183], v[188:191], v[52:55]
	v_mfma_f32_16x16x32_bf16 v[32:35], v[172:175], v[196:199], v[32:35]
	v_mfma_f32_16x16x32_bf16 v[36:39], v[180:183], v[196:199], v[36:39]
	v_mfma_f32_16x16x32_bf16 v[16:19], v[172:175], v[204:207], v[16:19]
	v_mfma_f32_16x16x32_bf16 v[20:23], v[180:183], v[204:207], v[20:23]
	v_mfma_f32_16x16x32_bf16 v[4:7], v[172:175], v[212:215], v[4:7]
	v_mfma_f32_16x16x32_bf16 v[0:3], v[180:183], v[212:215], v[0:3]
	v_mfma_f32_16x16x32_bf16 v[48:51], v[176:179], v[192:195], v[48:51]
	v_mfma_f32_16x16x32_bf16 v[52:55], v[184:187], v[192:195], v[52:55]
	v_mfma_f32_16x16x32_bf16 v[32:35], v[176:179], v[200:203], v[32:35]
	v_mfma_f32_16x16x32_bf16 v[36:39], v[184:187], v[200:203], v[36:39]
	v_mfma_f32_16x16x32_bf16 v[16:19], v[176:179], v[208:211], v[16:19]
	v_mfma_f32_16x16x32_bf16 v[20:23], v[184:187], v[208:211], v[20:23]
	v_mfma_f32_16x16x32_bf16 v[4:7], v[176:179], v[216:219], v[4:7]
	v_mfma_f32_16x16x32_bf16 v[0:3], v[184:187], v[216:219], v[0:3]
	s_setprio 0
	s_barrier
; #define PG8_STAGE(bufoff, rs_, soff_, voff) do { _Pragma("unroll") for (int _i = 0; _i < 2; ++_i) \
;         __builtin_amdgcn_raw_ptr_buffer_load_lds(rs_, (LAS void*)(lds + (bufoff) + ldsw + _i * 8192), 16, (int)(voff)[_i], (int)(soff_), 0, 0); } while (0)
; #define PG8_LDA(dst, b, h) do { _Pragma("unroll") for (int m = 0; m < 4; ++m) dst[m] = PG8_LD2(lds + PG8_SA(b, h) + aoff + m * 2048); } while (0)
; #define PG8_LDB(dst, b, h) do { _Pragma("unroll") for (int n = 0; n < 2; ++n) dst[n] = PG8_LD2(lds + PG8_SB(b, h) + boff + n * 2048); } while (0)
; #define PG8_WAIT_V(n) asm volatile("s_waitcnt vmcnt(" #n ")" ::: "memory")
; #define PG8_WAIT_L(n) asm volatile("s_waitcnt lgkmcnt(" #n ")" ::: "memory")
; #define PG8_BAR __builtin_amdgcn_s_barrier()
; #define PG8_SCHED __builtin_amdgcn_sched_barrier(0)
; template <class Epi, class Sched, bool ALIGN_EPI = false, bool SP2 = false, bool FP8 = false>
; __device__ __forceinline__ void gemm_phase(LAS unsigned char* lds, const Gemm g, const Sched& S, const Epi& E, int wbase) {
;     ...
;         for (int t = 0; t < nt; t += 2) {
;             const bool last = (t == nt - 2);
;             const unsigned a1 = cA + (unsigned)(t + 1) * kstep;
;             const unsigned a2 = last ? nA : cA + (unsigned)(t + 2) * kstep, b2 = last ? nB : cB + (unsigned)(t + 2) * kstep; const rsrc_t rA2 = (Sched::TWO && last) ? rAn : rAc, rB2 = (Sched::TWO && last) ? rBn : rBc;
;             const unsigned a3 = a2 + kstep, b3 = b2 + kstep;
;             if (last && has_next) S.a_ready(nxt);
;     ...
;             PG8_LDB(B0, 1, 0); PG8_LDB(B1, 1, 1); PG8_SCHED; PG8_LDA(At, 1, 0); PG8_STAGE(PG8_SA(0, 1), rA2, a2 + hstep, voffA);
;             PG8_WAIT_V(8); PG8_WAIT_L(0); PG8_BAR; PG8_MMA(0, 0, At, B0); PG8_MMA(0, 1, At, B1); PG8_BAR; PG8_SCHED;
;             PG8_LDA(At, 1, 1); PG8_STAGE(PG8_SB(1, 0), rB2, b3, voffB); PG8_STAGE(PG8_SB(1, 1), rB2, b3 + hstep, voffB); PG8_STAGE(PG8_SA(1, 0), rA2, a3, voffA);
;             PG8_WAIT_V(8); PG8_WAIT_L(0); PG8_BAR; PG8_MMA(1, 0, At, B0); PG8_MMA(1, 1, At, B1); PG8_BAR; PG8_SCHED;
	v_add_u32_e32 v136, 0x18000, v161
	ds_read_b128 v[128:131], v136
	ds_read_b128 v[132:135], v136 offset:1024
	ds_read_b128 v[164:167], v136 offset:2048
	ds_read_b128 v[168:171], v136 offset:3072
	v_add_u32_e32 v136, 0x1c000, v161
	ds_read_b128 v[172:175], v136
	ds_read_b128 v[176:179], v136 offset:1024
	ds_read_b128 v[180:183], v136 offset:2048
	ds_read_b128 v[184:187], v136 offset:3072
	s_add_i32 s65, s65, s22
	s_mov_b32 m0, s29
	ds_read_b128 v[188:191], v162 offset:32768
	ds_read_b128 v[192:195], v162 offset:33792
	ds_read_b128 v[196:199], v162 offset:34816
	ds_read_b128 v[200:203], v162 offset:35840
	ds_read_b128 v[204:207], v162 offset:36864
	ds_read_b128 v[208:211], v162 offset:37888
	ds_read_b128 v[212:215], v162 offset:38912
	ds_read_b128 v[216:219], v162 offset:39936
	buffer_load_dwordx4 v137, s[36:39], s65 offen lds
	s_mov_b32 m0, s30
	s_nop 0
	buffer_load_dwordx4 v145, s[36:39], s65 offen lds
	s_waitcnt vmcnt(8)
	s_waitcnt lgkmcnt(0)
	s_barrier
	s_setprio 1
	v_mfma_f32_16x16x32_bf16 v[120:123], v[128:131], v[188:191], v[120:123]
	v_mfma_f32_16x16x32_bf16 v[124:127], v[164:167], v[188:191], v[124:127]
	v_mfma_f32_16x16x32_bf16 v[104:107], v[128:131], v[196:199], v[104:107]
	v_mfma_f32_16x16x32_bf16 v[108:111], v[164:167], v[196:199], v[108:111]
	v_mfma_f32_16x16x32_bf16 v[88:91], v[128:131], v[204:207], v[88:91]
	v_mfma_f32_16x16x32_bf16 v[92:95], v[164:167], v[204:207], v[92:95]
	v_mfma_f32_16x16x32_bf16 v[72:75], v[128:131], v[212:215], v[72:75]
	v_mfma_f32_16x16x32_bf16 v[76:79], v[164:167], v[212:215], v[76:79]
	v_mfma_f32_16x16x32_bf16 v[120:123], v[132:135], v[192:195], v[120:123]
	v_mfma_f32_16x16x32_bf16 v[124:127], v[168:171], v[192:195], v[124:127]
	v_mfma_f32_16x16x32_bf16 v[104:107], v[132:135], v[200:203], v[104:107]
	v_mfma_f32_16x16x32_bf16 v[108:111], v[168:171], v[200:203], v[108:111]
	v_mfma_f32_16x16x32_bf16 v[88:91], v[132:135], v[208:211], v[88:91]
	v_mfma_f32_16x16x32_bf16 v[92:95], v[168:171], v[208:211], v[92:95]
	v_mfma_f32_16x16x32_bf16 v[72:75], v[132:135], v[216:219], v[72:75]
	v_mfma_f32_16x16x32_bf16 v[76:79], v[168:171], v[216:219], v[76:79]
	s_setprio 0
	s_setprio 1
	v_mfma_f32_16x16x32_bf16 v[112:115], v[172:175], v[188:191], v[112:115]
	v_mfma_f32_16x16x32_bf16 v[116:119], v[180:183], v[188:191], v[116:119]
	v_mfma_f32_16x16x32_bf16 v[96:99], v[172:175], v[196:199], v[96:99]
	v_mfma_f32_16x16x32_bf16 v[100:103], v[180:183], v[196:199], v[100:103]
	v_mfma_f32_16x16x32_bf16 v[80:83], v[172:175], v[204:207], v[80:83]
	v_mfma_f32_16x16x32_bf16 v[84:87], v[180:183], v[204:207], v[84:87]
	v_mfma_f32_16x16x32_bf16 v[64:67], v[172:175], v[212:215], v[64:67]
	v_mfma_f32_16x16x32_bf16 v[68:71], v[180:183], v[212:215], v[68:71]
	v_mfma_f32_16x16x32_bf16 v[112:115], v[176:179], v[192:195], v[112:115]
	v_mfma_f32_16x16x32_bf16 v[116:119], v[184:187], v[192:195], v[116:119]
	v_mfma_f32_16x16x32_bf16 v[96:99], v[176:179], v[200:203], v[96:99]
	v_mfma_f32_16x16x32_bf16 v[100:103], v[184:187], v[200:203], v[100:103]
	v_mfma_f32_16x16x32_bf16 v[80:83], v[176:179], v[208:211], v[80:83]
	v_mfma_f32_16x16x32_bf16 v[84:87], v[184:187], v[208:211], v[84:87]
	v_mfma_f32_16x16x32_bf16 v[64:67], v[176:179], v[216:219], v[64:67]
	v_mfma_f32_16x16x32_bf16 v[68:71], v[184:187], v[216:219], v[68:71]
	s_setprio 0
	s_barrier
	s_mov_b32 m0, s31
	s_bitset1_b32 s55, 7
	ds_read_b128 v[188:191], v162 offset:49152
	ds_read_b128 v[192:195], v162 offset:50176
	ds_read_b128 v[196:199], v162 offset:51200
	ds_read_b128 v[200:203], v162 offset:52224
	ds_read_b128 v[204:207], v162 offset:53248
	ds_read_b128 v[208:211], v162 offset:54272
	ds_read_b128 v[212:215], v162 offset:55296
	ds_read_b128 v[216:219], v162 offset:56320
	buffer_load_dwordx4 v141, s[4:7], s55 offen lds
	s_mov_b32 m0, s33
	s_nop 0
	buffer_load_dwordx4 v149, s[4:7], s55 offen lds
	s_add_i32 s55, s55, s22
	s_mov_b32 m0, s41
	s_nop 0
	buffer_load_dwordx4 v141, s[4:7], s55 offen lds
	s_mov_b32 m0, s42
	s_nop 0
	buffer_load_dwordx4 v149, s[4:7], s55 offen lds
	s_mov_b32 m0, s34
	s_nop 0
	buffer_load_dwordx4 v137, s[36:39], s54 offen lds
	s_mov_b32 m0, s35
	s_nop 0
	buffer_load_dwordx4 v145, s[36:39], s54 offen lds
	s_waitcnt vmcnt(8)
	s_waitcnt lgkmcnt(0)
	s_barrier
	s_setprio 1
	v_mfma_f32_16x16x32_bf16 v[56:59], v[128:131], v[188:191], v[56:59]
	v_mfma_f32_16x16x32_bf16 v[60:63], v[164:167], v[188:191], v[60:63]
	v_mfma_f32_16x16x32_bf16 v[40:43], v[128:131], v[196:199], v[40:43]
	v_mfma_f32_16x16x32_bf16 v[44:47], v[164:167], v[196:199], v[44:47]
	v_mfma_f32_16x16x32_bf16 v[24:27], v[128:131], v[204:207], v[24:27]
	v_mfma_f32_16x16x32_bf16 v[28:31], v[164:167], v[204:207], v[28:31]
	v_mfma_f32_16x16x32_bf16 v[8:11], v[128:131], v[212:215], v[8:11]
	v_mfma_f32_16x16x32_bf16 v[12:15], v[164:167], v[212:215], v[12:15]
	v_mfma_f32_16x16x32_bf16 v[56:59], v[132:135], v[192:195], v[56:59]
	v_mfma_f32_16x16x32_bf16 v[60:63], v[168:171], v[192:195], v[60:63]
	v_mfma_f32_16x16x32_bf16 v[40:43], v[132:135], v[200:203], v[40:43]
	v_mfma_f32_16x16x32_bf16 v[44:47], v[168:171], v[200:203], v[44:47]
	v_mfma_f32_16x16x32_bf16 v[24:27], v[132:135], v[208:211], v[24:27]
	v_mfma_f32_16x16x32_bf16 v[28:31], v[168:171], v[208:211], v[28:31]
	v_mfma_f32_16x16x32_bf16 v[8:11], v[132:135], v[216:219], v[8:11]
	v_mfma_f32_16x16x32_bf16 v[12:15], v[168:171], v[216:219], v[12:15]
	s_setprio 0
	s_setprio 1
	v_mfma_f32_16x16x32_bf16 v[48:51], v[172:175], v[188:191], v[48:51]
	v_mfma_f32_16x16x32_bf16 v[52:55], v[180:183], v[188:191], v[52:55]
	v_mfma_f32_16x16x32_bf16 v[32:35], v[172:175], v[196:199], v[32:35]
	v_mfma_f32_16x16x32_bf16 v[36:39], v[180:183], v[196:199], v[36:39]
	v_mfma_f32_16x16x32_bf16 v[16:19], v[172:175], v[204:207], v[16:19]
	v_mfma_f32_16x16x32_bf16 v[20:23], v[180:183], v[204:207], v[20:23]
	v_mfma_f32_16x16x32_bf16 v[4:7], v[172:175], v[212:215], v[4:7]
	v_mfma_f32_16x16x32_bf16 v[0:3], v[180:183], v[212:215], v[0:3]
	v_mfma_f32_16x16x32_bf16 v[48:51], v[176:179], v[192:195], v[48:51]
	v_mfma_f32_16x16x32_bf16 v[52:55], v[184:187], v[192:195], v[52:55]
	v_mfma_f32_16x16x32_bf16 v[32:35], v[176:179], v[200:203], v[32:35]
	v_mfma_f32_16x16x32_bf16 v[36:39], v[184:187], v[200:203], v[36:39]
	v_mfma_f32_16x16x32_bf16 v[16:19], v[176:179], v[208:211], v[16:19]
	v_mfma_f32_16x16x32_bf16 v[20:23], v[184:187], v[208:211], v[20:23]
	v_mfma_f32_16x16x32_bf16 v[4:7], v[176:179], v[216:219], v[4:7]
	v_mfma_f32_16x16x32_bf16 v[0:3], v[184:187], v[216:219], v[0:3]
	s_setprio 0
	s_barrier
	s_add_i32 s63, s63, 2
	s_addk_i32 s61, 0x100
	s_addk_i32 s62, 0x100
	s_cmp_ge_i32 s63, s44
	s_cbranch_scc0 .LBB0_1628
	s_and_b64 vcc, exec, s[14:15]
	s_cbranch_vccz .LBB0_1631

; #define PG8_STAGE(bufoff, rs_, soff_, voff) do { _Pragma("unroll") for (int _i = 0; _i < 2; ++_i) \
;         __builtin_amdgcn_raw_ptr_buffer_load_lds(rs_, (LAS void*)(lds + (bufoff) + ldsw + _i * 8192), 16, (int)(voff)[_i], (int)(soff_), 0, 0); } while (0)
; #define PG8_LDA(dst, b, h) do { _Pragma("unroll") for (int m = 0; m < 4; ++m) dst[m] = PG8_LD2(lds + PG8_SA(b, h) + aoff + m * 2048); } while (0)
; #define PG8_LDB(dst, b, h) do { _Pragma("unroll") for (int n = 0; n < 2; ++n) dst[n] = PG8_LD2(lds + PG8_SB(b, h) + boff + n * 2048); } while (0)
; #define PG8_BAR __builtin_amdgcn_s_barrier()
; template <class Epi, class Sched, bool ALIGN_EPI = false, bool SP2 = false, bool FP8 = false>
; __device__ __forceinline__ void gemm_phase(LAS unsigned char* lds, const Gemm g, const Sched& S, const Epi& E, int wbase) {
;     ...
;             const bool last = (t == nt - 2);
;             const unsigned a1 = cA + (unsigned)(t + 1) * kstep;
;             const unsigned a2 = last ? nA : cA + (unsigned)(t + 2) * kstep, b2 = last ? nB : cB + (unsigned)(t + 2) * kstep; const rsrc_t rA2 = (Sched::TWO && last) ? rAn : rAc, rB2 = (Sched::TWO && last) ? rBn : rBc;
;             const unsigned a3 = a2 + kstep, b3 = b2 + kstep;
;             if (last && has_next) S.a_ready(nxt);
;             if constexpr (SP2) {
;             PG8_LDB(B0, 0, 0); PG8_LDB(B1, 0, 1); PG8_SCHED; PG8_LDA(At, 0, 0); PG8_STAGE(PG8_SA(1, 1), rAc, a1 + hstep, voffA);
;             PG8_WAIT_V(8); PG8_WAIT_L(0); PG8_BAR; PG8_MMA(0, 0, At, B0); PG8_MMA(0, 1, At, B1); PG8_BAR; PG8_SCHED;
;             PG8_LDA(At, 0, 1); PG8_STAGE(PG8_SB(0, 0), rB2, b2, voffB); PG8_STAGE(PG8_SB(0, 1), rB2, b2 + hstep, voffB); PG8_STAGE(PG8_SA(0, 0), rA2, a2, voffA);
;             PG8_WAIT_V(8); PG8_WAIT_L(0); PG8_BAR; PG8_MMA(1, 0, At, B0); PG8_MMA(1, 1, At, B1); PG8_BAR; PG8_SCHED;
;             PG8_LDB(B0, 1, 0); PG8_LDB(B1, 1, 1); PG8_SCHED; PG8_LDA(At, 1, 0); PG8_STAGE(PG8_SA(0, 1), rA2, a2 + hstep, voffA);
;             PG8_WAIT_V(8); PG8_WAIT_L(0); PG8_BAR; PG8_MMA(0, 0, At, B0); PG8_MMA(0, 1, At, B1); PG8_BAR; PG8_SCHED;
;             PG8_LDA(At, 1, 1); PG8_STAGE(PG8_SB(1, 0), rB2, b3, voffB); PG8_STAGE(PG8_SB(1, 1), rB2, b3 + hstep, voffB); PG8_STAGE(PG8_SA(1, 0), rA2, a3, voffA);
;             PG8_WAIT_V(8); PG8_WAIT_L(0); PG8_BAR; PG8_MMA(1, 0, At, B0); PG8_MMA(1, 1, At, B1); PG8_BAR; PG8_SCHED;
.LBB0_1701:
	v_add_u32_e32 v140, 0x10000, v176
	v_add_u32_e32 v156, 0x14000, v176
	ds_read_b128 v[112:115], v140
	ds_read_b128 v[124:127], v140 offset:1024
	ds_read_b128 v[136:139], v140 offset:2048
	ds_read_b128 v[140:143], v140 offset:3072
	ds_read_b128 v[144:147], v156
	ds_read_b128 v[148:151], v156 offset:1024
	ds_read_b128 v[152:155], v156 offset:2048
	ds_read_b128 v[156:159], v156 offset:3072
	s_add_i32 s6, s65, 0x80
	s_cmp_eq_u32 s52, s67
	s_cselect_b32 s68, s21, s6
	s_cselect_b32 s55, s63, s66
	s_or_b32 s54, s68, 0x80
	s_add_i32 s6, s25, s65
	s_mov_b32 m0, s53
	ds_read_b128 v[160:163], v177
	ds_read_b128 v[164:167], v177 offset:1024
	ds_read_b128 v[178:181], v177 offset:2048
	ds_read_b128 v[182:185], v177 offset:3072
	ds_read_b128 v[186:189], v177 offset:4096
	ds_read_b128 v[190:193], v177 offset:5120
	ds_read_b128 v[194:197], v177 offset:6144
	ds_read_b128 v[198:201], v177 offset:7168
	buffer_load_dwordx4 v170, s[36:39], s6 offen lds
	s_mov_b32 m0, s56
	s_nop 0
	buffer_load_dwordx4 v172, s[36:39], s6 offen lds
	s_waitcnt vmcnt(8)
	s_waitcnt lgkmcnt(0)
	s_barrier
	s_setprio 1
	v_mfma_f32_16x16x32_bf16 v[132:135], v[112:115], v[160:163], v[132:135]
	v_mfma_f32_16x16x32_bf16 v[128:131], v[136:139], v[160:163], v[128:131]
	v_mfma_f32_16x16x32_bf16 v[108:111], v[112:115], v[178:181], v[108:111]
	v_mfma_f32_16x16x32_bf16 v[104:107], v[136:139], v[178:181], v[104:107]
	v_mfma_f32_16x16x32_bf16 v[92:95], v[112:115], v[186:189], v[92:95]
	v_mfma_f32_16x16x32_bf16 v[88:91], v[136:139], v[186:189], v[88:91]
	v_mfma_f32_16x16x32_bf16 v[76:79], v[112:115], v[194:197], v[76:79]
	v_mfma_f32_16x16x32_bf16 v[72:75], v[136:139], v[194:197], v[72:75]
	v_mfma_f32_16x16x32_bf16 v[132:135], v[124:127], v[164:167], v[132:135]
	v_mfma_f32_16x16x32_bf16 v[128:131], v[140:143], v[164:167], v[128:131]
	v_mfma_f32_16x16x32_bf16 v[108:111], v[124:127], v[182:185], v[108:111]
	v_mfma_f32_16x16x32_bf16 v[104:107], v[140:143], v[182:185], v[104:107]
	v_mfma_f32_16x16x32_bf16 v[92:95], v[124:127], v[190:193], v[92:95]
	v_mfma_f32_16x16x32_bf16 v[88:91], v[140:143], v[190:193], v[88:91]
	v_mfma_f32_16x16x32_bf16 v[76:79], v[124:127], v[198:201], v[76:79]
	v_mfma_f32_16x16x32_bf16 v[72:75], v[140:143], v[198:201], v[72:75]
	s_setprio 0
	s_setprio 1
	v_mfma_f32_16x16x32_bf16 v[120:123], v[144:147], v[160:163], v[120:123]
	v_mfma_f32_16x16x32_bf16 v[116:119], v[152:155], v[160:163], v[116:119]
	v_mfma_f32_16x16x32_bf16 v[100:103], v[144:147], v[178:181], v[100:103]
	v_mfma_f32_16x16x32_bf16 v[96:99], v[152:155], v[178:181], v[96:99]
	v_mfma_f32_16x16x32_bf16 v[84:87], v[144:147], v[186:189], v[84:87]
	v_mfma_f32_16x16x32_bf16 v[80:83], v[152:155], v[186:189], v[80:83]
	v_mfma_f32_16x16x32_bf16 v[68:71], v[144:147], v[194:197], v[68:71]
	v_mfma_f32_16x16x32_bf16 v[64:67], v[152:155], v[194:197], v[64:67]
	v_mfma_f32_16x16x32_bf16 v[120:123], v[148:151], v[164:167], v[120:123]
	v_mfma_f32_16x16x32_bf16 v[116:119], v[156:159], v[164:167], v[116:119]
	v_mfma_f32_16x16x32_bf16 v[100:103], v[148:151], v[182:185], v[100:103]
	v_mfma_f32_16x16x32_bf16 v[96:99], v[156:159], v[182:185], v[96:99]
	v_mfma_f32_16x16x32_bf16 v[84:87], v[148:151], v[190:193], v[84:87]
	v_mfma_f32_16x16x32_bf16 v[80:83], v[156:159], v[190:193], v[80:83]
	v_mfma_f32_16x16x32_bf16 v[68:71], v[148:151], v[198:201], v[68:71]
	v_mfma_f32_16x16x32_bf16 v[64:67], v[156:159], v[198:201], v[64:67]
	s_setprio 0
	s_barrier
	s_mov_b32 m0, s27
	s_mov_b32 s6, s38
	s_mov_b32 s7, s39
	ds_read_b128 v[160:163], v177 offset:16384
	ds_read_b128 v[164:167], v177 offset:17408
	ds_read_b128 v[178:181], v177 offset:18432
	ds_read_b128 v[182:185], v177 offset:19456
	ds_read_b128 v[186:189], v177 offset:20480
	ds_read_b128 v[190:193], v177 offset:21504
	ds_read_b128 v[194:197], v177 offset:22528
	ds_read_b128 v[198:201], v177 offset:23552
	buffer_load_dwordx4 v171, s[4:7], s55 offen lds
	s_mov_b32 m0, s28
	s_add_i32 s69, s55, s25
	buffer_load_dwordx4 v173, s[4:7], s55 offen lds
	s_mov_b32 m0, s29
	s_nop 0
	buffer_load_dwordx4 v171, s[4:7], s69 offen lds
	s_mov_b32 m0, s30
	s_nop 0
	buffer_load_dwordx4 v173, s[4:7], s69 offen lds
	s_mov_b32 m0, s26
	s_nop 0
	buffer_load_dwordx4 v170, s[36:39], s68 offen lds
	s_mov_b32 m0, s31
	s_nop 0
	buffer_load_dwordx4 v172, s[36:39], s68 offen lds
	s_waitcnt vmcnt(8)
	s_waitcnt lgkmcnt(0)
	s_barrier
	s_setprio 1
	v_mfma_f32_16x16x32_bf16 v[60:63], v[112:115], v[160:163], v[60:63]
	v_mfma_f32_16x16x32_bf16 v[56:59], v[136:139], v[160:163], v[56:59]
	v_mfma_f32_16x16x32_bf16 v[44:47], v[112:115], v[178:181], v[44:47]
	v_mfma_f32_16x16x32_bf16 v[40:43], v[136:139], v[178:181], v[40:43]
	v_mfma_f32_16x16x32_bf16 v[28:31], v[112:115], v[186:189], v[28:31]
	v_mfma_f32_16x16x32_bf16 v[24:27], v[136:139], v[186:189], v[24:27]
	v_mfma_f32_16x16x32_bf16 v[12:15], v[112:115], v[194:197], v[12:15]
	v_mfma_f32_16x16x32_bf16 v[8:11], v[136:139], v[194:197], v[8:11]
	v_mfma_f32_16x16x32_bf16 v[60:63], v[124:127], v[164:167], v[60:63]
	v_mfma_f32_16x16x32_bf16 v[56:59], v[140:143], v[164:167], v[56:59]
	v_mfma_f32_16x16x32_bf16 v[44:47], v[124:127], v[182:185], v[44:47]
	v_mfma_f32_16x16x32_bf16 v[40:43], v[140:143], v[182:185], v[40:43]
	v_mfma_f32_16x16x32_bf16 v[28:31], v[124:127], v[190:193], v[28:31]
	v_mfma_f32_16x16x32_bf16 v[24:27], v[140:143], v[190:193], v[24:27]
	v_mfma_f32_16x16x32_bf16 v[12:15], v[124:127], v[198:201], v[12:15]
	v_mfma_f32_16x16x32_bf16 v[8:11], v[140:143], v[198:201], v[8:11]
	s_setprio 0
	s_setprio 1
	v_mfma_f32_16x16x32_bf16 v[52:55], v[144:147], v[160:163], v[52:55]
	v_mfma_f32_16x16x32_bf16 v[48:51], v[152:155], v[160:163], v[48:51]
	v_mfma_f32_16x16x32_bf16 v[36:39], v[144:147], v[178:181], v[36:39]
	v_mfma_f32_16x16x32_bf16 v[32:35], v[152:155], v[178:181], v[32:35]
	v_mfma_f32_16x16x32_bf16 v[20:23], v[144:147], v[186:189], v[20:23]
	v_mfma_f32_16x16x32_bf16 v[16:19], v[152:155], v[186:189], v[16:19]
	v_mfma_f32_16x16x32_bf16 v[4:7], v[144:147], v[194:197], v[4:7]
	v_mfma_f32_16x16x32_bf16 v[0:3], v[152:155], v[194:197], v[0:3]
	v_mfma_f32_16x16x32_bf16 v[52:55], v[148:151], v[164:167], v[52:55]
	v_mfma_f32_16x16x32_bf16 v[48:51], v[156:159], v[164:167], v[48:51]
	v_mfma_f32_16x16x32_bf16 v[36:39], v[148:151], v[182:185], v[36:39]
	v_mfma_f32_16x16x32_bf16 v[32:35], v[156:159], v[182:185], v[32:35]
	v_mfma_f32_16x16x32_bf16 v[20:23], v[148:151], v[190:193], v[20:23]
	v_mfma_f32_16x16x32_bf16 v[16:19], v[156:159], v[190:193], v[16:19]
	v_mfma_f32_16x16x32_bf16 v[4:7], v[148:151], v[198:201], v[4:7]
	v_mfma_f32_16x16x32_bf16 v[0:3], v[156:159], v[198:201], v[0:3]
	s_setprio 0
	s_barrier
; #define PG8_STAGE(bufoff, rs_, soff_, voff) do { _Pragma("unroll") for (int _i = 0; _i < 2; ++_i) \
;         __builtin_amdgcn_raw_ptr_buffer_load_lds(rs_, (LAS void*)(lds + (bufoff) + ldsw + _i * 8192), 16, (int)(voff)[_i], (int)(soff_), 0, 0); } while (0)
; #define PG8_LDA(dst, b, h) do { _Pragma("unroll") for (int m = 0; m < 4; ++m) dst[m] = PG8_LD2(lds + PG8_SA(b, h) + aoff + m * 2048); } while (0)
; #define PG8_LDB(dst, b, h) do { _Pragma("unroll") for (int n = 0; n < 2; ++n) dst[n] = PG8_LD2(lds + PG8_SB(b, h) + boff + n * 2048); } while (0)
; #define PG8_WAIT_V(n) asm volatile("s_waitcnt vmcnt(" #n ")" ::: "memory")
; #define PG8_WAIT_L(n) asm volatile("s_waitcnt lgkmcnt(" #n ")" ::: "memory")
; #define PG8_BAR __builtin_amdgcn_s_barrier()
; #define PG8_SCHED __builtin_amdgcn_sched_barrier(0)
; template <class Epi, class Sched, bool ALIGN_EPI = false, bool SP2 = false, bool FP8 = false>
; __device__ __forceinline__ void gemm_phase(LAS unsigned char* lds, const Gemm g, const Sched& S, const Epi& E, int wbase) {
;     ...
;         for (int t = 0; t < nt; t += 2) {
;             const bool last = (t == nt - 2);
;             const unsigned a1 = cA + (unsigned)(t + 1) * kstep;
;             const unsigned a2 = last ? nA : cA + (unsigned)(t + 2) * kstep, b2 = last ? nB : cB + (unsigned)(t + 2) * kstep; const rsrc_t rA2 = (Sched::TWO && last) ? rAn : rAc, rB2 = (Sched::TWO && last) ? rBn : rBc;
;             const unsigned a3 = a2 + kstep, b3 = b2 + kstep;
;             if (last && has_next) S.a_ready(nxt);
;     ...
;             PG8_LDB(B0, 1, 0); PG8_LDB(B1, 1, 1); PG8_SCHED; PG8_LDA(At, 1, 0); PG8_STAGE(PG8_SA(0, 1), rA2, a2 + hstep, voffA);
;             PG8_WAIT_V(8); PG8_WAIT_L(0); PG8_BAR; PG8_MMA(0, 0, At, B0); PG8_MMA(0, 1, At, B1); PG8_BAR; PG8_SCHED;
;             PG8_LDA(At, 1, 1); PG8_STAGE(PG8_SB(1, 0), rB2, b3, voffB); PG8_STAGE(PG8_SB(1, 1), rB2, b3 + hstep, voffB); PG8_STAGE(PG8_SA(1, 0), rA2, a3, voffA);
;             PG8_WAIT_V(8); PG8_WAIT_L(0); PG8_BAR; PG8_MMA(1, 0, At, B0); PG8_MMA(1, 1, At, B1); PG8_BAR; PG8_SCHED;
	v_add_u32_e32 v140, 0x18000, v176
	v_add_u32_e32 v156, 0x1c000, v176
	ds_read_b128 v[112:115], v140
	ds_read_b128 v[124:127], v140 offset:1024
	ds_read_b128 v[136:139], v140 offset:2048
	ds_read_b128 v[140:143], v140 offset:3072
	ds_read_b128 v[144:147], v156
	ds_read_b128 v[148:151], v156 offset:1024
	ds_read_b128 v[152:155], v156 offset:2048
	ds_read_b128 v[156:159], v156 offset:3072
	s_add_i32 s68, s68, s25
	s_mov_b32 m0, s33
	ds_read_b128 v[160:163], v177 offset:32768
	ds_read_b128 v[164:167], v177 offset:33792
	ds_read_b128 v[178:181], v177 offset:34816
	ds_read_b128 v[182:185], v177 offset:35840
	ds_read_b128 v[186:189], v177 offset:36864
	ds_read_b128 v[190:193], v177 offset:37888
	ds_read_b128 v[194:197], v177 offset:38912
	ds_read_b128 v[198:201], v177 offset:39936
	buffer_load_dwordx4 v170, s[36:39], s68 offen lds
	s_mov_b32 m0, s34
	s_nop 0
	buffer_load_dwordx4 v172, s[36:39], s68 offen lds
	s_waitcnt vmcnt(8)
	s_waitcnt lgkmcnt(0)
	s_barrier
	s_setprio 1
	v_mfma_f32_16x16x32_bf16 v[132:135], v[112:115], v[160:163], v[132:135]
	v_mfma_f32_16x16x32_bf16 v[128:131], v[136:139], v[160:163], v[128:131]
	v_mfma_f32_16x16x32_bf16 v[108:111], v[112:115], v[178:181], v[108:111]
	v_mfma_f32_16x16x32_bf16 v[104:107], v[136:139], v[178:181], v[104:107]
	v_mfma_f32_16x16x32_bf16 v[92:95], v[112:115], v[186:189], v[92:95]
	v_mfma_f32_16x16x32_bf16 v[88:91], v[136:139], v[186:189], v[88:91]
	v_mfma_f32_16x16x32_bf16 v[76:79], v[112:115], v[194:197], v[76:79]
	v_mfma_f32_16x16x32_bf16 v[72:75], v[136:139], v[194:197], v[72:75]
	v_mfma_f32_16x16x32_bf16 v[132:135], v[124:127], v[164:167], v[132:135]
	v_mfma_f32_16x16x32_bf16 v[128:131], v[140:143], v[164:167], v[128:131]
	v_mfma_f32_16x16x32_bf16 v[108:111], v[124:127], v[182:185], v[108:111]
	v_mfma_f32_16x16x32_bf16 v[104:107], v[140:143], v[182:185], v[104:107]
	v_mfma_f32_16x16x32_bf16 v[92:95], v[124:127], v[190:193], v[92:95]
	v_mfma_f32_16x16x32_bf16 v[88:91], v[140:143], v[190:193], v[88:91]
	v_mfma_f32_16x16x32_bf16 v[76:79], v[124:127], v[198:201], v[76:79]
	v_mfma_f32_16x16x32_bf16 v[72:75], v[140:143], v[198:201], v[72:75]
	s_setprio 0
	s_setprio 1
	v_mfma_f32_16x16x32_bf16 v[120:123], v[144:147], v[160:163], v[120:123]
	v_mfma_f32_16x16x32_bf16 v[116:119], v[152:155], v[160:163], v[116:119]
	v_mfma_f32_16x16x32_bf16 v[100:103], v[144:147], v[178:181], v[100:103]
	v_mfma_f32_16x16x32_bf16 v[96:99], v[152:155], v[178:181], v[96:99]
	v_mfma_f32_16x16x32_bf16 v[84:87], v[144:147], v[186:189], v[84:87]
	v_mfma_f32_16x16x32_bf16 v[80:83], v[152:155], v[186:189], v[80:83]
	v_mfma_f32_16x16x32_bf16 v[68:71], v[144:147], v[194:197], v[68:71]
	v_mfma_f32_16x16x32_bf16 v[64:67], v[152:155], v[194:197], v[64:67]
	v_mfma_f32_16x16x32_bf16 v[120:123], v[148:151], v[164:167], v[120:123]
	v_mfma_f32_16x16x32_bf16 v[116:119], v[156:159], v[164:167], v[116:119]
	v_mfma_f32_16x16x32_bf16 v[100:103], v[148:151], v[182:185], v[100:103]
	v_mfma_f32_16x16x32_bf16 v[96:99], v[156:159], v[182:185], v[96:99]
	v_mfma_f32_16x16x32_bf16 v[84:87], v[148:151], v[190:193], v[84:87]
	v_mfma_f32_16x16x32_bf16 v[80:83], v[156:159], v[190:193], v[80:83]
	v_mfma_f32_16x16x32_bf16 v[68:71], v[148:151], v[198:201], v[68:71]
	v_mfma_f32_16x16x32_bf16 v[64:67], v[156:159], v[198:201], v[64:67]
	s_setprio 0
	s_barrier
	s_mov_b32 m0, s1
	s_bitset1_b32 s55, 7
	ds_read_b128 v[160:163], v177 offset:49152
	ds_read_b128 v[164:167], v177 offset:50176
	ds_read_b128 v[178:181], v177 offset:51200
	ds_read_b128 v[182:185], v177 offset:52224
	ds_read_b128 v[186:189], v177 offset:53248
	ds_read_b128 v[190:193], v177 offset:54272
	ds_read_b128 v[194:197], v177 offset:55296
	ds_read_b128 v[198:201], v177 offset:56320
	buffer_load_dwordx4 v171, s[4:7], s55 offen lds
	s_mov_b32 m0, s35
	s_nop 0
	buffer_load_dwordx4 v173, s[4:7], s55 offen lds
	s_add_i32 s55, s55, s25
	s_mov_b32 m0, s43
	s_nop 0
	buffer_load_dwordx4 v171, s[4:7], s55 offen lds
	s_mov_b32 m0, s44
	s_nop 0
	buffer_load_dwordx4 v173, s[4:7], s55 offen lds
	s_mov_b32 m0, s41
	s_nop 0
	buffer_load_dwordx4 v170, s[36:39], s54 offen lds
	s_mov_b32 m0, s42
	s_nop 0
	buffer_load_dwordx4 v172, s[36:39], s54 offen lds
	s_waitcnt vmcnt(8)
	s_waitcnt lgkmcnt(0)
	s_barrier
	s_setprio 1
	v_mfma_f32_16x16x32_bf16 v[60:63], v[112:115], v[160:163], v[60:63]
	v_mfma_f32_16x16x32_bf16 v[56:59], v[136:139], v[160:163], v[56:59]
	v_mfma_f32_16x16x32_bf16 v[44:47], v[112:115], v[178:181], v[44:47]
	v_mfma_f32_16x16x32_bf16 v[40:43], v[136:139], v[178:181], v[40:43]
	v_mfma_f32_16x16x32_bf16 v[28:31], v[112:115], v[186:189], v[28:31]
	v_mfma_f32_16x16x32_bf16 v[24:27], v[136:139], v[186:189], v[24:27]
	v_mfma_f32_16x16x32_bf16 v[12:15], v[112:115], v[194:197], v[12:15]
	v_mfma_f32_16x16x32_bf16 v[8:11], v[136:139], v[194:197], v[8:11]
	v_mfma_f32_16x16x32_bf16 v[60:63], v[124:127], v[164:167], v[60:63]
	v_mfma_f32_16x16x32_bf16 v[56:59], v[140:143], v[164:167], v[56:59]
	v_mfma_f32_16x16x32_bf16 v[44:47], v[124:127], v[182:185], v[44:47]
	v_mfma_f32_16x16x32_bf16 v[40:43], v[140:143], v[182:185], v[40:43]
	v_mfma_f32_16x16x32_bf16 v[28:31], v[124:127], v[190:193], v[28:31]
	v_mfma_f32_16x16x32_bf16 v[24:27], v[140:143], v[190:193], v[24:27]
	v_mfma_f32_16x16x32_bf16 v[12:15], v[124:127], v[198:201], v[12:15]
	v_mfma_f32_16x16x32_bf16 v[8:11], v[140:143], v[198:201], v[8:11]
	s_setprio 0
	s_setprio 1
	v_mfma_f32_16x16x32_bf16 v[52:55], v[144:147], v[160:163], v[52:55]
	v_mfma_f32_16x16x32_bf16 v[48:51], v[152:155], v[160:163], v[48:51]
	v_mfma_f32_16x16x32_bf16 v[36:39], v[144:147], v[178:181], v[36:39]
	v_mfma_f32_16x16x32_bf16 v[32:35], v[152:155], v[178:181], v[32:35]
	v_mfma_f32_16x16x32_bf16 v[20:23], v[144:147], v[186:189], v[20:23]
	v_mfma_f32_16x16x32_bf16 v[16:19], v[152:155], v[186:189], v[16:19]
	v_mfma_f32_16x16x32_bf16 v[4:7], v[144:147], v[194:197], v[4:7]
	v_mfma_f32_16x16x32_bf16 v[0:3], v[152:155], v[194:197], v[0:3]
	v_mfma_f32_16x16x32_bf16 v[52:55], v[148:151], v[164:167], v[52:55]
	v_mfma_f32_16x16x32_bf16 v[48:51], v[156:159], v[164:167], v[48:51]
	v_mfma_f32_16x16x32_bf16 v[36:39], v[148:151], v[182:185], v[36:39]
	v_mfma_f32_16x16x32_bf16 v[32:35], v[156:159], v[182:185], v[32:35]
	v_mfma_f32_16x16x32_bf16 v[20:23], v[148:151], v[190:193], v[20:23]
	v_mfma_f32_16x16x32_bf16 v[16:19], v[156:159], v[190:193], v[16:19]
	v_mfma_f32_16x16x32_bf16 v[4:7], v[148:151], v[198:201], v[4:7]
	v_mfma_f32_16x16x32_bf16 v[0:3], v[156:159], v[198:201], v[0:3]
	s_setprio 0
	s_barrier
	s_add_i32 s67, s67, 2
	s_addk_i32 s65, 0x100
	s_addk_i32 s66, 0x100
	s_cmp_ge_i32 s67, s47
	s_cbranch_scc0 .LBB0_1701
	v_readlane_b32 s68, v255, 22
	v_readlane_b32 s69, v255, 23
	s_and_b64 vcc, exec, s[16:17]
	s_cbranch_vccnz .LBB0_1704
	s_branch .LBB0_1705

; #define PG8_STAGE(bufoff, rs_, soff_, voff) do { _Pragma("unroll") for (int _i = 0; _i < 2; ++_i) \
;         __builtin_amdgcn_raw_ptr_buffer_load_lds(rs_, (LAS void*)(lds + (bufoff) + ldsw + _i * 8192), 16, (int)(voff)[_i], (int)(soff_), 0, 0); } while (0)
; #define PG8_LDA(dst, b, h) do { _Pragma("unroll") for (int m = 0; m < 4; ++m) dst[m] = PG8_LD2(lds + PG8_SA(b, h) + aoff + m * 2048); } while (0)
; #define PG8_LDB(dst, b, h) do { _Pragma("unroll") for (int n = 0; n < 2; ++n) dst[n] = PG8_LD2(lds + PG8_SB(b, h) + boff + n * 2048); } while (0)
; #define PG8_BAR __builtin_amdgcn_s_barrier()
; template <class Epi, class Sched, bool ALIGN_EPI = false, bool SP2 = false, bool FP8 = false>
; __device__ __forceinline__ void gemm_phase(LAS unsigned char* lds, const Gemm g, const Sched& S, const Epi& E, int wbase) {
;     ...
;             const bool last = (t == nt - 2);
;             const unsigned a1 = cA + (unsigned)(t + 1) * kstep;
;             const unsigned a2 = last ? nA : cA + (unsigned)(t + 2) * kstep, b2 = last ? nB : cB + (unsigned)(t + 2) * kstep; const rsrc_t rA2 = (Sched::TWO && last) ? rAn : rAc, rB2 = (Sched::TWO && last) ? rBn : rBc;
;             const unsigned a3 = a2 + kstep, b3 = b2 + kstep;
;             if (last && has_next) S.a_ready(nxt);
;             if constexpr (SP2) {
;             PG8_LDB(B0, 0, 0); PG8_LDB(B1, 0, 1); PG8_SCHED; PG8_LDA(At, 0, 0); PG8_STAGE(PG8_SA(1, 1), rAc, a1 + hstep, voffA);
;             PG8_WAIT_V(8); PG8_WAIT_L(0); PG8_BAR; PG8_MMA(0, 0, At, B0); PG8_MMA(0, 1, At, B1); PG8_BAR; PG8_SCHED;
;             PG8_LDA(At, 0, 1); PG8_STAGE(PG8_SB(0, 0), rB2, b2, voffB); PG8_STAGE(PG8_SB(0, 1), rB2, b2 + hstep, voffB); PG8_STAGE(PG8_SA(0, 0), rA2, a2, voffA);
;             PG8_WAIT_V(8); PG8_WAIT_L(0); PG8_BAR; PG8_MMA(1, 0, At, B0); PG8_MMA(1, 1, At, B1); PG8_BAR; PG8_SCHED;
;             PG8_LDB(B0, 1, 0); PG8_LDB(B1, 1, 1); PG8_SCHED; PG8_LDA(At, 1, 0); PG8_STAGE(PG8_SA(0, 1), rA2, a2 + hstep, voffA);
;             PG8_WAIT_V(8); PG8_WAIT_L(0); PG8_BAR; PG8_MMA(0, 0, At, B0); PG8_MMA(0, 1, At, B1); PG8_BAR; PG8_SCHED;
;             PG8_LDA(At, 1, 1); PG8_STAGE(PG8_SB(1, 0), rB2, b3, voffB); PG8_STAGE(PG8_SB(1, 1), rB2, b3 + hstep, voffB); PG8_STAGE(PG8_SA(1, 0), rA2, a3, voffA);
;             PG8_WAIT_V(8); PG8_WAIT_L(0); PG8_BAR; PG8_MMA(1, 0, At, B0); PG8_MMA(1, 1, At, B1); PG8_BAR; PG8_SCHED;
.LBB0_1781:
	v_add_u32_e32 v140, 0x10000, v154
	v_add_u32_e32 v144, 0x14000, v154
	ds_read_b128 v[128:131], v140
	ds_read_b128 v[132:135], v140 offset:1024
	ds_read_b128 v[136:139], v140 offset:2048
	ds_read_b128 v[140:143], v140 offset:3072
	ds_read_b128 v[156:159], v144
	ds_read_b128 v[160:163], v144 offset:1024
	ds_read_b128 v[164:167], v144 offset:2048
	ds_read_b128 v[168:171], v144 offset:3072
	s_add_i32 s6, s61, 0x80
	s_cmp_eq_u32 s45, s63
	s_cselect_b32 s65, s59, s6
	s_cselect_b32 s55, s60, s62
	s_or_b32 s54, s65, 0x80
	s_add_i32 s6, s21, s61
	s_mov_b32 m0, s46
	ds_read_b128 v[172:175], v155
	ds_read_b128 v[176:179], v155 offset:1024
	ds_read_b128 v[180:183], v155 offset:2048
	ds_read_b128 v[184:187], v155 offset:3072
	ds_read_b128 v[194:197], v155 offset:4096
	ds_read_b128 v[198:201], v155 offset:5120
	ds_read_b128 v[202:205], v155 offset:6144
	ds_read_b128 v[206:209], v155 offset:7168
	buffer_load_dwordx4 v148, s[36:39], s6 offen lds
	s_mov_b32 m0, s47
	s_nop 0
	buffer_load_dwordx4 v150, s[36:39], s6 offen lds
	s_waitcnt vmcnt(8)
	s_waitcnt lgkmcnt(0)
	s_barrier
	s_setprio 1
	v_mfma_f32_16x16x128_f8f6f4 v[120:123], v[128:135], v[172:179], v[120:123]
	v_mfma_f32_16x16x128_f8f6f4 v[124:127], v[136:143], v[172:179], v[124:127]
	v_mfma_f32_16x16x128_f8f6f4 v[104:107], v[128:135], v[180:187], v[104:107]
	v_mfma_f32_16x16x128_f8f6f4 v[108:111], v[136:143], v[180:187], v[108:111]
	v_mfma_f32_16x16x128_f8f6f4 v[144:147], v[128:135], v[194:201], v[88:91]
	v_mfma_f32_16x16x128_f8f6f4 v[188:191], v[136:143], v[194:201], v[92:95]
	v_mfma_f32_16x16x128_f8f6f4 v[210:213], v[128:135], v[202:209], v[72:75]
	v_mfma_f32_16x16x128_f8f6f4 v[214:217], v[136:143], v[202:209], v[76:79]
	s_setprio 0
	s_setprio 1
	v_mfma_f32_16x16x128_f8f6f4 v[112:115], v[156:163], v[172:179], v[112:115]
	v_mfma_f32_16x16x128_f8f6f4 v[116:119], v[164:171], v[172:179], v[116:119]
	v_mfma_f32_16x16x128_f8f6f4 v[96:99], v[156:163], v[180:187], v[96:99]
	v_mfma_f32_16x16x128_f8f6f4 v[100:103], v[164:171], v[180:187], v[100:103]
	v_mfma_f32_16x16x128_f8f6f4 v[172:175], v[156:163], v[194:201], v[80:83]
	v_mfma_f32_16x16x128_f8f6f4 v[176:179], v[164:171], v[194:201], v[84:87]
	v_mfma_f32_16x16x128_f8f6f4 v[180:183], v[156:163], v[202:209], v[64:67]
	v_mfma_f32_16x16x128_f8f6f4 v[184:187], v[164:171], v[202:209], v[68:71]
	s_setprio 0
	s_barrier
	s_mov_b32 m0, s23
	s_mov_b32 s6, s38
	s_mov_b32 s7, s39
	s_nop 0
	ds_read_b128 v[64:67], v155 offset:16384
	ds_read_b128 v[68:71], v155 offset:17408
	ds_read_b128 v[72:75], v155 offset:18432
	ds_read_b128 v[76:79], v155 offset:19456
	ds_read_b128 v[80:83], v155 offset:20480
	ds_read_b128 v[84:87], v155 offset:21504
	ds_read_b128 v[88:91], v155 offset:22528
	ds_read_b128 v[92:95], v155 offset:23552
	buffer_load_dwordx4 v149, s[4:7], s55 offen lds
	s_mov_b32 m0, s24
	s_add_i32 s66, s55, s21
	buffer_load_dwordx4 v151, s[4:7], s55 offen lds
	s_mov_b32 m0, s25
	s_nop 0
	buffer_load_dwordx4 v149, s[4:7], s66 offen lds
	s_mov_b32 m0, s26
	s_nop 0
	buffer_load_dwordx4 v151, s[4:7], s66 offen lds
	s_mov_b32 m0, s22
	s_nop 0
	buffer_load_dwordx4 v148, s[36:39], s65 offen lds
	s_mov_b32 m0, s27
	s_nop 0
	buffer_load_dwordx4 v150, s[36:39], s65 offen lds
	s_waitcnt vmcnt(8)
	s_waitcnt lgkmcnt(0)
	s_barrier
	s_setprio 1
	v_mfma_f32_16x16x128_f8f6f4 v[56:59], v[128:135], v[64:71], v[56:59]
	v_mfma_f32_16x16x128_f8f6f4 v[60:63], v[136:143], v[64:71], v[60:63]
	v_mfma_f32_16x16x128_f8f6f4 v[8:11], v[128:135], v[88:95], v[8:11]
	v_mfma_f32_16x16x128_f8f6f4 v[192:195], v[128:135], v[72:79], v[40:43]
	v_mfma_f32_16x16x128_f8f6f4 v[196:199], v[136:143], v[72:79], v[44:47]
	v_mfma_f32_16x16x128_f8f6f4 v[200:203], v[128:135], v[80:87], v[24:27]
	v_mfma_f32_16x16x128_f8f6f4 v[204:207], v[136:143], v[80:87], v[28:31]
	v_mfma_f32_16x16x128_f8f6f4 v[218:221], v[136:143], v[88:95], v[12:15]
	s_setprio 0
	s_setprio 1
	v_mfma_f32_16x16x128_f8f6f4 v[52:55], v[164:171], v[64:71], v[52:55]
	v_mfma_f32_16x16x128_f8f6f4 v[226:229], v[156:163], v[64:71], v[48:51]
	v_mfma_f32_16x16x128_f8f6f4 v[230:233], v[156:163], v[72:79], v[32:35]
	v_mfma_f32_16x16x128_f8f6f4 v[234:237], v[164:171], v[72:79], v[36:39]
	v_mfma_f32_16x16x128_f8f6f4 v[238:241], v[156:163], v[80:87], v[16:19]
	v_mfma_f32_16x16x128_f8f6f4 v[242:245], v[164:171], v[80:87], v[20:23]
	v_mfma_f32_16x16x128_f8f6f4 v[246:249], v[156:163], v[88:95], v[4:7]
	v_mfma_f32_16x16x128_f8f6f4 v[250:253], v[164:171], v[88:95], v[0:3]
	s_setprio 0
	s_barrier
; #define PG8_STAGE(bufoff, rs_, soff_, voff) do { _Pragma("unroll") for (int _i = 0; _i < 2; ++_i) \
;         __builtin_amdgcn_raw_ptr_buffer_load_lds(rs_, (LAS void*)(lds + (bufoff) + ldsw + _i * 8192), 16, (int)(voff)[_i], (int)(soff_), 0, 0); } while (0)
; #define PG8_LDA(dst, b, h) do { _Pragma("unroll") for (int m = 0; m < 4; ++m) dst[m] = PG8_LD2(lds + PG8_SA(b, h) + aoff + m * 2048); } while (0)
; #define PG8_LDB(dst, b, h) do { _Pragma("unroll") for (int n = 0; n < 2; ++n) dst[n] = PG8_LD2(lds + PG8_SB(b, h) + boff + n * 2048); } while (0)
; #define PG8_WAIT_V(n) asm volatile("s_waitcnt vmcnt(" #n ")" ::: "memory")
; #define PG8_WAIT_L(n) asm volatile("s_waitcnt lgkmcnt(" #n ")" ::: "memory")
; #define PG8_BAR __builtin_amdgcn_s_barrier()
; #define PG8_SCHED __builtin_amdgcn_sched_barrier(0)
; template <class Epi, class Sched, bool ALIGN_EPI = false, bool SP2 = false, bool FP8 = false>
; __device__ __forceinline__ void gemm_phase(LAS unsigned char* lds, const Gemm g, const Sched& S, const Epi& E, int wbase) {
;     ...
;         for (int t = 0; t < nt; t += 2) {
;             const bool last = (t == nt - 2);
;             const unsigned a1 = cA + (unsigned)(t + 1) * kstep;
;             const unsigned a2 = last ? nA : cA + (unsigned)(t + 2) * kstep, b2 = last ? nB : cB + (unsigned)(t + 2) * kstep; const rsrc_t rA2 = (Sched::TWO && last) ? rAn : rAc, rB2 = (Sched::TWO && last) ? rBn : rBc;
;             const unsigned a3 = a2 + kstep, b3 = b2 + kstep;
;             if (last && has_next) S.a_ready(nxt);
;     ...
;             PG8_LDB(B0, 1, 0); PG8_LDB(B1, 1, 1); PG8_SCHED; PG8_LDA(At, 1, 0); PG8_STAGE(PG8_SA(0, 1), rA2, a2 + hstep, voffA);
;             PG8_WAIT_V(8); PG8_WAIT_L(0); PG8_BAR; PG8_MMA(0, 0, At, B0); PG8_MMA(0, 1, At, B1); PG8_BAR; PG8_SCHED;
;             PG8_LDA(At, 1, 1); PG8_STAGE(PG8_SB(1, 0), rB2, b3, voffB); PG8_STAGE(PG8_SB(1, 1), rB2, b3 + hstep, voffB); PG8_STAGE(PG8_SA(1, 0), rA2, a3, voffA);
;             PG8_WAIT_V(8); PG8_WAIT_L(0); PG8_BAR; PG8_MMA(1, 0, At, B0); PG8_MMA(1, 1, At, B1); PG8_BAR; PG8_SCHED;
	s_nop 1
	v_add_u32_e32 v16, 0x18000, v154
	v_add_u32_e32 v20, 0x1c000, v154
	s_nop 0
	ds_read_b128 v[0:3], v16
	ds_read_b128 v[4:7], v16 offset:1024
	ds_read_b128 v[12:15], v16 offset:2048
	ds_read_b128 v[16:19], v16 offset:3072
	ds_read_b128 v[128:131], v20
	ds_read_b128 v[132:135], v20 offset:1024
	ds_read_b128 v[136:139], v20 offset:2048
	ds_read_b128 v[140:143], v20 offset:3072
	s_add_i32 s65, s65, s21
	s_mov_b32 m0, s28
	ds_read_b128 v[20:23], v155 offset:32768
	ds_read_b128 v[24:27], v155 offset:33792
	ds_read_b128 v[28:31], v155 offset:34816
	ds_read_b128 v[32:35], v155 offset:35840
	ds_read_b128 v[36:39], v155 offset:36864
	ds_read_b128 v[40:43], v155 offset:37888
	ds_read_b128 v[44:47], v155 offset:38912
	ds_read_b128 v[48:51], v155 offset:39936
	buffer_load_dwordx4 v148, s[36:39], s65 offen lds
	s_mov_b32 m0, s29
	s_nop 0
	buffer_load_dwordx4 v150, s[36:39], s65 offen lds
	s_waitcnt vmcnt(8)
	s_waitcnt lgkmcnt(0)
	s_barrier
	s_setprio 1
	v_mfma_f32_16x16x128_f8f6f4 v[120:123], v[0:7], v[20:27], v[120:123]
	v_mfma_f32_16x16x128_f8f6f4 v[124:127], v[12:19], v[20:27], v[124:127]
	v_mfma_f32_16x16x128_f8f6f4 v[104:107], v[0:7], v[28:35], v[104:107]
	v_mfma_f32_16x16x128_f8f6f4 v[108:111], v[12:19], v[28:35], v[108:111]
	v_mfma_f32_16x16x128_f8f6f4 v[88:91], v[0:7], v[36:43], v[144:147]
	v_mfma_f32_16x16x128_f8f6f4 v[92:95], v[12:19], v[36:43], v[188:191]
	v_mfma_f32_16x16x128_f8f6f4 v[72:75], v[0:7], v[44:51], v[210:213]
	v_mfma_f32_16x16x128_f8f6f4 v[76:79], v[12:19], v[44:51], v[214:217]
	s_setprio 0
	s_setprio 1
	v_mfma_f32_16x16x128_f8f6f4 v[112:115], v[128:135], v[20:27], v[112:115]
	v_mfma_f32_16x16x128_f8f6f4 v[116:119], v[136:143], v[20:27], v[116:119]
	v_mfma_f32_16x16x128_f8f6f4 v[96:99], v[128:135], v[28:35], v[96:99]
	v_mfma_f32_16x16x128_f8f6f4 v[100:103], v[136:143], v[28:35], v[100:103]
	v_mfma_f32_16x16x128_f8f6f4 v[80:83], v[128:135], v[36:43], v[172:175]
	v_mfma_f32_16x16x128_f8f6f4 v[84:87], v[136:143], v[36:43], v[176:179]
	v_mfma_f32_16x16x128_f8f6f4 v[64:67], v[128:135], v[44:51], v[180:183]
	v_mfma_f32_16x16x128_f8f6f4 v[68:71], v[136:143], v[44:51], v[184:187]
	s_setprio 0
	s_barrier
	s_mov_b32 m0, s30
	s_bitset1_b32 s55, 7
	ds_read_b128 v[32:35], v155 offset:49152
	ds_read_b128 v[36:39], v155 offset:50176
	ds_read_b128 v[156:159], v155 offset:51200
	ds_read_b128 v[160:163], v155 offset:52224
	ds_read_b128 v[164:167], v155 offset:53248
	ds_read_b128 v[168:171], v155 offset:54272
	ds_read_b128 v[172:175], v155 offset:55296
	ds_read_b128 v[176:179], v155 offset:56320
	buffer_load_dwordx4 v149, s[4:7], s55 offen lds
	s_mov_b32 m0, s31
	s_nop 0
	buffer_load_dwordx4 v151, s[4:7], s55 offen lds
	s_add_i32 s55, s55, s21
	s_mov_b32 m0, s35
	s_nop 0
	buffer_load_dwordx4 v149, s[4:7], s55 offen lds
	s_mov_b32 m0, s41
	s_nop 0
	buffer_load_dwordx4 v151, s[4:7], s55 offen lds
	s_mov_b32 m0, s33
	s_nop 0
	buffer_load_dwordx4 v148, s[36:39], s54 offen lds
	s_mov_b32 m0, s34
	s_nop 0
	buffer_load_dwordx4 v150, s[36:39], s54 offen lds
	s_waitcnt vmcnt(8)
	s_waitcnt lgkmcnt(0)
	s_barrier
	s_setprio 1
	v_mfma_f32_16x16x128_f8f6f4 v[56:59], v[0:7], v[32:39], v[56:59]
	v_mfma_f32_16x16x128_f8f6f4 v[60:63], v[12:19], v[32:39], v[60:63]
	v_mfma_f32_16x16x128_f8f6f4 v[40:43], v[0:7], v[156:163], v[192:195]
	v_mfma_f32_16x16x128_f8f6f4 v[44:47], v[12:19], v[156:163], v[196:199]
	v_mfma_f32_16x16x128_f8f6f4 v[24:27], v[0:7], v[164:171], v[200:203]
	v_mfma_f32_16x16x128_f8f6f4 v[28:31], v[12:19], v[164:171], v[204:207]
	v_mfma_f32_16x16x128_f8f6f4 v[8:11], v[0:7], v[172:179], v[8:11]
	v_mfma_f32_16x16x128_f8f6f4 v[12:15], v[12:19], v[172:179], v[218:221]
	s_setprio 0
	s_setprio 1
	v_mfma_f32_16x16x128_f8f6f4 v[48:51], v[128:135], v[32:39], v[226:229]
	v_mfma_f32_16x16x128_f8f6f4 v[52:55], v[136:143], v[32:39], v[52:55]
	v_mfma_f32_16x16x128_f8f6f4 v[32:35], v[128:135], v[156:163], v[230:233]
	v_mfma_f32_16x16x128_f8f6f4 v[36:39], v[136:143], v[156:163], v[234:237]
	v_mfma_f32_16x16x128_f8f6f4 v[16:19], v[128:135], v[164:171], v[238:241]
	v_mfma_f32_16x16x128_f8f6f4 v[20:23], v[136:143], v[164:171], v[242:245]
	v_mfma_f32_16x16x128_f8f6f4 v[4:7], v[128:135], v[172:179], v[246:249]
	v_mfma_f32_16x16x128_f8f6f4 v[0:3], v[136:143], v[172:179], v[250:253]
	s_setprio 0
	s_barrier
	s_add_i32 s63, s63, 2
	s_addk_i32 s61, 0x100
	s_addk_i32 s62, 0x100
	s_cmp_ge_i32 s63, s43
	s_cbranch_scc0 .LBB0_1781
	v_mov_b32_e32 v230, v222
	v_mov_b32_e32 v233, v223
	v_mov_b32_e32 v231, v225
	v_mov_b32_e32 v234, 0xff61b1e6
	s_and_b64 vcc, exec, s[16:17]
	s_cbranch_vccnz .LBB0_1784
	s_branch .LBB0_1785

; #define PG8_STAGE(bufoff, rs_, soff_, voff) do { _Pragma("unroll") for (int _i = 0; _i < 2; ++_i) \
;         __builtin_amdgcn_raw_ptr_buffer_load_lds(rs_, (LAS void*)(lds + (bufoff) + ldsw + _i * 8192), 16, (int)(voff)[_i], (int)(soff_), 0, 0); } while (0)
; #define PG8_LDA(dst, b, h) do { _Pragma("unroll") for (int m = 0; m < 4; ++m) dst[m] = PG8_LD2(lds + PG8_SA(b, h) + aoff + m * 2048); } while (0)
; #define PG8_LDB(dst, b, h) do { _Pragma("unroll") for (int n = 0; n < 2; ++n) dst[n] = PG8_LD2(lds + PG8_SB(b, h) + boff + n * 2048); } while (0)
; #define PG8_BAR __builtin_amdgcn_s_barrier()
; template <class Epi, class Sched, bool ALIGN_EPI = false, bool SP2 = false, bool FP8 = false>
; __device__ __forceinline__ void gemm_phase(LAS unsigned char* lds, const Gemm g, const Sched& S, const Epi& E, int wbase) {
;     ...
;             const bool last = (t == nt - 2);
;             const unsigned a1 = cA + (unsigned)(t + 1) * kstep;
;             const unsigned a2 = last ? nA : cA + (unsigned)(t + 2) * kstep, b2 = last ? nB : cB + (unsigned)(t + 2) * kstep; const rsrc_t rA2 = (Sched::TWO && last) ? rAn : rAc, rB2 = (Sched::TWO && last) ? rBn : rBc;
;             const unsigned a3 = a2 + kstep, b3 = b2 + kstep;
;             if (last && has_next) S.a_ready(nxt);
;             if constexpr (SP2) {
;             PG8_LDB(B0, 0, 0); PG8_LDB(B1, 0, 1); PG8_SCHED; PG8_LDA(At, 0, 0); PG8_STAGE(PG8_SA(1, 1), rAc, a1 + hstep, voffA);
;             PG8_WAIT_V(8); PG8_WAIT_L(0); PG8_BAR; PG8_MMA(0, 0, At, B0); PG8_MMA(0, 1, At, B1); PG8_BAR; PG8_SCHED;
;             PG8_LDA(At, 0, 1); PG8_STAGE(PG8_SB(0, 0), rB2, b2, voffB); PG8_STAGE(PG8_SB(0, 1), rB2, b2 + hstep, voffB); PG8_STAGE(PG8_SA(0, 0), rA2, a2, voffA);
;             PG8_WAIT_V(8); PG8_WAIT_L(0); PG8_BAR; PG8_MMA(1, 0, At, B0); PG8_MMA(1, 1, At, B1); PG8_BAR; PG8_SCHED;
;             PG8_LDB(B0, 1, 0); PG8_LDB(B1, 1, 1); PG8_SCHED; PG8_LDA(At, 1, 0); PG8_STAGE(PG8_SA(0, 1), rA2, a2 + hstep, voffA);
;             PG8_WAIT_V(8); PG8_WAIT_L(0); PG8_BAR; PG8_MMA(0, 0, At, B0); PG8_MMA(0, 1, At, B1); PG8_BAR; PG8_SCHED;
;             PG8_LDA(At, 1, 1); PG8_STAGE(PG8_SB(1, 0), rB2, b3, voffB); PG8_STAGE(PG8_SB(1, 1), rB2, b3 + hstep, voffB); PG8_STAGE(PG8_SA(1, 0), rA2, a3, voffA);
;             PG8_WAIT_V(8); PG8_WAIT_L(0); PG8_BAR; PG8_MMA(1, 0, At, B0); PG8_MMA(1, 1, At, B1); PG8_BAR; PG8_SCHED;
.LBB0_1854:
	v_add_u32_e32 v140, 0x10000, v176
	v_add_u32_e32 v156, 0x14000, v176
	ds_read_b128 v[128:131], v140
	ds_read_b128 v[132:135], v140 offset:1024
	ds_read_b128 v[136:139], v140 offset:2048
	ds_read_b128 v[140:143], v140 offset:3072
	ds_read_b128 v[144:147], v156
	ds_read_b128 v[148:151], v156 offset:1024
	ds_read_b128 v[152:155], v156 offset:2048
	ds_read_b128 v[156:159], v156 offset:3072
	s_add_i32 s6, s65, 0x80
	s_cmp_eq_u32 s52, s67
	s_cselect_b32 s68, s21, s6
	s_cselect_b32 s55, s63, s66
	s_or_b32 s54, s68, 0x80
	s_add_i32 s6, s24, s65
	s_mov_b32 m0, s53
	ds_read_b128 v[160:163], v177
	ds_read_b128 v[164:167], v177 offset:1024
	ds_read_b128 v[178:181], v177 offset:2048
	ds_read_b128 v[182:185], v177 offset:3072
	ds_read_b128 v[194:197], v177 offset:4096
	ds_read_b128 v[198:201], v177 offset:5120
	ds_read_b128 v[202:205], v177 offset:6144
	ds_read_b128 v[206:209], v177 offset:7168
	buffer_load_dwordx4 v170, s[36:39], s6 offen lds
	s_mov_b32 m0, s56
	s_nop 0
	buffer_load_dwordx4 v172, s[36:39], s6 offen lds
	s_waitcnt vmcnt(8)
	s_waitcnt lgkmcnt(0)
	s_barrier
	s_setprio 1
	v_mfma_f32_16x16x128_f8f6f4 v[124:127], v[128:135], v[160:167], v[124:127]
	v_mfma_f32_16x16x128_f8f6f4 v[120:123], v[136:143], v[160:167], v[120:123]
	v_mfma_f32_16x16x128_f8f6f4 v[108:111], v[128:135], v[178:185], v[108:111]
	v_mfma_f32_16x16x128_f8f6f4 v[104:107], v[136:143], v[178:185], v[104:107]
	v_mfma_f32_16x16x128_f8f6f4 v[186:189], v[128:135], v[194:201], v[92:95]
	v_mfma_f32_16x16x128_f8f6f4 v[190:193], v[136:143], v[194:201], v[88:91]
	v_mfma_f32_16x16x128_f8f6f4 v[210:213], v[128:135], v[202:209], v[76:79]
	v_mfma_f32_16x16x128_f8f6f4 v[214:217], v[136:143], v[202:209], v[72:75]
	s_setprio 0
	s_setprio 1
	v_mfma_f32_16x16x128_f8f6f4 v[116:119], v[144:151], v[160:167], v[116:119]
	v_mfma_f32_16x16x128_f8f6f4 v[112:115], v[152:159], v[160:167], v[112:115]
	v_mfma_f32_16x16x128_f8f6f4 v[100:103], v[144:151], v[178:185], v[100:103]
	v_mfma_f32_16x16x128_f8f6f4 v[96:99], v[152:159], v[178:185], v[96:99]
	v_mfma_f32_16x16x128_f8f6f4 v[160:163], v[144:151], v[194:201], v[84:87]
	v_mfma_f32_16x16x128_f8f6f4 v[164:167], v[152:159], v[194:201], v[80:83]
	v_mfma_f32_16x16x128_f8f6f4 v[178:181], v[144:151], v[202:209], v[68:71]
	v_mfma_f32_16x16x128_f8f6f4 v[182:185], v[152:159], v[202:209], v[64:67]
	s_setprio 0
	s_barrier
	s_mov_b32 m0, s26
	s_mov_b32 s6, s38
	s_mov_b32 s7, s39
	s_nop 1
	ds_read_b128 v[64:67], v177 offset:16384
	ds_read_b128 v[68:71], v177 offset:17408
	ds_read_b128 v[72:75], v177 offset:18432
	ds_read_b128 v[76:79], v177 offset:19456
	ds_read_b128 v[80:83], v177 offset:20480
	ds_read_b128 v[84:87], v177 offset:21504
	ds_read_b128 v[88:91], v177 offset:22528
	ds_read_b128 v[92:95], v177 offset:23552
	buffer_load_dwordx4 v171, s[4:7], s55 offen lds
	s_mov_b32 m0, s27
	s_add_i32 s69, s55, s24
	buffer_load_dwordx4 v173, s[4:7], s55 offen lds
	s_mov_b32 m0, s28
	s_nop 0
	buffer_load_dwordx4 v171, s[4:7], s69 offen lds
	s_mov_b32 m0, s29
	s_nop 0
	buffer_load_dwordx4 v173, s[4:7], s69 offen lds
	s_mov_b32 m0, s25
	s_nop 0
	buffer_load_dwordx4 v170, s[36:39], s68 offen lds
	s_mov_b32 m0, s30
	s_nop 0
	buffer_load_dwordx4 v172, s[36:39], s68 offen lds
	s_waitcnt vmcnt(8)
	s_waitcnt lgkmcnt(0)
	s_barrier
	s_setprio 1
	v_mfma_f32_16x16x128_f8f6f4 v[60:63], v[128:135], v[64:71], v[60:63]
	v_mfma_f32_16x16x128_f8f6f4 v[56:59], v[136:143], v[64:71], v[56:59]
	v_mfma_f32_16x16x128_f8f6f4 v[194:197], v[128:135], v[72:79], v[44:47]
	v_mfma_f32_16x16x128_f8f6f4 v[198:201], v[136:143], v[72:79], v[40:43]
	v_mfma_f32_16x16x128_f8f6f4 v[202:205], v[128:135], v[80:87], v[28:31]
	v_mfma_f32_16x16x128_f8f6f4 v[206:209], v[136:143], v[80:87], v[24:27]
	v_mfma_f32_16x16x128_f8f6f4 v[218:221], v[128:135], v[88:95], v[12:15]
	v_mfma_f32_16x16x128_f8f6f4 v[226:229], v[136:143], v[88:95], v[8:11]
	s_setprio 0
	s_setprio 1
	v_mfma_f32_16x16x128_f8f6f4 v[52:55], v[144:151], v[64:71], v[52:55]
	v_mfma_f32_16x16x128_f8f6f4 v[48:51], v[152:159], v[64:71], v[48:51]
	v_mfma_f32_16x16x128_f8f6f4 v[230:233], v[144:151], v[72:79], v[36:39]
	v_mfma_f32_16x16x128_f8f6f4 v[234:237], v[152:159], v[72:79], v[32:35]
	v_mfma_f32_16x16x128_f8f6f4 v[238:241], v[144:151], v[80:87], v[20:23]
	v_mfma_f32_16x16x128_f8f6f4 v[242:245], v[152:159], v[80:87], v[16:19]
	v_mfma_f32_16x16x128_f8f6f4 v[246:249], v[144:151], v[88:95], v[4:7]
	v_mfma_f32_16x16x128_f8f6f4 v[250:253], v[152:159], v[88:95], v[0:3]
	s_setprio 0
	s_barrier
; #define PG8_STAGE(bufoff, rs_, soff_, voff) do { _Pragma("unroll") for (int _i = 0; _i < 2; ++_i) \
;         __builtin_amdgcn_raw_ptr_buffer_load_lds(rs_, (LAS void*)(lds + (bufoff) + ldsw + _i * 8192), 16, (int)(voff)[_i], (int)(soff_), 0, 0); } while (0)
; #define PG8_LDA(dst, b, h) do { _Pragma("unroll") for (int m = 0; m < 4; ++m) dst[m] = PG8_LD2(lds + PG8_SA(b, h) + aoff + m * 2048); } while (0)
; #define PG8_LDB(dst, b, h) do { _Pragma("unroll") for (int n = 0; n < 2; ++n) dst[n] = PG8_LD2(lds + PG8_SB(b, h) + boff + n * 2048); } while (0)
; #define PG8_WAIT_V(n) asm volatile("s_waitcnt vmcnt(" #n ")" ::: "memory")
; #define PG8_WAIT_L(n) asm volatile("s_waitcnt lgkmcnt(" #n ")" ::: "memory")
; #define PG8_BAR __builtin_amdgcn_s_barrier()
; #define PG8_SCHED __builtin_amdgcn_sched_barrier(0)
; template <class Epi, class Sched, bool ALIGN_EPI = false, bool SP2 = false, bool FP8 = false>
; __device__ __forceinline__ void gemm_phase(LAS unsigned char* lds, const Gemm g, const Sched& S, const Epi& E, int wbase) {
;     ...
;         for (int t = 0; t < nt; t += 2) {
;             const bool last = (t == nt - 2);
;             const unsigned a1 = cA + (unsigned)(t + 1) * kstep;
;             const unsigned a2 = last ? nA : cA + (unsigned)(t + 2) * kstep, b2 = last ? nB : cB + (unsigned)(t + 2) * kstep; const rsrc_t rA2 = (Sched::TWO && last) ? rAn : rAc, rB2 = (Sched::TWO && last) ? rBn : rBc;
;             const unsigned a3 = a2 + kstep, b3 = b2 + kstep;
;             if (last && has_next) S.a_ready(nxt);
;     ...
;             PG8_LDB(B0, 1, 0); PG8_LDB(B1, 1, 1); PG8_SCHED; PG8_LDA(At, 1, 0); PG8_STAGE(PG8_SA(0, 1), rA2, a2 + hstep, voffA);
;             PG8_WAIT_V(8); PG8_WAIT_L(0); PG8_BAR; PG8_MMA(0, 0, At, B0); PG8_MMA(0, 1, At, B1); PG8_BAR; PG8_SCHED;
;             PG8_LDA(At, 1, 1); PG8_STAGE(PG8_SB(1, 0), rB2, b3, voffB); PG8_STAGE(PG8_SB(1, 1), rB2, b3 + hstep, voffB); PG8_STAGE(PG8_SA(1, 0), rA2, a3, voffA);
;             PG8_WAIT_V(8); PG8_WAIT_L(0); PG8_BAR; PG8_MMA(1, 0, At, B0); PG8_MMA(1, 1, At, B1); PG8_BAR; PG8_SCHED;
	v_add_u32_e32 v8, 0x18000, v176
	s_nop 3
	ds_read_b128 v[0:3], v8
	ds_read_b128 v[4:7], v8 offset:1024
	ds_read_b128 v[16:19], v8 offset:2048
	ds_read_b128 v[20:23], v8 offset:3072
	v_add_u32_e32 v8, 0x1c000, v176
	ds_read_b128 v[128:131], v8
	ds_read_b128 v[132:135], v8 offset:1024
	ds_read_b128 v[136:139], v8 offset:2048
	ds_read_b128 v[140:143], v8 offset:3072
	s_add_i32 s68, s68, s24
	s_mov_b32 m0, s31
	ds_read_b128 v[8:11], v177 offset:32768
	ds_read_b128 v[12:15], v177 offset:33792
	ds_read_b128 v[24:27], v177 offset:34816
	ds_read_b128 v[28:31], v177 offset:35840
	ds_read_b128 v[32:35], v177 offset:36864
	ds_read_b128 v[36:39], v177 offset:37888
	ds_read_b128 v[40:43], v177 offset:38912
	ds_read_b128 v[44:47], v177 offset:39936
	buffer_load_dwordx4 v170, s[36:39], s68 offen lds
	s_mov_b32 m0, s33
	s_nop 0
	buffer_load_dwordx4 v172, s[36:39], s68 offen lds
	s_waitcnt vmcnt(8)
	s_waitcnt lgkmcnt(0)
	s_barrier
	s_setprio 1
	v_mfma_f32_16x16x128_f8f6f4 v[124:127], v[0:7], v[8:15], v[124:127]
	v_mfma_f32_16x16x128_f8f6f4 v[120:123], v[16:23], v[8:15], v[120:123]
	v_mfma_f32_16x16x128_f8f6f4 v[108:111], v[0:7], v[24:31], v[108:111]
	v_mfma_f32_16x16x128_f8f6f4 v[104:107], v[16:23], v[24:31], v[104:107]
	v_mfma_f32_16x16x128_f8f6f4 v[92:95], v[0:7], v[32:39], v[186:189]
	v_mfma_f32_16x16x128_f8f6f4 v[88:91], v[16:23], v[32:39], v[190:193]
	v_mfma_f32_16x16x128_f8f6f4 v[76:79], v[0:7], v[40:47], v[210:213]
	v_mfma_f32_16x16x128_f8f6f4 v[72:75], v[16:23], v[40:47], v[214:217]
	s_setprio 0
	s_setprio 1
	v_mfma_f32_16x16x128_f8f6f4 v[116:119], v[128:135], v[8:15], v[116:119]
	v_mfma_f32_16x16x128_f8f6f4 v[112:115], v[136:143], v[8:15], v[112:115]
	v_mfma_f32_16x16x128_f8f6f4 v[100:103], v[128:135], v[24:31], v[100:103]
	v_mfma_f32_16x16x128_f8f6f4 v[96:99], v[136:143], v[24:31], v[96:99]
	v_mfma_f32_16x16x128_f8f6f4 v[84:87], v[128:135], v[32:39], v[160:163]
	v_mfma_f32_16x16x128_f8f6f4 v[80:83], v[136:143], v[32:39], v[164:167]
	v_mfma_f32_16x16x128_f8f6f4 v[68:71], v[128:135], v[40:47], v[178:181]
	v_mfma_f32_16x16x128_f8f6f4 v[64:67], v[136:143], v[40:47], v[182:185]
	s_setprio 0
	s_barrier
	s_mov_b32 m0, s34
	s_bitset1_b32 s55, 7
	ds_read_b128 v[32:35], v177 offset:49152
	ds_read_b128 v[36:39], v177 offset:50176
	ds_read_b128 v[144:147], v177 offset:51200
	ds_read_b128 v[148:151], v177 offset:52224
	ds_read_b128 v[152:155], v177 offset:53248
	ds_read_b128 v[156:159], v177 offset:54272
	ds_read_b128 v[160:163], v177 offset:55296
	ds_read_b128 v[164:167], v177 offset:56320
	buffer_load_dwordx4 v171, s[4:7], s55 offen lds
	s_mov_b32 m0, s35
	s_nop 0
	buffer_load_dwordx4 v173, s[4:7], s55 offen lds
	s_add_i32 s55, s55, s24
	s_mov_b32 m0, s43
	s_nop 0
	buffer_load_dwordx4 v171, s[4:7], s55 offen lds
	s_mov_b32 m0, s44
	s_nop 0
	buffer_load_dwordx4 v173, s[4:7], s55 offen lds
	s_mov_b32 m0, s41
	s_nop 0
	buffer_load_dwordx4 v170, s[36:39], s54 offen lds
	s_mov_b32 m0, s42
	s_nop 0
	buffer_load_dwordx4 v172, s[36:39], s54 offen lds
	s_waitcnt vmcnt(8)
	s_waitcnt lgkmcnt(0)
	s_barrier
	s_setprio 1
	v_mfma_f32_16x16x128_f8f6f4 v[60:63], v[0:7], v[32:39], v[60:63]
	v_mfma_f32_16x16x128_f8f6f4 v[56:59], v[16:23], v[32:39], v[56:59]
	v_mfma_f32_16x16x128_f8f6f4 v[44:47], v[0:7], v[144:151], v[194:197]
	v_mfma_f32_16x16x128_f8f6f4 v[40:43], v[16:23], v[144:151], v[198:201]
	v_mfma_f32_16x16x128_f8f6f4 v[28:31], v[0:7], v[152:159], v[202:205]
	v_mfma_f32_16x16x128_f8f6f4 v[24:27], v[16:23], v[152:159], v[206:209]
	v_mfma_f32_16x16x128_f8f6f4 v[12:15], v[0:7], v[160:167], v[218:221]
	v_mfma_f32_16x16x128_f8f6f4 v[8:11], v[16:23], v[160:167], v[226:229]
	s_setprio 0
	s_setprio 1
	v_mfma_f32_16x16x128_f8f6f4 v[52:55], v[128:135], v[32:39], v[52:55]
	v_mfma_f32_16x16x128_f8f6f4 v[48:51], v[136:143], v[32:39], v[48:51]
	v_mfma_f32_16x16x128_f8f6f4 v[36:39], v[128:135], v[144:151], v[230:233]
	v_mfma_f32_16x16x128_f8f6f4 v[32:35], v[136:143], v[144:151], v[234:237]
	v_mfma_f32_16x16x128_f8f6f4 v[20:23], v[128:135], v[152:159], v[238:241]
	v_mfma_f32_16x16x128_f8f6f4 v[16:19], v[136:143], v[152:159], v[242:245]
	v_mfma_f32_16x16x128_f8f6f4 v[4:7], v[128:135], v[160:167], v[246:249]
	v_mfma_f32_16x16x128_f8f6f4 v[0:3], v[136:143], v[160:167], v[250:253]
	s_setprio 0
	s_barrier
	s_add_i32 s67, s67, 2
	s_addk_i32 s65, 0x100
	s_addk_i32 s66, 0x100
	s_cmp_ge_i32 s67, s47
	s_cbranch_scc0 .LBB0_1854
	v_readlane_b32 s68, v255, 22
	v_readlane_b32 s69, v255, 23
	v_mov_b32_e32 v230, v168
	v_mov_b32_e32 v233, v169
	v_mov_b32_e32 v231, v222
	v_mov_b32_e32 v234, v223
	s_and_b64 vcc, exec, s[16:17]
	s_cbranch_vccnz .LBB0_1857
	s_branch .LBB0_1858

; #define PG8_STAGE(bufoff, rs_, soff_, voff) do { _Pragma("unroll") for (int _i = 0; _i < 2; ++_i) \
;         __builtin_amdgcn_raw_ptr_buffer_load_lds(rs_, (LAS void*)(lds + (bufoff) + ldsw + _i * 8192), 16, (int)(voff)[_i], (int)(soff_), 0, 0); } while (0)
; #define PG8_LDA(dst, b, h) do { _Pragma("unroll") for (int m = 0; m < 4; ++m) dst[m] = PG8_LD2(lds + PG8_SA(b, h) + aoff + m * 2048); } while (0)
; #define PG8_LDB(dst, b, h) do { _Pragma("unroll") for (int n = 0; n < 2; ++n) dst[n] = PG8_LD2(lds + PG8_SB(b, h) + boff + n * 2048); } while (0)
; #define PG8_WAIT_V(n) asm volatile("s_waitcnt vmcnt(" #n ")" ::: "memory")
; #define PG8_WAIT_L(n) asm volatile("s_waitcnt lgkmcnt(" #n ")" ::: "memory")
; #define PG8_BAR __builtin_amdgcn_s_barrier()
; #define PG8_SCHED __builtin_amdgcn_sched_barrier(0)
; template <class Epi, class Sched, bool ALIGN_EPI = false, bool SP2 = false, bool FP8 = false>
; __device__ __forceinline__ void gemm_phase(LAS unsigned char* lds, const Gemm g, const Sched& S, const Epi& E, int wbase) {
;     ...
;             PG8_LDB(B0, 0, 0); PG8_LDB(B1, 0, 1); PG8_SCHED; PG8_LDA(At, 0, 0); PG8_STAGE(PG8_SA(1, 1), rAc, a1 + hstep, voffA);
;             PG8_WAIT_V(8); PG8_WAIT_L(0); PG8_BAR; PG8_MMA(0, 0, At, B0); PG8_MMA(0, 1, At, B1); PG8_BAR; PG8_SCHED;
;             PG8_LDA(At, 0, 1); PG8_STAGE(PG8_SB(0, 0), rB2, b2, voffB); PG8_STAGE(PG8_SB(0, 1), rB2, b2 + hstep, voffB); PG8_STAGE(PG8_SA(0, 0), rA2, a2, voffA);
;             PG8_WAIT_V(8); PG8_WAIT_L(0); PG8_BAR; PG8_MMA(1, 0, At, B0); PG8_MMA(1, 1, At, B1); PG8_BAR; PG8_SCHED;
.LBB0_1944:
	v_add_u32_e32 v136, 0x10000, v174
	v_add_u32_e32 v156, 0x14000, v174
	ds_read_b128 v[120:123], v136
	ds_read_b128 v[124:127], v136 offset:1024
	ds_read_b128 v[132:135], v136 offset:2048
	ds_read_b128 v[136:139], v136 offset:3072
	ds_read_b128 v[144:147], v156
	ds_read_b128 v[148:151], v156 offset:1024
	ds_read_b128 v[152:155], v156 offset:2048
	ds_read_b128 v[156:159], v156 offset:3072
	s_add_i32 s6, s61, 0x80
	s_cmp_eq_u32 s77, s63
	s_cselect_b32 s66, s29, s6
	s_cselect_b32 s55, s60, s62
	s_or_b32 s54, s66, 0x80
	s_add_i32 s6, s33, s61
	s_mov_b32 m0, s79
	ds_read_b128 v[160:163], v175
	ds_read_b128 v[164:167], v175 offset:1024
	ds_read_b128 v[176:179], v175 offset:2048
	ds_read_b128 v[180:183], v175 offset:3072
	ds_read_b128 v[184:187], v175 offset:4096
	ds_read_b128 v[188:191], v175 offset:5120
	ds_read_b128 v[192:195], v175 offset:6144
	ds_read_b128 v[196:199], v175 offset:7168
	buffer_load_dwordx4 v168, s[36:39], s6 offen lds
	s_mov_b32 m0, s82
	s_nop 0
	buffer_load_dwordx4 v170, s[36:39], s6 offen lds
	s_waitcnt vmcnt(8)
	s_waitcnt lgkmcnt(0)
	s_barrier
	s_setprio 1
	v_mfma_f32_16x16x32_bf16 v[140:143], v[120:123], v[160:163], v[140:143]
	v_mfma_f32_16x16x32_bf16 v[128:131], v[132:135], v[160:163], v[128:131]
	v_mfma_f32_16x16x32_bf16 v[108:111], v[120:123], v[176:179], v[108:111]
	v_mfma_f32_16x16x32_bf16 v[104:107], v[132:135], v[176:179], v[104:107]
	v_mfma_f32_16x16x32_bf16 v[92:95], v[120:123], v[184:187], v[92:95]
	v_mfma_f32_16x16x32_bf16 v[88:91], v[132:135], v[184:187], v[88:91]
	v_mfma_f32_16x16x32_bf16 v[76:79], v[120:123], v[192:195], v[76:79]
	v_mfma_f32_16x16x32_bf16 v[72:75], v[132:135], v[192:195], v[72:75]
	v_mfma_f32_16x16x32_bf16 v[140:143], v[124:127], v[164:167], v[140:143]
	v_mfma_f32_16x16x32_bf16 v[128:131], v[136:139], v[164:167], v[128:131]
	v_mfma_f32_16x16x32_bf16 v[108:111], v[124:127], v[180:183], v[108:111]
	v_mfma_f32_16x16x32_bf16 v[104:107], v[136:139], v[180:183], v[104:107]
	v_mfma_f32_16x16x32_bf16 v[92:95], v[124:127], v[188:191], v[92:95]
	v_mfma_f32_16x16x32_bf16 v[88:91], v[136:139], v[188:191], v[88:91]
	v_mfma_f32_16x16x32_bf16 v[76:79], v[124:127], v[196:199], v[76:79]
	v_mfma_f32_16x16x32_bf16 v[72:75], v[136:139], v[196:199], v[72:75]
	s_setprio 0
	s_setprio 1
	v_mfma_f32_16x16x32_bf16 v[116:119], v[144:147], v[160:163], v[116:119]
	v_mfma_f32_16x16x32_bf16 v[112:115], v[152:155], v[160:163], v[112:115]
	v_mfma_f32_16x16x32_bf16 v[100:103], v[144:147], v[176:179], v[100:103]
	v_mfma_f32_16x16x32_bf16 v[96:99], v[152:155], v[176:179], v[96:99]
	v_mfma_f32_16x16x32_bf16 v[84:87], v[144:147], v[184:187], v[84:87]
	v_mfma_f32_16x16x32_bf16 v[80:83], v[152:155], v[184:187], v[80:83]
	v_mfma_f32_16x16x32_bf16 v[68:71], v[144:147], v[192:195], v[68:71]
	v_mfma_f32_16x16x32_bf16 v[64:67], v[152:155], v[192:195], v[64:67]
	v_mfma_f32_16x16x32_bf16 v[116:119], v[148:151], v[164:167], v[116:119]
	v_mfma_f32_16x16x32_bf16 v[112:115], v[156:159], v[164:167], v[112:115]
	v_mfma_f32_16x16x32_bf16 v[100:103], v[148:151], v[180:183], v[100:103]
	v_mfma_f32_16x16x32_bf16 v[96:99], v[156:159], v[180:183], v[96:99]
	v_mfma_f32_16x16x32_bf16 v[84:87], v[148:151], v[188:191], v[84:87]
	v_mfma_f32_16x16x32_bf16 v[80:83], v[156:159], v[188:191], v[80:83]
	v_mfma_f32_16x16x32_bf16 v[68:71], v[148:151], v[196:199], v[68:71]
	v_mfma_f32_16x16x32_bf16 v[64:67], v[156:159], v[196:199], v[64:67]
	s_setprio 0
	s_barrier
	s_mov_b32 m0, s35
	s_mov_b32 s6, s38
	s_mov_b32 s7, s39
	ds_read_b128 v[160:163], v175 offset:16384
	ds_read_b128 v[164:167], v175 offset:17408
	ds_read_b128 v[176:179], v175 offset:18432
	ds_read_b128 v[180:183], v175 offset:19456
	ds_read_b128 v[184:187], v175 offset:20480
	ds_read_b128 v[188:191], v175 offset:21504
	ds_read_b128 v[192:195], v175 offset:22528
	ds_read_b128 v[196:199], v175 offset:23552
	buffer_load_dwordx4 v169, s[4:7], s55 offen lds
	s_mov_b32 m0, s41
	s_add_i32 s67, s55, s33
	buffer_load_dwordx4 v171, s[4:7], s55 offen lds
	s_mov_b32 m0, s42
	s_nop 0
	buffer_load_dwordx4 v169, s[4:7], s67 offen lds
	s_mov_b32 m0, s43
	s_nop 0
	buffer_load_dwordx4 v171, s[4:7], s67 offen lds
	s_mov_b32 m0, s34
	s_nop 0
	buffer_load_dwordx4 v168, s[36:39], s66 offen lds
	s_mov_b32 m0, s44
	s_nop 0
	buffer_load_dwordx4 v170, s[36:39], s66 offen lds
	s_waitcnt vmcnt(8)
	s_waitcnt lgkmcnt(0)
	s_barrier
	s_setprio 1
	v_mfma_f32_16x16x32_bf16 v[60:63], v[120:123], v[160:163], v[60:63]
	v_mfma_f32_16x16x32_bf16 v[56:59], v[132:135], v[160:163], v[56:59]
	v_mfma_f32_16x16x32_bf16 v[44:47], v[120:123], v[176:179], v[44:47]
	v_mfma_f32_16x16x32_bf16 v[40:43], v[132:135], v[176:179], v[40:43]
	v_mfma_f32_16x16x32_bf16 v[28:31], v[120:123], v[184:187], v[28:31]
	v_mfma_f32_16x16x32_bf16 v[24:27], v[132:135], v[184:187], v[24:27]
	v_mfma_f32_16x16x32_bf16 v[12:15], v[120:123], v[192:195], v[12:15]
	v_mfma_f32_16x16x32_bf16 v[8:11], v[132:135], v[192:195], v[8:11]
	v_mfma_f32_16x16x32_bf16 v[60:63], v[124:127], v[164:167], v[60:63]
	v_mfma_f32_16x16x32_bf16 v[56:59], v[136:139], v[164:167], v[56:59]
	v_mfma_f32_16x16x32_bf16 v[44:47], v[124:127], v[180:183], v[44:47]
	v_mfma_f32_16x16x32_bf16 v[40:43], v[136:139], v[180:183], v[40:43]
	v_mfma_f32_16x16x32_bf16 v[28:31], v[124:127], v[188:191], v[28:31]
	v_mfma_f32_16x16x32_bf16 v[24:27], v[136:139], v[188:191], v[24:27]
	v_mfma_f32_16x16x32_bf16 v[12:15], v[124:127], v[196:199], v[12:15]
	v_mfma_f32_16x16x32_bf16 v[8:11], v[136:139], v[196:199], v[8:11]
	s_setprio 0
	s_setprio 1
	v_mfma_f32_16x16x32_bf16 v[52:55], v[144:147], v[160:163], v[52:55]
	v_mfma_f32_16x16x32_bf16 v[48:51], v[152:155], v[160:163], v[48:51]
	v_mfma_f32_16x16x32_bf16 v[36:39], v[144:147], v[176:179], v[36:39]
	v_mfma_f32_16x16x32_bf16 v[32:35], v[152:155], v[176:179], v[32:35]
	v_mfma_f32_16x16x32_bf16 v[20:23], v[144:147], v[184:187], v[20:23]
	v_mfma_f32_16x16x32_bf16 v[16:19], v[152:155], v[184:187], v[16:19]
	v_mfma_f32_16x16x32_bf16 v[4:7], v[144:147], v[192:195], v[4:7]
	v_mfma_f32_16x16x32_bf16 v[0:3], v[152:155], v[192:195], v[0:3]
	v_mfma_f32_16x16x32_bf16 v[52:55], v[148:151], v[164:167], v[52:55]
	v_mfma_f32_16x16x32_bf16 v[48:51], v[156:159], v[164:167], v[48:51]
	v_mfma_f32_16x16x32_bf16 v[36:39], v[148:151], v[180:183], v[36:39]
	v_mfma_f32_16x16x32_bf16 v[32:35], v[156:159], v[180:183], v[32:35]
	v_mfma_f32_16x16x32_bf16 v[20:23], v[148:151], v[188:191], v[20:23]
	v_mfma_f32_16x16x32_bf16 v[16:19], v[156:159], v[188:191], v[16:19]
	v_mfma_f32_16x16x32_bf16 v[4:7], v[148:151], v[196:199], v[4:7]
	v_mfma_f32_16x16x32_bf16 v[0:3], v[156:159], v[196:199], v[0:3]
	s_setprio 0
	s_barrier
; #define PG8_STAGE(bufoff, rs_, soff_, voff) do { _Pragma("unroll") for (int _i = 0; _i < 2; ++_i) \
;         __builtin_amdgcn_raw_ptr_buffer_load_lds(rs_, (LAS void*)(lds + (bufoff) + ldsw + _i * 8192), 16, (int)(voff)[_i], (int)(soff_), 0, 0); } while (0)
; #define PG8_LDA(dst, b, h) do { _Pragma("unroll") for (int m = 0; m < 4; ++m) dst[m] = PG8_LD2(lds + PG8_SA(b, h) + aoff + m * 2048); } while (0)
; #define PG8_LDB(dst, b, h) do { _Pragma("unroll") for (int n = 0; n < 2; ++n) dst[n] = PG8_LD2(lds + PG8_SB(b, h) + boff + n * 2048); } while (0)
; #define PG8_WAIT_V(n) asm volatile("s_waitcnt vmcnt(" #n ")" ::: "memory")
; #define PG8_WAIT_L(n) asm volatile("s_waitcnt lgkmcnt(" #n ")" ::: "memory")
; #define PG8_BAR __builtin_amdgcn_s_barrier()
; #define PG8_SCHED __builtin_amdgcn_sched_barrier(0)
; template <class Epi, class Sched, bool ALIGN_EPI = false, bool SP2 = false, bool FP8 = false>
; __device__ __forceinline__ void gemm_phase(LAS unsigned char* lds, const Gemm g, const Sched& S, const Epi& E, int wbase) {
;     ...
;             PG8_LDB(B0, 1, 0); PG8_LDB(B1, 1, 1); PG8_SCHED; PG8_LDA(At, 1, 0); PG8_STAGE(PG8_SA(0, 1), rA2, a2 + hstep, voffA);
;             PG8_WAIT_V(8); PG8_WAIT_L(0); PG8_BAR; PG8_MMA(0, 0, At, B0); PG8_MMA(0, 1, At, B1); PG8_BAR; PG8_SCHED;
;             PG8_LDA(At, 1, 1); PG8_STAGE(PG8_SB(1, 0), rB2, b3, voffB); PG8_STAGE(PG8_SB(1, 1), rB2, b3 + hstep, voffB); PG8_STAGE(PG8_SA(1, 0), rA2, a3, voffA);
;             PG8_WAIT_V(8); PG8_WAIT_L(0); PG8_BAR; PG8_MMA(1, 0, At, B0); PG8_MMA(1, 1, At, B1); PG8_BAR; PG8_SCHED;
	v_add_u32_e32 v136, 0x18000, v174
	v_add_u32_e32 v156, 0x1c000, v174
	ds_read_b128 v[120:123], v136
	ds_read_b128 v[124:127], v136 offset:1024
	ds_read_b128 v[132:135], v136 offset:2048
	ds_read_b128 v[136:139], v136 offset:3072
	ds_read_b128 v[144:147], v156
	ds_read_b128 v[148:151], v156 offset:1024
	ds_read_b128 v[152:155], v156 offset:2048
	ds_read_b128 v[156:159], v156 offset:3072
	s_add_i32 s66, s66, s33
	s_mov_b32 m0, s45
	ds_read_b128 v[160:163], v175 offset:32768
	ds_read_b128 v[164:167], v175 offset:33792
	ds_read_b128 v[176:179], v175 offset:34816
	ds_read_b128 v[180:183], v175 offset:35840
	ds_read_b128 v[184:187], v175 offset:36864
	ds_read_b128 v[188:191], v175 offset:37888
	ds_read_b128 v[192:195], v175 offset:38912
	ds_read_b128 v[196:199], v175 offset:39936
	buffer_load_dwordx4 v168, s[36:39], s66 offen lds
	s_mov_b32 m0, s46
	s_nop 0
	buffer_load_dwordx4 v170, s[36:39], s66 offen lds
	s_waitcnt vmcnt(8)
	s_waitcnt lgkmcnt(0)
	s_barrier
	s_setprio 1
	v_mfma_f32_16x16x32_bf16 v[140:143], v[120:123], v[160:163], v[140:143]
	v_mfma_f32_16x16x32_bf16 v[128:131], v[132:135], v[160:163], v[128:131]
	v_mfma_f32_16x16x32_bf16 v[108:111], v[120:123], v[176:179], v[108:111]
	v_mfma_f32_16x16x32_bf16 v[104:107], v[132:135], v[176:179], v[104:107]
	v_mfma_f32_16x16x32_bf16 v[92:95], v[120:123], v[184:187], v[92:95]
	v_mfma_f32_16x16x32_bf16 v[88:91], v[132:135], v[184:187], v[88:91]
	v_mfma_f32_16x16x32_bf16 v[76:79], v[120:123], v[192:195], v[76:79]
	v_mfma_f32_16x16x32_bf16 v[72:75], v[132:135], v[192:195], v[72:75]
	v_mfma_f32_16x16x32_bf16 v[140:143], v[124:127], v[164:167], v[140:143]
	v_mfma_f32_16x16x32_bf16 v[128:131], v[136:139], v[164:167], v[128:131]
	v_mfma_f32_16x16x32_bf16 v[108:111], v[124:127], v[180:183], v[108:111]
	v_mfma_f32_16x16x32_bf16 v[104:107], v[136:139], v[180:183], v[104:107]
	v_mfma_f32_16x16x32_bf16 v[92:95], v[124:127], v[188:191], v[92:95]
	v_mfma_f32_16x16x32_bf16 v[88:91], v[136:139], v[188:191], v[88:91]
	v_mfma_f32_16x16x32_bf16 v[76:79], v[124:127], v[196:199], v[76:79]
	v_mfma_f32_16x16x32_bf16 v[72:75], v[136:139], v[196:199], v[72:75]
	s_setprio 0
	s_setprio 1
	v_mfma_f32_16x16x32_bf16 v[116:119], v[144:147], v[160:163], v[116:119]
	v_mfma_f32_16x16x32_bf16 v[112:115], v[152:155], v[160:163], v[112:115]
	v_mfma_f32_16x16x32_bf16 v[100:103], v[144:147], v[176:179], v[100:103]
	v_mfma_f32_16x16x32_bf16 v[96:99], v[152:155], v[176:179], v[96:99]
	v_mfma_f32_16x16x32_bf16 v[84:87], v[144:147], v[184:187], v[84:87]
	v_mfma_f32_16x16x32_bf16 v[80:83], v[152:155], v[184:187], v[80:83]
	v_mfma_f32_16x16x32_bf16 v[68:71], v[144:147], v[192:195], v[68:71]
	v_mfma_f32_16x16x32_bf16 v[64:67], v[152:155], v[192:195], v[64:67]
	v_mfma_f32_16x16x32_bf16 v[116:119], v[148:151], v[164:167], v[116:119]
	v_mfma_f32_16x16x32_bf16 v[112:115], v[156:159], v[164:167], v[112:115]
	v_mfma_f32_16x16x32_bf16 v[100:103], v[148:151], v[180:183], v[100:103]
	v_mfma_f32_16x16x32_bf16 v[96:99], v[156:159], v[180:183], v[96:99]
	v_mfma_f32_16x16x32_bf16 v[84:87], v[148:151], v[188:191], v[84:87]
	v_mfma_f32_16x16x32_bf16 v[80:83], v[156:159], v[188:191], v[80:83]
	v_mfma_f32_16x16x32_bf16 v[68:71], v[148:151], v[196:199], v[68:71]
	v_mfma_f32_16x16x32_bf16 v[64:67], v[156:159], v[196:199], v[64:67]
	s_setprio 0
	s_barrier
	s_mov_b32 m0, s47
	s_bitset1_b32 s55, 7
	ds_read_b128 v[160:163], v175 offset:49152
	ds_read_b128 v[164:167], v175 offset:50176
	ds_read_b128 v[176:179], v175 offset:51200
	ds_read_b128 v[180:183], v175 offset:52224
	ds_read_b128 v[184:187], v175 offset:53248
	ds_read_b128 v[188:191], v175 offset:54272
	ds_read_b128 v[192:195], v175 offset:55296
	ds_read_b128 v[196:199], v175 offset:56320
	buffer_load_dwordx4 v169, s[4:7], s55 offen lds
	s_mov_b32 m0, s48
	s_nop 0
	buffer_load_dwordx4 v171, s[4:7], s55 offen lds
	s_add_i32 s55, s55, s33
	s_mov_b32 m0, s56
	s_nop 0
	buffer_load_dwordx4 v169, s[4:7], s55 offen lds
	s_mov_b32 m0, s57
	s_nop 0
	buffer_load_dwordx4 v171, s[4:7], s55 offen lds
	s_mov_b32 m0, s52
	s_nop 0
	buffer_load_dwordx4 v168, s[36:39], s54 offen lds
	s_mov_b32 m0, s53
	s_nop 0
	buffer_load_dwordx4 v170, s[36:39], s54 offen lds
	s_waitcnt vmcnt(8)
	s_waitcnt lgkmcnt(0)
	s_barrier
	s_setprio 1
	v_mfma_f32_16x16x32_bf16 v[60:63], v[120:123], v[160:163], v[60:63]
	v_mfma_f32_16x16x32_bf16 v[56:59], v[132:135], v[160:163], v[56:59]
	v_mfma_f32_16x16x32_bf16 v[44:47], v[120:123], v[176:179], v[44:47]
	v_mfma_f32_16x16x32_bf16 v[40:43], v[132:135], v[176:179], v[40:43]
	v_mfma_f32_16x16x32_bf16 v[28:31], v[120:123], v[184:187], v[28:31]
	v_mfma_f32_16x16x32_bf16 v[24:27], v[132:135], v[184:187], v[24:27]
	v_mfma_f32_16x16x32_bf16 v[12:15], v[120:123], v[192:195], v[12:15]
	v_mfma_f32_16x16x32_bf16 v[8:11], v[132:135], v[192:195], v[8:11]
	v_mfma_f32_16x16x32_bf16 v[60:63], v[124:127], v[164:167], v[60:63]
	v_mfma_f32_16x16x32_bf16 v[56:59], v[136:139], v[164:167], v[56:59]
	v_mfma_f32_16x16x32_bf16 v[44:47], v[124:127], v[180:183], v[44:47]
	v_mfma_f32_16x16x32_bf16 v[40:43], v[136:139], v[180:183], v[40:43]
	v_mfma_f32_16x16x32_bf16 v[28:31], v[124:127], v[188:191], v[28:31]
	v_mfma_f32_16x16x32_bf16 v[24:27], v[136:139], v[188:191], v[24:27]
	v_mfma_f32_16x16x32_bf16 v[12:15], v[124:127], v[196:199], v[12:15]
	v_mfma_f32_16x16x32_bf16 v[8:11], v[136:139], v[196:199], v[8:11]
	s_setprio 0
	s_setprio 1
	v_mfma_f32_16x16x32_bf16 v[52:55], v[144:147], v[160:163], v[52:55]
	v_mfma_f32_16x16x32_bf16 v[48:51], v[152:155], v[160:163], v[48:51]
	v_mfma_f32_16x16x32_bf16 v[36:39], v[144:147], v[176:179], v[36:39]
	v_mfma_f32_16x16x32_bf16 v[32:35], v[152:155], v[176:179], v[32:35]
	v_mfma_f32_16x16x32_bf16 v[20:23], v[144:147], v[184:187], v[20:23]
	v_mfma_f32_16x16x32_bf16 v[16:19], v[152:155], v[184:187], v[16:19]
	v_mfma_f32_16x16x32_bf16 v[4:7], v[144:147], v[192:195], v[4:7]
	v_mfma_f32_16x16x32_bf16 v[0:3], v[152:155], v[192:195], v[0:3]
	v_mfma_f32_16x16x32_bf16 v[52:55], v[148:151], v[164:167], v[52:55]
	v_mfma_f32_16x16x32_bf16 v[48:51], v[156:159], v[164:167], v[48:51]
	v_mfma_f32_16x16x32_bf16 v[36:39], v[148:151], v[180:183], v[36:39]
	v_mfma_f32_16x16x32_bf16 v[32:35], v[156:159], v[180:183], v[32:35]
	v_mfma_f32_16x16x32_bf16 v[20:23], v[148:151], v[188:191], v[20:23]
	v_mfma_f32_16x16x32_bf16 v[16:19], v[156:159], v[188:191], v[16:19]
	v_mfma_f32_16x16x32_bf16 v[4:7], v[148:151], v[196:199], v[4:7]
	v_mfma_f32_16x16x32_bf16 v[0:3], v[156:159], v[196:199], v[0:3]
	s_setprio 0
	s_barrier
	s_add_i32 s63, s63, 2
	s_addk_i32 s61, 0x100
	s_addk_i32 s62, 0x100
	s_cmp_ge_i32 s63, s65
	s_cbranch_scc0 .LBB0_1944
	s_and_b64 vcc, exec, s[24:25]
	s_cbranch_vccz .LBB0_1947

; #define PG8_STAGE(bufoff, rs_, soff_, voff) do { _Pragma("unroll") for (int _i = 0; _i < 2; ++_i) \
;         __builtin_amdgcn_raw_ptr_buffer_load_lds(rs_, (LAS void*)(lds + (bufoff) + ldsw + _i * 8192), 16, (int)(voff)[_i], (int)(soff_), 0, 0); } while (0)
; #define PG8_LDA(dst, b, h) do { _Pragma("unroll") for (int m = 0; m < 4; ++m) dst[m] = PG8_LD2(lds + PG8_SA(b, h) + aoff + m * 2048); } while (0)
; #define PG8_LDB(dst, b, h) do { _Pragma("unroll") for (int n = 0; n < 2; ++n) dst[n] = PG8_LD2(lds + PG8_SB(b, h) + boff + n * 2048); } while (0)
; #define PG8_WAIT_V(n) asm volatile("s_waitcnt vmcnt(" #n ")" ::: "memory")
; #define PG8_WAIT_L(n) asm volatile("s_waitcnt lgkmcnt(" #n ")" ::: "memory")
; #define PG8_BAR __builtin_amdgcn_s_barrier()
; #define PG8_SCHED __builtin_amdgcn_sched_barrier(0)
; template <class Epi, class Sched, bool ALIGN_EPI = false, bool SP2 = false, bool FP8 = false>
; __device__ __forceinline__ void gemm_phase(LAS unsigned char* lds, const Gemm g, const Sched& S, const Epi& E, int wbase) {
;     ...
;             PG8_LDB(B0, 0, 0); PG8_LDB(B1, 0, 1); PG8_SCHED; PG8_LDA(At, 0, 0); PG8_STAGE(PG8_SA(1, 1), rAc, a1 + hstep, voffA);
;             PG8_WAIT_V(8); PG8_WAIT_L(0); PG8_BAR; PG8_MMA(0, 0, At, B0); PG8_MMA(0, 1, At, B1); PG8_BAR; PG8_SCHED;
;             PG8_LDA(At, 0, 1); PG8_STAGE(PG8_SB(0, 0), rB2, b2, voffB); PG8_STAGE(PG8_SB(0, 1), rB2, b2 + hstep, voffB); PG8_STAGE(PG8_SA(0, 0), rA2, a2, voffA);
;             PG8_WAIT_V(8); PG8_WAIT_L(0); PG8_BAR; PG8_MMA(1, 0, At, B0); PG8_MMA(1, 1, At, B1); PG8_BAR; PG8_SCHED;
.LBB0_1990:
	v_add_u32_e32 v136, 0x10000, v180
	v_add_u32_e32 v156, 0x14000, v180
	ds_read_b128 v[120:123], v136
	ds_read_b128 v[124:127], v136 offset:1024
	ds_read_b128 v[132:135], v136 offset:2048
	ds_read_b128 v[136:139], v136 offset:3072
	ds_read_b128 v[144:147], v156
	ds_read_b128 v[148:151], v156 offset:1024
	ds_read_b128 v[152:155], v156 offset:2048
	ds_read_b128 v[156:159], v156 offset:3072
	s_add_i32 s14, s4, 0x80
	s_cmp_eq_u32 s84, s61
	s_cselect_b32 s62, s2, s14
	s_cselect_b32 s55, s3, s5
	s_or_b32 s54, s62, 0x80
	s_add_i32 s14, s42, s4
	s_mov_b32 m0, s85
	ds_read_b128 v[160:163], v181
	ds_read_b128 v[164:167], v181 offset:1024
	ds_read_b128 v[182:185], v181 offset:2048
	ds_read_b128 v[186:189], v181 offset:3072
	ds_read_b128 v[194:197], v181 offset:4096
	ds_read_b128 v[198:201], v181 offset:5120
	ds_read_b128 v[202:205], v181 offset:6144
	ds_read_b128 v[206:209], v181 offset:7168
	buffer_load_dwordx4 v174, s[36:39], s14 offen lds
	s_mov_b32 m0, s8
	s_nop 0
	buffer_load_dwordx4 v176, s[36:39], s14 offen lds
	s_waitcnt vmcnt(8)
	s_waitcnt lgkmcnt(0)
	s_barrier
	s_setprio 1
	v_mfma_f32_16x16x128_f8f6f4 v[140:143], v[120:127], v[160:167], v[140:143]
	v_mfma_f32_16x16x128_f8f6f4 v[128:131], v[132:139], v[160:167], v[128:131]
	v_mfma_f32_16x16x128_f8f6f4 v[108:111], v[120:127], v[182:189], v[108:111]
	v_mfma_f32_16x16x128_f8f6f4 v[104:107], v[132:139], v[182:189], v[104:107]
	v_mfma_f32_16x16x128_f8f6f4 v[168:171], v[120:127], v[194:201], v[92:95]
	v_mfma_f32_16x16x128_f8f6f4 v[190:193], v[132:139], v[194:201], v[88:91]
	v_mfma_f32_16x16x128_f8f6f4 v[210:213], v[120:127], v[202:209], v[76:79]
	v_mfma_f32_16x16x128_f8f6f4 v[214:217], v[132:139], v[202:209], v[72:75]
	s_setprio 0
	s_setprio 1
	v_mfma_f32_16x16x128_f8f6f4 v[116:119], v[144:151], v[160:167], v[116:119]
	v_mfma_f32_16x16x128_f8f6f4 v[112:115], v[152:159], v[160:167], v[112:115]
	v_mfma_f32_16x16x128_f8f6f4 v[100:103], v[144:151], v[182:189], v[100:103]
	v_mfma_f32_16x16x128_f8f6f4 v[96:99], v[152:159], v[182:189], v[96:99]
	v_mfma_f32_16x16x128_f8f6f4 v[160:163], v[144:151], v[194:201], v[84:87]
	v_mfma_f32_16x16x128_f8f6f4 v[164:167], v[152:159], v[194:201], v[80:83]
	v_mfma_f32_16x16x128_f8f6f4 v[182:185], v[144:151], v[202:209], v[68:71]
	v_mfma_f32_16x16x128_f8f6f4 v[186:189], v[152:159], v[202:209], v[64:67]
	s_setprio 0
	s_barrier
	s_mov_b32 m0, s44
	s_mov_b32 s14, s38
	s_mov_b32 s15, s39
	s_nop 1
	ds_read_b128 v[64:67], v181 offset:16384
	ds_read_b128 v[68:71], v181 offset:17408
	ds_read_b128 v[72:75], v181 offset:18432
	ds_read_b128 v[76:79], v181 offset:19456
	ds_read_b128 v[80:83], v181 offset:20480
	ds_read_b128 v[84:87], v181 offset:21504
	ds_read_b128 v[88:91], v181 offset:22528
	ds_read_b128 v[92:95], v181 offset:23552
	buffer_load_dwordx4 v175, s[12:15], s55 offen lds
	s_mov_b32 m0, s45
	s_add_i32 s63, s55, s42
	buffer_load_dwordx4 v177, s[12:15], s55 offen lds
	s_mov_b32 m0, s46
	s_nop 0
	buffer_load_dwordx4 v175, s[12:15], s63 offen lds
	s_mov_b32 m0, s47
	s_nop 0
	buffer_load_dwordx4 v177, s[12:15], s63 offen lds
	s_mov_b32 m0, s43
	s_nop 0
	buffer_load_dwordx4 v174, s[36:39], s62 offen lds
	s_mov_b32 m0, s48
	s_nop 0
	buffer_load_dwordx4 v176, s[36:39], s62 offen lds
	s_waitcnt vmcnt(8)
	s_waitcnt lgkmcnt(0)
	s_barrier
	s_setprio 1
	v_mfma_f32_16x16x128_f8f6f4 v[60:63], v[120:127], v[64:71], v[60:63]
	v_mfma_f32_16x16x128_f8f6f4 v[56:59], v[132:139], v[64:71], v[56:59]
	v_mfma_f32_16x16x128_f8f6f4 v[194:197], v[120:127], v[72:79], v[44:47]
	v_mfma_f32_16x16x128_f8f6f4 v[198:201], v[132:139], v[72:79], v[40:43]
	v_mfma_f32_16x16x128_f8f6f4 v[202:205], v[120:127], v[80:87], v[28:31]
	v_mfma_f32_16x16x128_f8f6f4 v[206:209], v[132:139], v[80:87], v[24:27]
	v_mfma_f32_16x16x128_f8f6f4 v[218:221], v[120:127], v[88:95], v[12:15]
	v_mfma_f32_16x16x128_f8f6f4 v[226:229], v[132:139], v[88:95], v[8:11]
	s_setprio 0
	s_setprio 1
	v_mfma_f32_16x16x128_f8f6f4 v[52:55], v[144:151], v[64:71], v[52:55]
	v_mfma_f32_16x16x128_f8f6f4 v[48:51], v[152:159], v[64:71], v[48:51]
	v_mfma_f32_16x16x128_f8f6f4 v[230:233], v[144:151], v[72:79], v[36:39]
	v_mfma_f32_16x16x128_f8f6f4 v[234:237], v[152:159], v[72:79], v[32:35]
	v_mfma_f32_16x16x128_f8f6f4 v[238:241], v[144:151], v[80:87], v[20:23]
	v_mfma_f32_16x16x128_f8f6f4 v[242:245], v[152:159], v[80:87], v[16:19]
	v_mfma_f32_16x16x128_f8f6f4 v[246:249], v[144:151], v[88:95], v[4:7]
	v_mfma_f32_16x16x128_f8f6f4 v[250:253], v[152:159], v[88:95], v[0:3]
	s_setprio 0
	s_barrier
; #define PG8_STAGE(bufoff, rs_, soff_, voff) do { _Pragma("unroll") for (int _i = 0; _i < 2; ++_i) \
;         __builtin_amdgcn_raw_ptr_buffer_load_lds(rs_, (LAS void*)(lds + (bufoff) + ldsw + _i * 8192), 16, (int)(voff)[_i], (int)(soff_), 0, 0); } while (0)
; #define PG8_LDA(dst, b, h) do { _Pragma("unroll") for (int m = 0; m < 4; ++m) dst[m] = PG8_LD2(lds + PG8_SA(b, h) + aoff + m * 2048); } while (0)
; #define PG8_LDB(dst, b, h) do { _Pragma("unroll") for (int n = 0; n < 2; ++n) dst[n] = PG8_LD2(lds + PG8_SB(b, h) + boff + n * 2048); } while (0)
; #define PG8_WAIT_V(n) asm volatile("s_waitcnt vmcnt(" #n ")" ::: "memory")
; #define PG8_WAIT_L(n) asm volatile("s_waitcnt lgkmcnt(" #n ")" ::: "memory")
; #define PG8_BAR __builtin_amdgcn_s_barrier()
; #define PG8_SCHED __builtin_amdgcn_sched_barrier(0)
; template <class Epi, class Sched, bool ALIGN_EPI = false, bool SP2 = false, bool FP8 = false>
; __device__ __forceinline__ void gemm_phase(LAS unsigned char* lds, const Gemm g, const Sched& S, const Epi& E, int wbase) {
;     ...
;             PG8_LDB(B0, 1, 0); PG8_LDB(B1, 1, 1); PG8_SCHED; PG8_LDA(At, 1, 0); PG8_STAGE(PG8_SA(0, 1), rA2, a2 + hstep, voffA);
;             PG8_WAIT_V(8); PG8_WAIT_L(0); PG8_BAR; PG8_MMA(0, 0, At, B0); PG8_MMA(0, 1, At, B1); PG8_BAR; PG8_SCHED;
;             PG8_LDA(At, 1, 1); PG8_STAGE(PG8_SB(1, 0), rB2, b3, voffB); PG8_STAGE(PG8_SB(1, 1), rB2, b3 + hstep, voffB); PG8_STAGE(PG8_SA(1, 0), rA2, a3, voffA);
;             PG8_WAIT_V(8); PG8_WAIT_L(0); PG8_BAR; PG8_MMA(1, 0, At, B0); PG8_MMA(1, 1, At, B1); PG8_BAR; PG8_SCHED;
	v_add_u32_e32 v8, 0x18000, v180
	s_nop 3
	ds_read_b128 v[0:3], v8
	ds_read_b128 v[4:7], v8 offset:1024
	ds_read_b128 v[16:19], v8 offset:2048
	ds_read_b128 v[20:23], v8 offset:3072
	v_add_u32_e32 v8, 0x1c000, v180
	ds_read_b128 v[120:123], v8
	ds_read_b128 v[124:127], v8 offset:1024
	ds_read_b128 v[132:135], v8 offset:2048
	ds_read_b128 v[136:139], v8 offset:3072
	s_add_i32 s62, s62, s42
	s_mov_b32 m0, s52
	ds_read_b128 v[8:11], v181 offset:32768
	ds_read_b128 v[12:15], v181 offset:33792
	ds_read_b128 v[24:27], v181 offset:34816
	ds_read_b128 v[28:31], v181 offset:35840
	ds_read_b128 v[32:35], v181 offset:36864
	ds_read_b128 v[36:39], v181 offset:37888
	ds_read_b128 v[40:43], v181 offset:38912
	ds_read_b128 v[44:47], v181 offset:39936
	buffer_load_dwordx4 v174, s[36:39], s62 offen lds
	s_mov_b32 m0, s53
	s_nop 0
	buffer_load_dwordx4 v176, s[36:39], s62 offen lds
	s_waitcnt vmcnt(8)
	s_waitcnt lgkmcnt(0)
	s_barrier
	s_setprio 1
	v_mfma_f32_16x16x128_f8f6f4 v[140:143], v[0:7], v[8:15], v[140:143]
	v_mfma_f32_16x16x128_f8f6f4 v[128:131], v[16:23], v[8:15], v[128:131]
	v_mfma_f32_16x16x128_f8f6f4 v[108:111], v[0:7], v[24:31], v[108:111]
	v_mfma_f32_16x16x128_f8f6f4 v[104:107], v[16:23], v[24:31], v[104:107]
	v_mfma_f32_16x16x128_f8f6f4 v[92:95], v[0:7], v[32:39], v[168:171]
	v_mfma_f32_16x16x128_f8f6f4 v[88:91], v[16:23], v[32:39], v[190:193]
	v_mfma_f32_16x16x128_f8f6f4 v[76:79], v[0:7], v[40:47], v[210:213]
	v_mfma_f32_16x16x128_f8f6f4 v[72:75], v[16:23], v[40:47], v[214:217]
	s_setprio 0
	s_setprio 1
	v_mfma_f32_16x16x128_f8f6f4 v[116:119], v[120:127], v[8:15], v[116:119]
	v_mfma_f32_16x16x128_f8f6f4 v[112:115], v[132:139], v[8:15], v[112:115]
	v_mfma_f32_16x16x128_f8f6f4 v[100:103], v[120:127], v[24:31], v[100:103]
	v_mfma_f32_16x16x128_f8f6f4 v[96:99], v[132:139], v[24:31], v[96:99]
	v_mfma_f32_16x16x128_f8f6f4 v[84:87], v[120:127], v[32:39], v[160:163]
	v_mfma_f32_16x16x128_f8f6f4 v[80:83], v[132:139], v[32:39], v[164:167]
	v_mfma_f32_16x16x128_f8f6f4 v[68:71], v[120:127], v[40:47], v[182:185]
	v_mfma_f32_16x16x128_f8f6f4 v[64:67], v[132:139], v[40:47], v[186:189]
	s_setprio 0
	s_barrier
	s_mov_b32 m0, s56
	s_bitset1_b32 s55, 7
	ds_read_b128 v[32:35], v181 offset:49152
	ds_read_b128 v[36:39], v181 offset:50176
	ds_read_b128 v[144:147], v181 offset:51200
	ds_read_b128 v[148:151], v181 offset:52224
	ds_read_b128 v[152:155], v181 offset:53248
	ds_read_b128 v[156:159], v181 offset:54272
	ds_read_b128 v[160:163], v181 offset:55296
	ds_read_b128 v[164:167], v181 offset:56320
	buffer_load_dwordx4 v175, s[12:15], s55 offen lds
	s_mov_b32 m0, s57
	s_nop 0
	buffer_load_dwordx4 v177, s[12:15], s55 offen lds
	s_add_i32 s55, s55, s42
	s_mov_b32 m0, s65
	s_nop 0
	buffer_load_dwordx4 v175, s[12:15], s55 offen lds
	s_mov_b32 m0, s76
	s_nop 0
	buffer_load_dwordx4 v177, s[12:15], s55 offen lds
	s_mov_b32 m0, s58
	s_nop 0
	buffer_load_dwordx4 v174, s[36:39], s54 offen lds
	s_mov_b32 m0, s59
	s_nop 0
	buffer_load_dwordx4 v176, s[36:39], s54 offen lds
	s_waitcnt vmcnt(8)
	s_waitcnt lgkmcnt(0)
	s_barrier
	s_setprio 1
	v_mfma_f32_16x16x128_f8f6f4 v[60:63], v[0:7], v[32:39], v[60:63]
	v_mfma_f32_16x16x128_f8f6f4 v[56:59], v[16:23], v[32:39], v[56:59]
	v_mfma_f32_16x16x128_f8f6f4 v[44:47], v[0:7], v[144:151], v[194:197]
	v_mfma_f32_16x16x128_f8f6f4 v[40:43], v[16:23], v[144:151], v[198:201]
	v_mfma_f32_16x16x128_f8f6f4 v[28:31], v[0:7], v[152:159], v[202:205]
	v_mfma_f32_16x16x128_f8f6f4 v[24:27], v[16:23], v[152:159], v[206:209]
	v_mfma_f32_16x16x128_f8f6f4 v[12:15], v[0:7], v[160:167], v[218:221]
	v_mfma_f32_16x16x128_f8f6f4 v[8:11], v[16:23], v[160:167], v[226:229]
	s_setprio 0
	s_setprio 1
	v_mfma_f32_16x16x128_f8f6f4 v[52:55], v[120:127], v[32:39], v[52:55]
	v_mfma_f32_16x16x128_f8f6f4 v[48:51], v[132:139], v[32:39], v[48:51]
	v_mfma_f32_16x16x128_f8f6f4 v[36:39], v[120:127], v[144:151], v[230:233]
	v_mfma_f32_16x16x128_f8f6f4 v[32:35], v[132:139], v[144:151], v[234:237]
	v_mfma_f32_16x16x128_f8f6f4 v[20:23], v[120:127], v[152:159], v[238:241]
	v_mfma_f32_16x16x128_f8f6f4 v[16:19], v[132:139], v[152:159], v[242:245]
	v_mfma_f32_16x16x128_f8f6f4 v[4:7], v[120:127], v[160:167], v[246:249]
	v_mfma_f32_16x16x128_f8f6f4 v[0:3], v[132:139], v[160:167], v[250:253]
	s_setprio 0
	s_barrier
	s_add_i32 s61, s61, 2
	s_addk_i32 s4, 0x100
	s_addk_i32 s5, 0x100
	s_cmp_ge_i32 s61, s82
	s_cbranch_scc0 .LBB0_1990
	v_mov_b32_e32 v230, v172
	v_mov_b32_e32 v233, v173
	v_mov_b32_e32 v231, v222
	v_mov_b32_e32 v234, v223
	s_and_b64 vcc, exec, s[28:29]
	s_cbranch_vccnz .LBB0_1993
	s_branch .LBB0_1994
